# LN2 output stores sc1 too (on top of QKV sc1): L2 clean at the grid barrier after LN2
# speedup vs baseline: 1.0113x; 1.0090x over previous
.LBB0_994:
	s_waitcnt vmcnt(0)
	v_lshlrev_b32_e32 v44, 2, v44
	v_add_u32_e32 v44, s5, v44
	ds_read_b32 v48, v44
	v_ashrrev_i32_e32 v51, 31, v45
	v_mov_b32_e32 v50, v45
	v_lshlrev_b32_e32 v46, 2, v46
	v_add_u32_e32 v46, s5, v46
	s_waitcnt lgkmcnt(0)
	v_ashrrev_i32_e32 v49, 31, v48
	v_lshlrev_b64 v[44:45], 18, v[48:49]
	v_lshlrev_b64 v[48:49], 10, v[50:51]
	v_lshl_add_u64 v[44:45], s[22:23], 0, v[44:45]
	v_lshl_add_u64 v[44:45], v[44:45], 0, v[48:49]
	ds_read_b32 v48, v46
	v_ashrrev_i32_e32 v51, 31, v47
	v_mov_b32_e32 v50, v47
	v_lshl_add_u64 v[44:45], v[44:45], 0, v[80:81]
	global_load_dwordx2 v[122:123], v[44:45], off nt
	s_waitcnt lgkmcnt(0)
	v_ashrrev_i32_e32 v49, 31, v48
	v_lshlrev_b64 v[46:47], 18, v[48:49]
	v_lshlrev_b64 v[48:49], 10, v[50:51]
	v_lshl_add_u64 v[46:47], s[22:23], 0, v[46:47]
	v_lshl_add_u64 v[46:47], v[46:47], 0, v[48:49]
	v_add_co_u32_e32 v48, vcc, s13, v82
	v_lshl_add_u64 v[46:47], v[46:47], 0, v[80:81]
	s_nop 0
	v_addc_co_u32_e32 v49, vcc, -1, v83, vcc
	global_load_dwordx4 v[76:79], v[48:49], off offset:-3072
	global_load_dwordx2 v[120:121], v[46:47], off nt
	global_load_dwordx4 v[72:75], v[48:49], off offset:-2048
	global_load_dwordx2 v[134:135], v[44:45], off offset:512 nt
	global_load_dwordx2 v[132:133], v[46:47], off offset:512 nt
	v_lshlrev_b32_e32 v40, 2, v40
	v_add_u32_e32 v40, s5, v40
	ds_read_b32 v44, v40
	v_ashrrev_i32_e32 v47, 31, v41
	v_mov_b32_e32 v46, v41
	v_lshlrev_b32_e32 v42, 2, v42
	v_add_u32_e32 v42, s5, v42
	s_waitcnt lgkmcnt(0)
	v_ashrrev_i32_e32 v45, 31, v44
	v_lshlrev_b64 v[40:41], 18, v[44:45]
	v_lshlrev_b64 v[44:45], 10, v[46:47]
	v_lshl_add_u64 v[40:41], s[22:23], 0, v[40:41]
	v_lshl_add_u64 v[40:41], v[40:41], 0, v[44:45]
	ds_read_b32 v44, v42
	v_ashrrev_i32_e32 v47, 31, v43
	v_mov_b32_e32 v46, v43
	v_lshl_add_u64 v[40:41], v[40:41], 0, v[80:81]
	global_load_dwordx4 v[68:71], v[48:49], off offset:-1024
	s_waitcnt lgkmcnt(0)
	v_ashrrev_i32_e32 v45, 31, v44
	v_lshlrev_b64 v[42:43], 18, v[44:45]
	v_lshlrev_b64 v[44:45], 10, v[46:47]
	v_lshl_add_u64 v[42:43], s[22:23], 0, v[42:43]
	v_lshl_add_u64 v[42:43], v[42:43], 0, v[44:45]
	global_load_dwordx2 v[130:131], v[40:41], off nt
	v_lshl_add_u64 v[42:43], v[42:43], 0, v[80:81]
	v_lshlrev_b32_e32 v36, 2, v36
	global_load_dwordx2 v[128:129], v[42:43], off nt
	global_load_dwordx4 v[64:67], v[82:83], off offset:-4096
	global_load_dwordx2 v[102:103], v[40:41], off offset:512 nt
	global_load_dwordx2 v[100:101], v[42:43], off offset:512 nt
	v_add_u32_e32 v36, s5, v36
	ds_read_b32 v40, v36
	v_ashrrev_i32_e32 v43, 31, v37
	v_mov_b32_e32 v42, v37
	v_lshlrev_b32_e32 v38, 2, v38
	v_add_u32_e32 v38, s5, v38
	s_waitcnt lgkmcnt(0)
	v_ashrrev_i32_e32 v41, 31, v40
	v_lshlrev_b64 v[36:37], 18, v[40:41]
	v_lshlrev_b64 v[40:41], 10, v[42:43]
	v_lshl_add_u64 v[36:37], s[22:23], 0, v[36:37]
	v_lshl_add_u64 v[36:37], v[36:37], 0, v[40:41]
	ds_read_b32 v40, v38
	v_ashrrev_i32_e32 v43, 31, v39
	v_mov_b32_e32 v42, v39
	v_lshl_add_u64 v[36:37], v[36:37], 0, v[80:81]
	global_load_dwordx4 v[60:63], v[82:83], off offset:-3072
	s_waitcnt lgkmcnt(0)
	v_ashrrev_i32_e32 v41, 31, v40
	v_lshlrev_b64 v[38:39], 18, v[40:41]
	v_lshlrev_b64 v[40:41], 10, v[42:43]
	v_lshl_add_u64 v[38:39], s[22:23], 0, v[38:39]
	v_lshl_add_u64 v[38:39], v[38:39], 0, v[40:41]
	global_load_dwordx2 v[118:119], v[36:37], off nt
	v_lshl_add_u64 v[38:39], v[38:39], 0, v[80:81]
	global_load_dwordx2 v[104:105], v[38:39], off nt
	global_load_dwordx4 v[56:59], v[82:83], off offset:-2048
	global_load_dwordx2 v[108:109], v[36:37], off offset:512 nt
	global_load_dwordx2 v[106:107], v[38:39], off offset:512 nt
	v_lshlrev_b32_e32 v32, 2, v32
	v_add_u32_e32 v32, s5, v32
	ds_read_b32 v36, v32
	v_ashrrev_i32_e32 v39, 31, v33
	v_mov_b32_e32 v38, v33
	v_lshlrev_b32_e32 v34, 2, v34
	v_add_u32_e32 v34, s5, v34
	s_waitcnt lgkmcnt(0)
	v_ashrrev_i32_e32 v37, 31, v36
	v_lshlrev_b64 v[32:33], 18, v[36:37]
	v_lshlrev_b64 v[36:37], 10, v[38:39]
	v_lshl_add_u64 v[32:33], s[22:23], 0, v[32:33]
	v_lshl_add_u64 v[32:33], v[32:33], 0, v[36:37]
	ds_read_b32 v36, v34
	v_ashrrev_i32_e32 v39, 31, v35
	v_mov_b32_e32 v38, v35
	v_lshl_add_u64 v[32:33], v[32:33], 0, v[80:81]
	global_load_dwordx4 v[52:55], v[82:83], off offset:-1024
	s_waitcnt lgkmcnt(0)
	v_ashrrev_i32_e32 v37, 31, v36
	v_lshlrev_b64 v[34:35], 18, v[36:37]
	v_lshlrev_b64 v[36:37], 10, v[38:39]
	v_lshl_add_u64 v[34:35], s[22:23], 0, v[34:35]
	v_lshl_add_u64 v[34:35], v[34:35], 0, v[36:37]
	global_load_dwordx2 v[116:117], v[32:33], off nt
	v_lshl_add_u64 v[34:35], v[34:35], 0, v[80:81]
	global_load_dwordx2 v[110:111], v[34:35], off nt
	global_load_dwordx4 v[48:51], v[82:83], off
	global_load_dwordx2 v[114:115], v[32:33], off offset:512 nt
	global_load_dwordx2 v[112:113], v[34:35], off offset:512 nt
	s_waitcnt vmcnt(23)
	v_cvt_pk_f32_fp8_e32 v[148:149], v122
	v_cvt_pk_f32_fp8_sdwa v[150:151], v122 src0_sel:WORD_1
	v_cvt_pk_f32_fp8_e32 v[152:153], v123
	v_cvt_pk_f32_fp8_sdwa v[154:155], v123 src0_sel:WORD_1
	s_waitcnt vmcnt(21)
	v_cvt_pk_f32_fp8_e32 v[122:123], v120
	v_cvt_pk_f32_fp8_sdwa v[156:157], v120 src0_sel:WORD_1
	v_cvt_pk_f32_fp8_e32 v[158:159], v121
	v_cvt_pk_f32_fp8_sdwa v[160:161], v121 src0_sel:WORD_1
	v_mul_f32_e32 v146, 0x3d000000, v99
	v_mul_f32_e32 v98, 0x3d000000, v98
	v_pk_mul_f32 v[120:121], v[146:147], v[156:157] op_sel_hi:[0,1]
	v_pk_mul_f32 v[122:123], v[146:147], v[122:123] op_sel_hi:[0,1]
	v_lshlrev_b32_e32 v124, 16, v76
	v_and_b32_e32 v125, 0xffff0000, v76
	v_lshlrev_b32_e32 v76, 16, v77
	v_and_b32_e32 v77, 0xffff0000, v77
	v_pk_fma_f32 v[122:123], v[98:99], v[148:149], v[122:123] op_sel_hi:[0,1,1]
	v_pk_fma_f32 v[120:121], v[98:99], v[150:151], v[120:121] op_sel_hi:[0,1,1]
	v_pk_fma_f32 v[120:121], v[76:77], s[12:13], v[120:121] op_sel_hi:[1,0,1]
	v_pk_fma_f32 v[122:123], v[124:125], s[12:13], v[122:123] op_sel_hi:[1,0,1]
	v_pk_mul_f32 v[76:77], v[146:147], v[160:161] op_sel_hi:[0,1]
	v_pk_mul_f32 v[124:125], v[146:147], v[158:159] op_sel_hi:[0,1]
	v_lshlrev_b32_e32 v126, 16, v78
	v_and_b32_e32 v127, 0xffff0000, v78
	v_lshlrev_b32_e32 v78, 16, v79
	v_and_b32_e32 v79, 0xffff0000, v79
	v_pk_fma_f32 v[148:149], v[98:99], v[152:153], v[124:125] op_sel_hi:[0,1,1]
	v_pk_fma_f32 v[76:77], v[98:99], v[154:155], v[76:77] op_sel_hi:[0,1,1]
	s_waitcnt vmcnt(18)
	v_cvt_pk_f32_fp8_e32 v[154:155], v132
	v_pk_fma_f32 v[124:125], v[78:79], s[12:13], v[76:77] op_sel_hi:[1,0,1]
	v_pk_fma_f32 v[126:127], v[126:127], s[12:13], v[148:149] op_sel_hi:[1,0,1]
	v_lshlrev_b32_e32 v78, 16, v74
	v_and_b32_e32 v79, 0xffff0000, v74
	v_lshlrev_b32_e32 v148, 16, v75
	v_and_b32_e32 v149, 0xffff0000, v75
	v_cvt_pk_f32_fp8_e32 v[74:75], v134
	v_cvt_pk_f32_fp8_sdwa v[156:157], v132 src0_sel:WORD_1
	v_cvt_pk_f32_fp8_e32 v[158:159], v133
	v_cvt_pk_f32_fp8_sdwa v[132:133], v133 src0_sel:WORD_1
	v_cvt_pk_f32_fp8_sdwa v[150:151], v134 src0_sel:WORD_1
	v_cvt_pk_f32_fp8_e32 v[152:153], v135
	v_cvt_pk_f32_fp8_sdwa v[134:135], v135 src0_sel:WORD_1
	v_pk_mul_f32 v[154:155], v[146:147], v[154:155] op_sel_hi:[0,1]
	v_lshlrev_b32_e32 v76, 16, v72
	v_and_b32_e32 v77, 0xffff0000, v72
	v_pk_fma_f32 v[74:75], v[98:99], v[74:75], v[154:155] op_sel_hi:[0,1,1]
	v_pk_mul_f32 v[156:157], v[146:147], v[156:157] op_sel_hi:[0,1]
	v_pk_fma_f32 v[74:75], v[76:77], s[12:13], v[74:75] op_sel_hi:[1,0,1]
	v_pk_mul_f32 v[76:77], v[146:147], v[132:133] op_sel_hi:[0,1]
	v_pk_mul_f32 v[132:133], v[146:147], v[158:159] op_sel_hi:[0,1]
	v_lshlrev_b32_e32 v72, 16, v73
	v_and_b32_e32 v73, 0xffff0000, v73
	v_pk_fma_f32 v[150:151], v[98:99], v[150:151], v[156:157] op_sel_hi:[0,1,1]
	v_pk_fma_f32 v[132:133], v[98:99], v[152:153], v[132:133] op_sel_hi:[0,1,1]
	v_pk_fma_f32 v[72:73], v[72:73], s[12:13], v[150:151] op_sel_hi:[1,0,1]
	v_pk_fma_f32 v[76:77], v[98:99], v[134:135], v[76:77] op_sel_hi:[0,1,1]
	v_pk_fma_f32 v[78:79], v[78:79], s[12:13], v[132:133] op_sel_hi:[1,0,1]
	v_mov_b32_e32 v98, v122
	v_mov_b32_e32 v99, v74
	v_mov_b32_e32 v132, v123
	v_mov_b32_e32 v133, v75
	v_pk_add_f32 v[98:99], v[98:99], v[132:133]
	v_mov_b32_e32 v132, v120
	v_mov_b32_e32 v133, v72
	v_mov_b32_e32 v134, v121
	v_mov_b32_e32 v135, v73
	v_pk_add_f32 v[132:133], v[132:133], v[134:135]
	v_pk_fma_f32 v[76:77], v[148:149], s[12:13], v[76:77] op_sel_hi:[1,0,1]
	v_pk_add_f32 v[98:99], v[98:99], v[132:133]
	v_mov_b32_e32 v132, v126
	v_mov_b32_e32 v133, v78
	v_mov_b32_e32 v134, v127
	v_mov_b32_e32 v135, v79
	v_pk_add_f32 v[132:133], v[132:133], v[134:135]
	v_mov_b32_e32 v134, v124
	v_mov_b32_e32 v135, v76
	v_mov_b32_e32 v146, v125
	v_mov_b32_e32 v147, v77
	v_pk_add_f32 v[134:135], v[134:135], v[146:147]
	s_waitcnt vmcnt(15)
	v_cvt_pk_f32_fp8_e32 v[154:155], v128
	v_pk_add_f32 v[132:133], v[132:133], v[134:135]
	v_lshlrev_b32_e32 v148, 16, v71
	v_pk_add_f32 v[98:99], v[98:99], v[132:133]
	v_and_b32_e32 v149, 0xffff0000, v71
	v_add_f32_e32 v98, 0, v98
	v_add_f32_e32 v132, v98, v99
	v_lshlrev_b32_e32 v98, 16, v70
	v_and_b32_e32 v99, 0xffff0000, v70
	v_cvt_pk_f32_fp8_e32 v[70:71], v130
	v_cvt_pk_f32_fp8_sdwa v[156:157], v128 src0_sel:WORD_1
	v_cvt_pk_f32_fp8_e32 v[158:159], v129
	v_cvt_pk_f32_fp8_sdwa v[128:129], v129 src0_sel:WORD_1
	v_mul_f32_e32 v146, 0x3d000000, v97
	v_cvt_pk_f32_fp8_sdwa v[150:151], v130 src0_sel:WORD_1
	v_cvt_pk_f32_fp8_e32 v[152:153], v131
	v_cvt_pk_f32_fp8_sdwa v[130:131], v131 src0_sel:WORD_1
	v_mul_f32_e32 v134, 0x3d000000, v96
	v_pk_mul_f32 v[154:155], v[146:147], v[154:155] op_sel_hi:[0,1]
	v_lshlrev_b32_e32 v96, 16, v68
	v_and_b32_e32 v97, 0xffff0000, v68
	v_pk_fma_f32 v[70:71], v[134:135], v[70:71], v[154:155] op_sel_hi:[0,1,1]
	v_pk_fma_f32 v[70:71], v[96:97], s[12:13], v[70:71] op_sel_hi:[1,0,1]
	v_pk_mul_f32 v[96:97], v[146:147], v[128:129] op_sel_hi:[0,1]
	v_pk_fma_f32 v[96:97], v[134:135], v[130:131], v[96:97] op_sel_hi:[0,1,1]
	s_waitcnt vmcnt(12)
	v_cvt_pk_f32_fp8_e32 v[154:155], v100
	v_pk_mul_f32 v[156:157], v[146:147], v[156:157] op_sel_hi:[0,1]
	v_pk_fma_f32 v[96:97], v[148:149], s[12:13], v[96:97] op_sel_hi:[1,0,1]
	v_lshlrev_b32_e32 v130, 16, v66
	v_and_b32_e32 v131, 0xffff0000, v66
	v_lshlrev_b32_e32 v148, 16, v67
	v_and_b32_e32 v149, 0xffff0000, v67
	v_cvt_pk_f32_fp8_e32 v[66:67], v102
	v_lshlrev_b32_e32 v68, 16, v69
	v_and_b32_e32 v69, 0xffff0000, v69
	v_pk_fma_f32 v[150:151], v[134:135], v[150:151], v[156:157] op_sel_hi:[0,1,1]
	v_pk_mul_f32 v[128:129], v[146:147], v[158:159] op_sel_hi:[0,1]
	v_cvt_pk_f32_fp8_sdwa v[156:157], v100 src0_sel:WORD_1
	v_cvt_pk_f32_fp8_e32 v[158:159], v101
	v_pk_fma_f32 v[68:69], v[68:69], s[12:13], v[150:151] op_sel_hi:[1,0,1]
	v_pk_fma_f32 v[128:129], v[134:135], v[152:153], v[128:129] op_sel_hi:[0,1,1]
	v_cvt_pk_f32_fp8_sdwa v[150:151], v102 src0_sel:WORD_1
	v_cvt_pk_f32_fp8_e32 v[152:153], v103
	v_cvt_pk_f32_fp8_sdwa v[100:101], v101 src0_sel:WORD_1
	v_cvt_pk_f32_fp8_sdwa v[102:103], v103 src0_sel:WORD_1
	v_pk_mul_f32 v[154:155], v[146:147], v[154:155] op_sel_hi:[0,1]
	v_pk_fma_f32 v[98:99], v[98:99], s[12:13], v[128:129] op_sel_hi:[1,0,1]
	v_lshlrev_b32_e32 v128, 16, v64
	v_and_b32_e32 v129, 0xffff0000, v64
	v_pk_fma_f32 v[66:67], v[134:135], v[66:67], v[154:155] op_sel_hi:[0,1,1]
	v_pk_mul_f32 v[156:157], v[146:147], v[156:157] op_sel_hi:[0,1]
	v_pk_fma_f32 v[66:67], v[128:129], s[12:13], v[66:67] op_sel_hi:[1,0,1]
	v_pk_mul_f32 v[128:129], v[146:147], v[158:159] op_sel_hi:[0,1]
	v_lshlrev_b32_e32 v64, 16, v65
	v_and_b32_e32 v65, 0xffff0000, v65
	v_pk_fma_f32 v[150:151], v[134:135], v[150:151], v[156:157] op_sel_hi:[0,1,1]
	v_pk_mul_f32 v[100:101], v[146:147], v[100:101] op_sel_hi:[0,1]
	v_pk_fma_f32 v[128:129], v[134:135], v[152:153], v[128:129] op_sel_hi:[0,1,1]
	v_pk_fma_f32 v[64:65], v[64:65], s[12:13], v[150:151] op_sel_hi:[1,0,1]
	v_pk_fma_f32 v[100:101], v[134:135], v[102:103], v[100:101] op_sel_hi:[0,1,1]
	v_pk_fma_f32 v[102:103], v[130:131], s[12:13], v[128:129] op_sel_hi:[1,0,1]
	v_mov_b32_e32 v128, v70
	v_mov_b32_e32 v129, v66
	v_mov_b32_e32 v130, v71
	v_mov_b32_e32 v131, v67
	v_pk_add_f32 v[128:129], v[128:129], v[130:131]
	v_mov_b32_e32 v130, v68
	v_mov_b32_e32 v131, v64
	v_mov_b32_e32 v134, v69
	v_mov_b32_e32 v135, v65
	v_pk_add_f32 v[130:131], v[130:131], v[134:135]
	v_pk_fma_f32 v[100:101], v[148:149], s[12:13], v[100:101] op_sel_hi:[1,0,1]
	v_pk_add_f32 v[128:129], v[128:129], v[130:131]
	v_mov_b32_e32 v130, v98
	v_mov_b32_e32 v131, v102
	v_mov_b32_e32 v134, v99
	v_mov_b32_e32 v135, v103
	v_pk_add_f32 v[130:131], v[130:131], v[134:135]
	v_mov_b32_e32 v134, v96
	v_mov_b32_e32 v135, v100
	v_mov_b32_e32 v146, v97
	v_mov_b32_e32 v147, v101
	s_waitcnt vmcnt(9)
	v_cvt_pk_f32_fp8_e32 v[154:155], v104
	v_pk_add_f32 v[134:135], v[134:135], v[146:147]
	v_lshlrev_b32_e32 v146, 16, v62
	v_and_b32_e32 v147, 0xffff0000, v62
	v_lshlrev_b32_e32 v148, 16, v63
	v_and_b32_e32 v149, 0xffff0000, v63
	v_cvt_pk_f32_fp8_e32 v[62:63], v118
	v_cvt_pk_f32_fp8_sdwa v[156:157], v104 src0_sel:WORD_1
	v_cvt_pk_f32_fp8_e32 v[158:159], v105
	v_cvt_pk_f32_fp8_sdwa v[104:105], v105 src0_sel:WORD_1
	v_pk_add_f32 v[130:131], v[130:131], v[134:135]
	v_mul_f32_e32 v134, 0x3d000000, v95
	v_cvt_pk_f32_fp8_sdwa v[150:151], v118 src0_sel:WORD_1
	v_cvt_pk_f32_fp8_e32 v[152:153], v119
	v_cvt_pk_f32_fp8_sdwa v[118:119], v119 src0_sel:WORD_1
	v_pk_add_f32 v[128:129], v[128:129], v[130:131]
	v_mul_f32_e32 v130, 0x3d000000, v94
	v_pk_mul_f32 v[154:155], v[134:135], v[154:155] op_sel_hi:[0,1]
	v_lshlrev_b32_e32 v94, 16, v60
	v_and_b32_e32 v95, 0xffff0000, v60
	v_pk_fma_f32 v[62:63], v[130:131], v[62:63], v[154:155] op_sel_hi:[0,1,1]
	v_pk_fma_f32 v[62:63], v[94:95], s[12:13], v[62:63] op_sel_hi:[1,0,1]
	v_pk_mul_f32 v[94:95], v[134:135], v[104:105] op_sel_hi:[0,1]
	v_pk_mul_f32 v[104:105], v[134:135], v[158:159] op_sel_hi:[0,1]
	v_pk_fma_f32 v[104:105], v[130:131], v[152:153], v[104:105] op_sel_hi:[0,1,1]
	v_pk_fma_f32 v[94:95], v[130:131], v[118:119], v[94:95] op_sel_hi:[0,1,1]
	s_waitcnt vmcnt(6)
	v_cvt_pk_f32_fp8_e32 v[154:155], v106
	v_pk_mul_f32 v[156:157], v[134:135], v[156:157] op_sel_hi:[0,1]
	v_pk_fma_f32 v[94:95], v[148:149], s[12:13], v[94:95] op_sel_hi:[1,0,1]
	v_pk_fma_f32 v[104:105], v[146:147], s[12:13], v[104:105] op_sel_hi:[1,0,1]
	v_lshlrev_b32_e32 v146, 16, v58
	v_and_b32_e32 v147, 0xffff0000, v58
	v_lshlrev_b32_e32 v148, 16, v59
	v_and_b32_e32 v149, 0xffff0000, v59
	v_cvt_pk_f32_fp8_e32 v[58:59], v108
	v_lshlrev_b32_e32 v60, 16, v61
	v_and_b32_e32 v61, 0xffff0000, v61
	v_pk_fma_f32 v[150:151], v[130:131], v[150:151], v[156:157] op_sel_hi:[0,1,1]
	v_cvt_pk_f32_fp8_sdwa v[156:157], v106 src0_sel:WORD_1
	v_cvt_pk_f32_fp8_e32 v[158:159], v107
	v_pk_fma_f32 v[60:61], v[60:61], s[12:13], v[150:151] op_sel_hi:[1,0,1]
	v_cvt_pk_f32_fp8_sdwa v[150:151], v108 src0_sel:WORD_1
	v_cvt_pk_f32_fp8_e32 v[152:153], v109
	v_cvt_pk_f32_fp8_sdwa v[106:107], v107 src0_sel:WORD_1
	v_cvt_pk_f32_fp8_sdwa v[108:109], v109 src0_sel:WORD_1
	v_pk_mul_f32 v[154:155], v[134:135], v[154:155] op_sel_hi:[0,1]
	v_lshlrev_b32_e32 v118, 16, v56
	v_and_b32_e32 v119, 0xffff0000, v56
	v_pk_fma_f32 v[58:59], v[130:131], v[58:59], v[154:155] op_sel_hi:[0,1,1]
	v_pk_mul_f32 v[156:157], v[134:135], v[156:157] op_sel_hi:[0,1]
	v_pk_fma_f32 v[58:59], v[118:119], s[12:13], v[58:59] op_sel_hi:[1,0,1]
	v_pk_mul_f32 v[118:119], v[134:135], v[158:159] op_sel_hi:[0,1]
	v_lshlrev_b32_e32 v56, 16, v57
	v_and_b32_e32 v57, 0xffff0000, v57
	v_pk_fma_f32 v[150:151], v[130:131], v[150:151], v[156:157] op_sel_hi:[0,1,1]
	v_pk_mul_f32 v[106:107], v[134:135], v[106:107] op_sel_hi:[0,1]
	v_pk_fma_f32 v[118:119], v[130:131], v[152:153], v[118:119] op_sel_hi:[0,1,1]
	v_pk_fma_f32 v[56:57], v[56:57], s[12:13], v[150:151] op_sel_hi:[1,0,1]
	v_pk_fma_f32 v[106:107], v[130:131], v[108:109], v[106:107] op_sel_hi:[0,1,1]
	v_pk_fma_f32 v[108:109], v[146:147], s[12:13], v[118:119] op_sel_hi:[1,0,1]
	v_mov_b32_e32 v118, v62
	v_mov_b32_e32 v119, v58
	v_mov_b32_e32 v130, v63
	v_mov_b32_e32 v131, v59
	v_pk_add_f32 v[118:119], v[118:119], v[130:131]
	v_mov_b32_e32 v130, v60
	v_mov_b32_e32 v131, v56
	v_mov_b32_e32 v134, v61
	v_mov_b32_e32 v135, v57
	v_pk_add_f32 v[130:131], v[130:131], v[134:135]
	v_pk_fma_f32 v[106:107], v[148:149], s[12:13], v[106:107] op_sel_hi:[1,0,1]
	v_pk_add_f32 v[118:119], v[118:119], v[130:131]
	v_mov_b32_e32 v130, v104
	v_mov_b32_e32 v131, v108
	v_mov_b32_e32 v134, v105
	v_mov_b32_e32 v135, v109
	v_pk_add_f32 v[130:131], v[130:131], v[134:135]
	v_mov_b32_e32 v134, v94
	v_mov_b32_e32 v135, v106
	v_mov_b32_e32 v146, v95
	v_mov_b32_e32 v147, v107
	v_pk_add_f32 v[134:135], v[134:135], v[146:147]
	s_waitcnt vmcnt(3)
	v_cvt_pk_f32_fp8_e32 v[152:153], v110
	v_pk_add_f32 v[130:131], v[130:131], v[134:135]
	v_lshlrev_b32_e32 v134, 16, v54
	v_and_b32_e32 v135, 0xffff0000, v54
	v_lshlrev_b32_e32 v146, 16, v55
	v_and_b32_e32 v147, 0xffff0000, v55
	v_cvt_pk_f32_fp8_e32 v[54:55], v116
	v_pk_add_f32 v[118:119], v[118:119], v[130:131]
	v_cvt_pk_f32_fp8_sdwa v[154:155], v110 src0_sel:WORD_1
	v_cvt_pk_f32_fp8_e32 v[156:157], v111
	v_cvt_pk_f32_fp8_sdwa v[110:111], v111 src0_sel:WORD_1
	v_add_f32_e32 v128, 0, v128
	v_add_f32_e32 v118, 0, v118
	v_mul_f32_e32 v130, 0x3d000000, v93
	v_cvt_pk_f32_fp8_sdwa v[148:149], v116 src0_sel:WORD_1
	v_cvt_pk_f32_fp8_e32 v[150:151], v117
	v_cvt_pk_f32_fp8_sdwa v[116:117], v117 src0_sel:WORD_1
	v_add_f32_e32 v128, v128, v129
	v_add_f32_e32 v129, v118, v119
	v_mul_f32_e32 v118, 0x3d000000, v92
	v_pk_mul_f32 v[152:153], v[130:131], v[152:153] op_sel_hi:[0,1]
	v_lshlrev_b32_e32 v92, 16, v52
	v_and_b32_e32 v93, 0xffff0000, v52
	v_pk_fma_f32 v[54:55], v[118:119], v[54:55], v[152:153] op_sel_hi:[0,1,1]
	v_pk_mul_f32 v[154:155], v[130:131], v[154:155] op_sel_hi:[0,1]
	v_pk_fma_f32 v[54:55], v[92:93], s[12:13], v[54:55] op_sel_hi:[1,0,1]
	v_pk_mul_f32 v[92:93], v[130:131], v[110:111] op_sel_hi:[0,1]
	v_lshlrev_b32_e32 v52, 16, v53
	v_and_b32_e32 v53, 0xffff0000, v53
	v_pk_fma_f32 v[148:149], v[118:119], v[148:149], v[154:155] op_sel_hi:[0,1,1]
	v_pk_mul_f32 v[110:111], v[130:131], v[156:157] op_sel_hi:[0,1]
	v_pk_fma_f32 v[92:93], v[118:119], v[116:117], v[92:93] op_sel_hi:[0,1,1]
	s_waitcnt vmcnt(0)
	v_cvt_pk_f32_fp8_sdwa v[154:155], v112 src0_sel:WORD_1
	v_pk_fma_f32 v[52:53], v[52:53], s[12:13], v[148:149] op_sel_hi:[1,0,1]
	v_pk_fma_f32 v[110:111], v[118:119], v[150:151], v[110:111] op_sel_hi:[0,1,1]
	v_pk_fma_f32 v[92:93], v[146:147], s[12:13], v[92:93] op_sel_hi:[1,0,1]
	v_cvt_pk_f32_fp8_e32 v[146:147], v114
	v_cvt_pk_f32_fp8_sdwa v[148:149], v114 src0_sel:WORD_1
	v_cvt_pk_f32_fp8_e32 v[150:151], v115
	v_cvt_pk_f32_fp8_sdwa v[152:153], v115 src0_sel:WORD_1
	v_cvt_pk_f32_fp8_e32 v[114:115], v112
	v_cvt_pk_f32_fp8_sdwa v[158:159], v113 src0_sel:WORD_1
	v_cvt_pk_f32_fp8_e32 v[156:157], v113
	v_pk_mul_f32 v[112:113], v[130:131], v[154:155] op_sel_hi:[0,1]
	v_lshlrev_b32_e32 v116, 16, v48
	v_and_b32_e32 v117, 0xffff0000, v48
	v_lshlrev_b32_e32 v48, 16, v49
	v_and_b32_e32 v49, 0xffff0000, v49
	v_pk_mul_f32 v[114:115], v[130:131], v[114:115] op_sel_hi:[0,1]
	v_pk_fma_f32 v[112:113], v[118:119], v[148:149], v[112:113] op_sel_hi:[0,1,1]
	v_pk_fma_f32 v[114:115], v[118:119], v[146:147], v[114:115] op_sel_hi:[0,1,1]
	v_pk_fma_f32 v[112:113], v[48:49], s[12:13], v[112:113] op_sel_hi:[1,0,1]
	v_pk_mul_f32 v[48:49], v[130:131], v[158:159] op_sel_hi:[0,1]
	v_pk_fma_f32 v[110:111], v[134:135], s[12:13], v[110:111] op_sel_hi:[1,0,1]
	v_lshlrev_b32_e32 v134, 16, v50
	v_and_b32_e32 v135, 0xffff0000, v50
	v_lshlrev_b32_e32 v50, 16, v51
	v_and_b32_e32 v51, 0xffff0000, v51
	v_pk_fma_f32 v[114:115], v[116:117], s[12:13], v[114:115] op_sel_hi:[1,0,1]
	v_pk_mul_f32 v[116:117], v[130:131], v[156:157] op_sel_hi:[0,1]
	v_pk_fma_f32 v[48:49], v[118:119], v[152:153], v[48:49] op_sel_hi:[0,1,1]
	v_pk_fma_f32 v[130:131], v[118:119], v[150:151], v[116:117] op_sel_hi:[0,1,1]
	v_pk_fma_f32 v[116:117], v[50:51], s[12:13], v[48:49] op_sel_hi:[1,0,1]
	v_mov_b32_e32 v48, v54
	v_mov_b32_e32 v49, v114
	v_mov_b32_e32 v50, v55
	v_mov_b32_e32 v51, v115
	v_pk_fma_f32 v[118:119], v[134:135], s[12:13], v[130:131] op_sel_hi:[1,0,1]
	v_pk_add_f32 v[48:49], v[48:49], v[50:51]
	v_mov_b32_e32 v50, v52
	v_mov_b32_e32 v51, v112
	v_mov_b32_e32 v130, v53
	v_mov_b32_e32 v131, v113
	v_pk_add_f32 v[50:51], v[50:51], v[130:131]
	v_mov_b32_e32 v130, v111
	v_pk_add_f32 v[48:49], v[48:49], v[50:51]
	v_mov_b32_e32 v50, v110
	v_mov_b32_e32 v51, v118
	v_mov_b32_e32 v131, v119
	v_pk_add_f32 v[50:51], v[50:51], v[130:131]
	v_mov_b32_e32 v130, v92
	v_mov_b32_e32 v131, v116
	v_mov_b32_e32 v134, v93
	v_mov_b32_e32 v135, v117
	v_pk_add_f32 v[130:131], v[130:131], v[134:135]
	s_add_i32 s18, s0, s4
	v_pk_add_f32 v[50:51], v[50:51], v[130:131]
	s_cmp_lt_i32 s18, 0x8000
	v_pk_add_f32 v[48:49], v[48:49], v[50:51]
	ds_bpermute_b32 v50, v137, v128
	v_add_f32_e32 v48, 0, v48
	v_add_f32_e32 v48, v48, v49
	ds_bpermute_b32 v49, v137, v132
	ds_bpermute_b32 v51, v137, v129
	s_waitcnt lgkmcnt(2)
	v_add_f32_e32 v50, v128, v50
	ds_bpermute_b32 v128, v137, v48
	s_cselect_b64 s[14:15], -1, 0
	s_waitcnt lgkmcnt(2)
	v_add_f32_e32 v49, v132, v49
	s_waitcnt lgkmcnt(1)
	v_add_f32_e32 v51, v129, v51
	s_and_b64 s[20:21], s[14:15], exec
	s_waitcnt lgkmcnt(0)
	v_add_f32_e32 v48, v48, v128
	ds_bpermute_b32 v128, v138, v49
	s_cselect_b32 s0, s18, s0
	s_ashr_i32 s1, s0, 31
	s_lshl_b64 s[0:1], s[0:1], 5
	s_add_u32 s0, s26, s0
	s_waitcnt lgkmcnt(0)
	v_add_f32_e32 v49, v49, v128
	ds_bpermute_b32 v128, v138, v50
	s_addc_u32 s1, s27, s1
	global_load_dwordx2 v[84:85], v136, s[0:1] offset:16
	global_load_dwordx4 v[44:47], v136, s[0:1]
	global_load_dwordx2 v[86:87], v136, s[0:1] offset:48
	global_load_dwordx4 v[40:43], v136, s[0:1] offset:32
	global_load_dwordx2 v[88:89], v136, s[0:1] offset:80
	global_load_dwordx4 v[36:39], v136, s[0:1] offset:64
	global_load_dwordx2 v[90:91], v136, s[0:1] offset:112
	global_load_dwordx4 v[32:35], v136, s[0:1] offset:96
	s_waitcnt lgkmcnt(0)
	v_add_f32_e32 v50, v50, v128
	ds_bpermute_b32 v128, v138, v51
	s_waitcnt lgkmcnt(0)
	v_add_f32_e32 v51, v51, v128
	ds_bpermute_b32 v128, v138, v48
	s_waitcnt lgkmcnt(0)
	v_add_f32_e32 v48, v48, v128
	ds_bpermute_b32 v128, v139, v49
	s_waitcnt lgkmcnt(0)
	v_add_f32_e32 v49, v49, v128
	ds_bpermute_b32 v128, v139, v50
	s_waitcnt lgkmcnt(0)
	v_add_f32_e32 v50, v50, v128
	ds_bpermute_b32 v128, v139, v51
	s_waitcnt lgkmcnt(0)
	v_add_f32_e32 v51, v51, v128
	ds_bpermute_b32 v128, v139, v48
	s_waitcnt lgkmcnt(0)
	v_add_f32_e32 v48, v48, v128
	ds_bpermute_b32 v128, v140, v49
	s_waitcnt lgkmcnt(0)
	v_add_f32_e32 v49, v49, v128
	ds_bpermute_b32 v128, v140, v50
	s_waitcnt lgkmcnt(0)
	v_add_f32_e32 v50, v50, v128
	ds_bpermute_b32 v128, v140, v51
	s_waitcnt lgkmcnt(0)
	v_add_f32_e32 v51, v51, v128
	ds_bpermute_b32 v128, v140, v48
	s_waitcnt lgkmcnt(0)
	v_add_f32_e32 v48, v48, v128
	ds_bpermute_b32 v128, v141, v49
	s_waitcnt lgkmcnt(0)
	v_add_f32_e32 v49, v49, v128
	ds_bpermute_b32 v128, v141, v50
	s_waitcnt lgkmcnt(0)
	v_add_f32_e32 v50, v50, v128
	ds_bpermute_b32 v128, v141, v51
	s_waitcnt lgkmcnt(0)
	v_add_f32_e32 v51, v51, v128
	ds_bpermute_b32 v128, v141, v48
	s_waitcnt lgkmcnt(0)
	v_add_f32_e32 v48, v48, v128
	ds_bpermute_b32 v128, v142, v49
	s_waitcnt lgkmcnt(0)
	v_add_f32_e32 v132, v49, v128
	ds_bpermute_b32 v49, v142, v50
	v_fmamk_f32 v123, v132, 0xba800000, v123
	v_fmac_f32_e32 v122, 0xba800000, v132
	v_fmamk_f32 v121, v132, 0xba800000, v121
	v_fmac_f32_e32 v120, 0xba800000, v132
	s_waitcnt lgkmcnt(0)
	v_add_f32_e32 v133, v50, v49
	ds_bpermute_b32 v49, v142, v51
	v_fmamk_f32 v127, v132, 0xba800000, v127
	v_fmac_f32_e32 v126, 0xba800000, v132
	v_fmamk_f32 v125, v132, 0xba800000, v125
	v_fmac_f32_e32 v124, 0xba800000, v132
	s_waitcnt lgkmcnt(0)
	v_add_f32_e32 v134, v51, v49
	ds_bpermute_b32 v49, v142, v48
	v_pk_mul_f32 v[50:51], v[122:123], v[122:123]
	v_fmac_f32_e32 v74, 0xba800000, v132
	v_fmamk_f32 v75, v132, 0xba800000, v75
	v_fmac_f32_e32 v72, 0xba800000, v132
	s_waitcnt lgkmcnt(0)
	v_add_f32_e32 v135, v48, v49
	v_pk_mul_f32 v[48:49], v[120:121], v[120:121]
	v_fmamk_f32 v73, v132, 0xba800000, v73
	v_pk_mov_b32 v[128:129], v[50:51], v[48:49] op_sel:[1,0]
	v_mov_b32_e32 v51, v49
	v_pk_add_f32 v[48:49], v[128:129], v[50:51]
	v_pk_mul_f32 v[50:51], v[124:125], v[124:125]
	v_pk_add_f32 v[48:49], v[48:49], v[48:49] op_sel_hi:[0,1]
	v_pk_mul_f32 v[128:129], v[126:127], v[126:127]
	v_mul_f32_e32 v48, v74, v74
	v_pk_mov_b32 v[130:131], v[128:129], v[50:51] op_sel:[1,0]
	v_mov_b32_e32 v129, v51
	v_pk_add_f32 v[50:51], v[130:131], v[128:129]
	v_pk_fma_f32 v[128:129], v[74:75], v[74:75], v[48:49] op_sel_hi:[1,1,0]
	v_mul_f32_e32 v48, v72, v72
	v_pk_add_f32 v[50:51], v[50:51], v[50:51] op_sel_hi:[0,1]
	v_pk_fma_f32 v[130:131], v[72:73], v[72:73], v[48:49] op_sel_hi:[1,1,0]
	v_fmamk_f32 v77, v132, 0xba800000, v77
	v_fmac_f32_e32 v76, 0xba800000, v132
	v_fmamk_f32 v79, v132, 0xba800000, v79
	v_fmac_f32_e32 v78, 0xba800000, v132
	v_mul_f32_e32 v128, v78, v78
	v_mul_f32_e32 v130, v79, v79
	v_mul_f32_e32 v48, v76, v76
	v_mul_f32_e32 v50, v77, v77
	v_pk_add_f32 v[128:129], v[128:129], v[130:131]
	v_pk_add_f32 v[48:49], v[48:49], v[50:51]
	v_fmamk_f32 v71, v133, 0xba800000, v71
	v_pk_add_f32 v[48:49], v[128:129], v[48:49]
	v_fmac_f32_e32 v70, 0xba800000, v133
	v_fmamk_f32 v69, v133, 0xba800000, v69
	v_fmac_f32_e32 v68, 0xba800000, v133
	v_add_f32_e32 v132, v48, v49
	v_pk_mul_f32 v[48:49], v[68:69], v[68:69]
	v_pk_mul_f32 v[50:51], v[70:71], v[70:71]
	v_fmamk_f32 v99, v133, 0xba800000, v99
	v_pk_mov_b32 v[128:129], v[50:51], v[48:49] op_sel:[1,0]
	v_mov_b32_e32 v51, v49
	v_pk_add_f32 v[48:49], v[128:129], v[50:51]
	v_fmac_f32_e32 v98, 0xba800000, v133
	v_fmamk_f32 v97, v133, 0xba800000, v97
	v_fmac_f32_e32 v96, 0xba800000, v133
	v_pk_add_f32 v[48:49], v[48:49], v[48:49] op_sel_hi:[0,1]
	v_pk_mul_f32 v[50:51], v[96:97], v[96:97]
	v_pk_mul_f32 v[128:129], v[98:99], v[98:99]
	v_fmac_f32_e32 v66, 0xba800000, v133
	v_pk_mov_b32 v[130:131], v[128:129], v[50:51] op_sel:[1,0]
	v_mov_b32_e32 v129, v51
	v_fmamk_f32 v67, v133, 0xba800000, v67
	v_fmac_f32_e32 v64, 0xba800000, v133
	v_mul_f32_e32 v48, v66, v66
	v_pk_add_f32 v[50:51], v[130:131], v[128:129]
	v_fmamk_f32 v65, v133, 0xba800000, v65
	v_pk_fma_f32 v[128:129], v[66:67], v[66:67], v[48:49] op_sel_hi:[1,1,0]
	v_mul_f32_e32 v48, v64, v64
	v_pk_add_f32 v[50:51], v[50:51], v[50:51] op_sel_hi:[0,1]
	v_pk_fma_f32 v[130:131], v[64:65], v[64:65], v[48:49] op_sel_hi:[1,1,0]
	v_fmamk_f32 v101, v133, 0xba800000, v101
	v_fmac_f32_e32 v100, 0xba800000, v133
	v_fmamk_f32 v103, v133, 0xba800000, v103
	v_fmac_f32_e32 v102, 0xba800000, v133
	v_mul_f32_e32 v128, v102, v102
	v_mul_f32_e32 v130, v103, v103
	v_mul_f32_e32 v48, v100, v100
	v_mul_f32_e32 v50, v101, v101
	v_pk_add_f32 v[128:129], v[128:129], v[130:131]
	v_pk_add_f32 v[48:49], v[48:49], v[50:51]
	v_fmamk_f32 v63, v134, 0xba800000, v63
	v_pk_add_f32 v[48:49], v[128:129], v[48:49]
	v_fmac_f32_e32 v62, 0xba800000, v134
	v_fmamk_f32 v61, v134, 0xba800000, v61
	v_fmac_f32_e32 v60, 0xba800000, v134
	v_add_f32_e32 v133, v48, v49
	v_pk_mul_f32 v[48:49], v[60:61], v[60:61]
	v_pk_mul_f32 v[50:51], v[62:63], v[62:63]
	v_fmamk_f32 v105, v134, 0xba800000, v105
	v_pk_mov_b32 v[128:129], v[50:51], v[48:49] op_sel:[1,0]
	v_mov_b32_e32 v51, v49
	v_pk_add_f32 v[48:49], v[128:129], v[50:51]
	v_fmac_f32_e32 v104, 0xba800000, v134
	v_fmamk_f32 v95, v134, 0xba800000, v95
	v_fmac_f32_e32 v94, 0xba800000, v134
	v_pk_add_f32 v[48:49], v[48:49], v[48:49] op_sel_hi:[0,1]
	v_pk_mul_f32 v[50:51], v[94:95], v[94:95]
	v_pk_mul_f32 v[128:129], v[104:105], v[104:105]
	v_fmac_f32_e32 v58, 0xba800000, v134
	v_pk_mov_b32 v[130:131], v[128:129], v[50:51] op_sel:[1,0]
	v_mov_b32_e32 v129, v51
	v_fmamk_f32 v59, v134, 0xba800000, v59
	v_fmac_f32_e32 v56, 0xba800000, v134
	v_mul_f32_e32 v48, v58, v58
	v_pk_add_f32 v[50:51], v[130:131], v[128:129]
	v_fmamk_f32 v57, v134, 0xba800000, v57
	v_pk_fma_f32 v[128:129], v[58:59], v[58:59], v[48:49] op_sel_hi:[1,1,0]
	v_mul_f32_e32 v48, v56, v56
	v_pk_add_f32 v[50:51], v[50:51], v[50:51] op_sel_hi:[0,1]
	v_pk_fma_f32 v[130:131], v[56:57], v[56:57], v[48:49] op_sel_hi:[1,1,0]
	v_fmamk_f32 v107, v134, 0xba800000, v107
	v_fmac_f32_e32 v106, 0xba800000, v134
	v_fmamk_f32 v109, v134, 0xba800000, v109
	v_fmac_f32_e32 v108, 0xba800000, v134
	v_mul_f32_e32 v128, v108, v108
	v_mul_f32_e32 v130, v109, v109
	v_mul_f32_e32 v48, v106, v106
	v_mul_f32_e32 v50, v107, v107
	v_pk_add_f32 v[128:129], v[128:129], v[130:131]
	v_pk_add_f32 v[48:49], v[48:49], v[50:51]
	v_fmamk_f32 v55, v135, 0xba800000, v55
	v_pk_add_f32 v[48:49], v[128:129], v[48:49]
	v_fmac_f32_e32 v54, 0xba800000, v135
	v_fmamk_f32 v53, v135, 0xba800000, v53
	v_fmac_f32_e32 v52, 0xba800000, v135
	v_add_f32_e32 v134, v48, v49
	v_pk_mul_f32 v[48:49], v[52:53], v[52:53]
	v_pk_mul_f32 v[50:51], v[54:55], v[54:55]
	v_fmamk_f32 v111, v135, 0xba800000, v111
	v_pk_mov_b32 v[128:129], v[50:51], v[48:49] op_sel:[1,0]
	v_mov_b32_e32 v51, v49
	v_pk_add_f32 v[48:49], v[128:129], v[50:51]
	v_fmac_f32_e32 v110, 0xba800000, v135
	v_fmamk_f32 v93, v135, 0xba800000, v93
	v_fmac_f32_e32 v92, 0xba800000, v135
	v_pk_add_f32 v[48:49], v[48:49], v[48:49] op_sel_hi:[0,1]
	v_pk_mul_f32 v[50:51], v[92:93], v[92:93]
	v_pk_mul_f32 v[128:129], v[110:111], v[110:111]
	v_fmac_f32_e32 v114, 0xba800000, v135
	v_pk_mov_b32 v[130:131], v[128:129], v[50:51] op_sel:[1,0]
	v_mov_b32_e32 v129, v51
	v_fmamk_f32 v115, v135, 0xba800000, v115
	v_fmac_f32_e32 v112, 0xba800000, v135
	v_mul_f32_e32 v48, v114, v114
	v_pk_add_f32 v[50:51], v[130:131], v[128:129]
	v_fmamk_f32 v113, v135, 0xba800000, v113
	v_pk_fma_f32 v[128:129], v[114:115], v[114:115], v[48:49] op_sel_hi:[1,1,0]
	v_mul_f32_e32 v48, v112, v112
	v_pk_add_f32 v[50:51], v[50:51], v[50:51] op_sel_hi:[0,1]
	v_pk_fma_f32 v[130:131], v[112:113], v[112:113], v[48:49] op_sel_hi:[1,1,0]
	v_fmamk_f32 v117, v135, 0xba800000, v117
	v_fmac_f32_e32 v116, 0xba800000, v135
	v_fmamk_f32 v119, v135, 0xba800000, v119
	v_fmac_f32_e32 v118, 0xba800000, v135
	v_mul_f32_e32 v128, v118, v118
	v_mul_f32_e32 v130, v119, v119
	v_mul_f32_e32 v48, v116, v116
	v_mul_f32_e32 v50, v117, v117
	v_pk_add_f32 v[128:129], v[128:129], v[130:131]
	v_pk_add_f32 v[48:49], v[48:49], v[50:51]
	ds_bpermute_b32 v50, v137, v133
	v_pk_add_f32 v[48:49], v[128:129], v[48:49]
	ds_bpermute_b32 v51, v137, v134
	v_add_f32_e32 v48, v48, v49
	ds_bpermute_b32 v49, v137, v132
	ds_bpermute_b32 v128, v137, v48
	s_waitcnt lgkmcnt(3)
	v_add_f32_e32 v50, v133, v50
	s_waitcnt lgkmcnt(2)
	v_add_f32_e32 v51, v134, v51
	s_waitcnt lgkmcnt(1)
	v_add_f32_e32 v49, v132, v49
	s_waitcnt lgkmcnt(0)
	v_add_f32_e32 v48, v48, v128
	ds_bpermute_b32 v128, v138, v49
	s_waitcnt lgkmcnt(0)
	v_add_f32_e32 v49, v49, v128
	ds_bpermute_b32 v128, v138, v50
	s_waitcnt lgkmcnt(0)
	v_add_f32_e32 v50, v50, v128
	ds_bpermute_b32 v128, v138, v51
	s_waitcnt lgkmcnt(0)
	v_add_f32_e32 v51, v51, v128
	ds_bpermute_b32 v128, v138, v48
	s_waitcnt lgkmcnt(0)
	v_add_f32_e32 v48, v48, v128
	ds_bpermute_b32 v128, v139, v49
	s_waitcnt lgkmcnt(0)
	v_add_f32_e32 v49, v49, v128
	ds_bpermute_b32 v128, v139, v50
	s_waitcnt lgkmcnt(0)
	v_add_f32_e32 v50, v50, v128
	ds_bpermute_b32 v128, v139, v51
	s_waitcnt lgkmcnt(0)
	v_add_f32_e32 v51, v51, v128
	ds_bpermute_b32 v128, v139, v48
	s_waitcnt lgkmcnt(0)
	v_add_f32_e32 v48, v48, v128
	ds_bpermute_b32 v128, v140, v49
	s_waitcnt lgkmcnt(0)
	v_add_f32_e32 v49, v49, v128
	ds_bpermute_b32 v128, v140, v50
	s_waitcnt lgkmcnt(0)
	v_add_f32_e32 v50, v50, v128
	ds_bpermute_b32 v128, v140, v51
	s_waitcnt lgkmcnt(0)
	v_add_f32_e32 v51, v51, v128
	ds_bpermute_b32 v128, v140, v48
	s_waitcnt lgkmcnt(0)
	v_add_f32_e32 v48, v48, v128
	ds_bpermute_b32 v128, v141, v49
	s_waitcnt lgkmcnt(0)
	v_add_f32_e32 v49, v49, v128
	ds_bpermute_b32 v128, v141, v50
	s_waitcnt lgkmcnt(0)
	v_add_f32_e32 v50, v50, v128
	ds_bpermute_b32 v128, v141, v51
	s_waitcnt lgkmcnt(0)
	v_add_f32_e32 v51, v51, v128
	ds_bpermute_b32 v128, v141, v48
	s_waitcnt lgkmcnt(0)
	v_add_f32_e32 v48, v48, v128
	ds_bpermute_b32 v128, v142, v49
	s_waitcnt lgkmcnt(0)
	v_add_f32_e32 v49, v49, v128
	ds_bpermute_b32 v128, v142, v50
	s_waitcnt lgkmcnt(0)
	v_add_f32_e32 v131, v50, v128
	ds_bpermute_b32 v50, v142, v51
	s_waitcnt lgkmcnt(0)
	v_add_f32_e32 v130, v51, v50
	ds_bpermute_b32 v50, v142, v48
	s_waitcnt lgkmcnt(0)
	v_add_f32_e32 v129, v48, v50
	v_fmamk_f32 v48, v49, 0x3a800000, v143
	v_cmp_gt_f32_e32 vcc, s16, v48
	v_mul_f32_e32 v49, 0x4f800000, v48
	s_nop 0
	v_cndmask_b32_e32 v48, v48, v49, vcc
	v_sqrt_f32_e32 v49, v48
	s_nop 0
	v_add_u32_e32 v50, -1, v49
	v_fma_f32 v51, -v50, v49, v48
	v_cmp_ge_f32_e64 s[0:1], 0, v51
	v_add_u32_e32 v51, 1, v49
	s_nop 0
	v_cndmask_b32_e64 v50, v49, v50, s[0:1]
	v_fma_f32 v49, -v51, v49, v48
	v_cmp_lt_f32_e64 s[0:1], 0, v49
	s_nop 1
	v_cndmask_b32_e64 v49, v50, v51, s[0:1]
	v_mul_f32_e32 v50, 0x37800000, v49
	v_cndmask_b32_e32 v49, v49, v50, vcc
	v_cmp_class_f32_e32 vcc, v48, v144
	s_nop 1
	v_cndmask_b32_e32 v48, v49, v48, vcc
	v_div_scale_f32 v49, s[0:1], v48, v48, 1.0
	v_rcp_f32_e32 v50, v49
	s_nop 0
	v_fma_f32 v51, -v49, v50, 1.0
	v_fmac_f32_e32 v50, v51, v50
	v_div_scale_f32 v51, vcc, 1.0, v48, 1.0
	v_mul_f32_e32 v128, v51, v50
	v_fma_f32 v132, -v49, v128, v51
	v_fmac_f32_e32 v128, v132, v50
	v_fma_f32 v49, -v49, v128, v51
	v_div_fmas_f32 v49, v49, v50, v128
	v_div_fixup_f32 v128, v49, v48, 1.0
	v_pk_mul_f32 v[48:49], v[126:127], v[128:129] op_sel_hi:[1,0]
	v_pk_mul_f32 v[50:51], v[124:125], v[128:129] op_sel_hi:[1,0]
	v_pk_mul_f32 v[120:121], v[120:121], v[128:129] op_sel_hi:[1,0]
	v_pk_fma_f32 v[124:125], v[2:3], v[50:51], v[10:11]
	v_pk_fma_f32 v[50:51], v[0:1], v[48:49], v[8:9]
	v_pk_mul_f32 v[48:49], v[122:123], v[128:129] op_sel_hi:[1,0]
	v_pk_fma_f32 v[120:121], v[6:7], v[120:121], v[14:15]
	v_pk_fma_f32 v[48:49], v[4:5], v[48:49], v[12:13]
	v_pk_mul_f32 v[72:73], v[72:73], v[128:129] op_sel_hi:[1,0]
	v_cvt_pk_bf16_f32 v48, v48, v49
	v_cvt_pk_bf16_f32 v49, v120, v121
	v_add_co_u32_e32 v120, vcc, s17, v82
	v_cvt_pk_bf16_f32 v50, v50, v51
	v_cvt_pk_bf16_f32 v51, v124, v125
	v_pk_fma_f32 v[72:73], v[22:23], v[72:73], v[30:31]
	s_nop 0
	v_addc_co_u32_e32 v121, vcc, -1, v83, vcc
	global_store_dwordx4 v[120:121], v[48:51], off offset:-3072 sc1
	s_nop 1
	v_pk_mul_f32 v[48:49], v[78:79], v[128:129] op_sel_hi:[1,0]
	v_pk_mul_f32 v[50:51], v[76:77], v[128:129] op_sel_hi:[1,0]
	s_nop 0
	v_pk_fma_f32 v[76:77], v[18:19], v[50:51], v[26:27]
	v_pk_fma_f32 v[50:51], v[16:17], v[48:49], v[24:25]
	v_pk_mul_f32 v[48:49], v[74:75], v[128:129] op_sel_hi:[1,0]
	s_nop 0
	v_pk_fma_f32 v[48:49], v[20:21], v[48:49], v[28:29]
	s_nop 0
	v_cvt_pk_bf16_f32 v48, v48, v49
	v_cvt_pk_bf16_f32 v49, v72, v73
	v_cvt_pk_bf16_f32 v50, v50, v51
	v_cvt_pk_bf16_f32 v51, v76, v77
	global_store_dwordx4 v[120:121], v[48:51], off offset:-2048 sc1
	s_nop 1
	v_fmamk_f32 v48, v131, 0x3a800000, v143
	v_cmp_gt_f32_e32 vcc, s16, v48
	v_mul_f32_e32 v49, 0x4f800000, v48
	s_nop 0
	v_cndmask_b32_e32 v48, v48, v49, vcc
	v_sqrt_f32_e32 v49, v48
	s_nop 0
	v_add_u32_e32 v50, -1, v49
	v_fma_f32 v51, -v50, v49, v48
	v_cmp_ge_f32_e64 s[0:1], 0, v51
	v_add_u32_e32 v51, 1, v49
	s_nop 0
	v_cndmask_b32_e64 v50, v49, v50, s[0:1]
	v_fma_f32 v49, -v51, v49, v48
	v_cmp_lt_f32_e64 s[0:1], 0, v49
	s_nop 1
	v_cndmask_b32_e64 v49, v50, v51, s[0:1]
	v_mul_f32_e32 v50, 0x37800000, v49
	v_cndmask_b32_e32 v49, v49, v50, vcc
	v_cmp_class_f32_e32 vcc, v48, v144
	s_nop 1
	v_cndmask_b32_e32 v48, v49, v48, vcc
	v_div_scale_f32 v49, s[0:1], v48, v48, 1.0
	v_rcp_f32_e32 v50, v49
	s_nop 0
	v_fma_f32 v51, -v49, v50, 1.0
	v_fmac_f32_e32 v50, v51, v50
	v_div_scale_f32 v51, vcc, 1.0, v48, 1.0
	v_mul_f32_e32 v72, v51, v50
	v_fma_f32 v73, -v49, v72, v51
	v_fmac_f32_e32 v72, v73, v50
	v_fma_f32 v49, -v49, v72, v51
	v_div_fmas_f32 v49, v49, v50, v72
	v_div_fixup_f32 v72, v49, v48, 1.0
	v_pk_mul_f32 v[48:49], v[98:99], v[72:73] op_sel_hi:[1,0]
	v_pk_mul_f32 v[50:51], v[96:97], v[72:73] op_sel_hi:[1,0]
	v_pk_mul_f32 v[68:69], v[68:69], v[72:73] op_sel_hi:[1,0]
	v_pk_fma_f32 v[74:75], v[2:3], v[50:51], v[10:11]
	v_pk_fma_f32 v[50:51], v[0:1], v[48:49], v[8:9]
	v_pk_mul_f32 v[48:49], v[70:71], v[72:73] op_sel_hi:[1,0]
	v_pk_fma_f32 v[68:69], v[6:7], v[68:69], v[14:15]
	v_pk_fma_f32 v[48:49], v[4:5], v[48:49], v[12:13]
	v_pk_mul_f32 v[64:65], v[64:65], v[72:73] op_sel_hi:[1,0]
	v_cvt_pk_bf16_f32 v48, v48, v49
	v_cvt_pk_bf16_f32 v49, v68, v69
	v_cvt_pk_bf16_f32 v50, v50, v51
	v_cvt_pk_bf16_f32 v51, v74, v75
	global_store_dwordx4 v[120:121], v[48:51], off offset:-1024 sc1
	v_pk_fma_f32 v[64:65], v[22:23], v[64:65], v[30:31]
	s_waitcnt vmcnt(10)
	v_mov_b64_e32 v[98:99], v[84:85]
	v_pk_mul_f32 v[48:49], v[102:103], v[72:73] op_sel_hi:[1,0]
	v_pk_mul_f32 v[50:51], v[100:101], v[72:73] op_sel_hi:[1,0]
	s_waitcnt vmcnt(8)
	v_mov_b64_e32 v[96:97], v[86:87]
	v_pk_fma_f32 v[68:69], v[18:19], v[50:51], v[26:27]
	v_pk_fma_f32 v[50:51], v[16:17], v[48:49], v[24:25]
	v_pk_mul_f32 v[48:49], v[66:67], v[72:73] op_sel_hi:[1,0]
	s_nop 0
	v_pk_fma_f32 v[48:49], v[20:21], v[48:49], v[28:29]
	s_nop 0
	v_cvt_pk_bf16_f32 v48, v48, v49
	v_cvt_pk_bf16_f32 v49, v64, v65
	v_add_co_u32_e32 v64, vcc, s24, v82
	v_cvt_pk_bf16_f32 v50, v50, v51
	v_cvt_pk_bf16_f32 v51, v68, v69
	s_nop 1
	v_addc_co_u32_e32 v65, vcc, -1, v83, vcc
	global_store_dwordx4 v[64:65], v[48:51], off offset:-4096 sc1
	v_lshl_add_u64 v[82:83], v[82:83], 0, s[6:7]
	s_nop 0
	v_fmamk_f32 v48, v130, 0x3a800000, v143
	v_cmp_gt_f32_e32 vcc, s16, v48
	v_mul_f32_e32 v49, 0x4f800000, v48
	s_nop 0
	v_cndmask_b32_e32 v48, v48, v49, vcc
	v_sqrt_f32_e32 v49, v48
	s_nop 0
	v_add_u32_e32 v50, -1, v49
	v_fma_f32 v51, -v50, v49, v48
	v_cmp_ge_f32_e64 s[0:1], 0, v51
	v_add_u32_e32 v51, 1, v49
	s_nop 0
	v_cndmask_b32_e64 v50, v49, v50, s[0:1]
	v_fma_f32 v49, -v51, v49, v48
	v_cmp_lt_f32_e64 s[0:1], 0, v49
	s_nop 1
	v_cndmask_b32_e64 v49, v50, v51, s[0:1]
	v_mul_f32_e32 v50, 0x37800000, v49
	v_cndmask_b32_e32 v49, v49, v50, vcc
	v_cmp_class_f32_e32 vcc, v48, v144
	s_nop 1
	v_cndmask_b32_e32 v48, v49, v48, vcc
	v_div_scale_f32 v49, s[0:1], v48, v48, 1.0
	v_rcp_f32_e32 v50, v49
	s_nop 0
	v_fma_f32 v51, -v49, v50, 1.0
	v_fmac_f32_e32 v50, v51, v50
	v_div_scale_f32 v51, vcc, 1.0, v48, 1.0
	v_mul_f32_e32 v66, v51, v50
	v_fma_f32 v67, -v49, v66, v51
	v_fmac_f32_e32 v66, v67, v50
	v_fma_f32 v49, -v49, v66, v51
	v_div_fmas_f32 v49, v49, v50, v66
	v_div_fixup_f32 v66, v49, v48, 1.0
	v_pk_mul_f32 v[48:49], v[104:105], v[66:67] op_sel_hi:[1,0]
	v_pk_mul_f32 v[50:51], v[94:95], v[66:67] op_sel_hi:[1,0]
	v_pk_mul_f32 v[60:61], v[60:61], v[66:67] op_sel_hi:[1,0]
	v_pk_fma_f32 v[68:69], v[2:3], v[50:51], v[10:11]
	v_pk_fma_f32 v[50:51], v[0:1], v[48:49], v[8:9]
	v_pk_mul_f32 v[48:49], v[62:63], v[66:67] op_sel_hi:[1,0]
	v_pk_fma_f32 v[60:61], v[6:7], v[60:61], v[14:15]
	v_pk_fma_f32 v[48:49], v[4:5], v[48:49], v[12:13]
	v_pk_mul_f32 v[56:57], v[56:57], v[66:67] op_sel_hi:[1,0]
	v_cvt_pk_bf16_f32 v48, v48, v49
	v_cvt_pk_bf16_f32 v49, v60, v61
	v_cvt_pk_bf16_f32 v50, v50, v51
	v_cvt_pk_bf16_f32 v51, v68, v69
	global_store_dwordx4 v[64:65], v[48:51], off offset:-3072 sc1
	v_pk_fma_f32 v[56:57], v[22:23], v[56:57], v[30:31]
	s_waitcnt vmcnt(8)
	v_mov_b64_e32 v[94:95], v[88:89]
	v_pk_mul_f32 v[48:49], v[108:109], v[66:67] op_sel_hi:[1,0]
	v_pk_mul_f32 v[50:51], v[106:107], v[66:67] op_sel_hi:[1,0]
	s_nop 0
	v_pk_fma_f32 v[60:61], v[18:19], v[50:51], v[26:27]
	v_pk_fma_f32 v[50:51], v[16:17], v[48:49], v[24:25]
	v_pk_mul_f32 v[48:49], v[58:59], v[66:67] op_sel_hi:[1,0]
	s_nop 0
	v_pk_fma_f32 v[48:49], v[20:21], v[48:49], v[28:29]
	s_nop 0
	v_cvt_pk_bf16_f32 v48, v48, v49
	v_cvt_pk_bf16_f32 v49, v56, v57
	v_cvt_pk_bf16_f32 v50, v50, v51
	v_cvt_pk_bf16_f32 v51, v60, v61
	global_store_dwordx4 v[64:65], v[48:51], off offset:-2048 sc1
	s_nop 1
	v_fmamk_f32 v48, v129, 0x3a800000, v143
	v_cmp_gt_f32_e32 vcc, s16, v48
	v_mul_f32_e32 v49, 0x4f800000, v48
	s_nop 0
	v_cndmask_b32_e32 v48, v48, v49, vcc
	v_sqrt_f32_e32 v49, v48
	s_nop 0
	v_add_u32_e32 v50, -1, v49
	v_fma_f32 v51, -v50, v49, v48
	v_cmp_ge_f32_e64 s[0:1], 0, v51
	v_add_u32_e32 v51, 1, v49
	s_nop 0
	v_cndmask_b32_e64 v50, v49, v50, s[0:1]
	v_fma_f32 v49, -v51, v49, v48
	v_cmp_lt_f32_e64 s[0:1], 0, v49
	s_nop 1
	v_cndmask_b32_e64 v49, v50, v51, s[0:1]
	v_mul_f32_e32 v50, 0x37800000, v49
	v_cndmask_b32_e32 v49, v49, v50, vcc
	v_cmp_class_f32_e32 vcc, v48, v144
	s_nop 1
	v_cndmask_b32_e32 v48, v49, v48, vcc
	v_div_scale_f32 v49, s[0:1], v48, v48, 1.0
	v_rcp_f32_e32 v50, v49
	s_mov_b32 s0, s18
	v_fma_f32 v51, -v49, v50, 1.0
	v_fmac_f32_e32 v50, v51, v50
	v_div_scale_f32 v51, vcc, 1.0, v48, 1.0
	v_mul_f32_e32 v56, v51, v50
	v_fma_f32 v57, -v49, v56, v51
	v_fmac_f32_e32 v56, v57, v50
	v_fma_f32 v49, -v49, v56, v51
	v_div_fmas_f32 v49, v49, v50, v56
	v_div_fixup_f32 v56, v49, v48, 1.0
	v_pk_mul_f32 v[48:49], v[110:111], v[56:57] op_sel_hi:[1,0]
	v_pk_mul_f32 v[50:51], v[92:93], v[56:57] op_sel_hi:[1,0]
	v_pk_mul_f32 v[52:53], v[52:53], v[56:57] op_sel_hi:[1,0]
	v_pk_fma_f32 v[58:59], v[2:3], v[50:51], v[10:11]
	v_pk_fma_f32 v[50:51], v[0:1], v[48:49], v[8:9]
	v_pk_mul_f32 v[48:49], v[54:55], v[56:57] op_sel_hi:[1,0]
	v_pk_fma_f32 v[52:53], v[6:7], v[52:53], v[14:15]
	v_pk_fma_f32 v[48:49], v[4:5], v[48:49], v[12:13]
	v_pk_mul_f32 v[54:55], v[112:113], v[56:57] op_sel_hi:[1,0]
	v_cvt_pk_bf16_f32 v48, v48, v49
	v_cvt_pk_bf16_f32 v49, v52, v53
	v_cvt_pk_bf16_f32 v50, v50, v51
	v_cvt_pk_bf16_f32 v51, v58, v59
	global_store_dwordx4 v[64:65], v[48:51], off offset:-1024 sc1
	s_and_b64 vcc, s[14:15], exec
	s_waitcnt vmcnt(8)
	v_mov_b64_e32 v[92:93], v[90:91]
	v_pk_mul_f32 v[48:49], v[118:119], v[56:57] op_sel_hi:[1,0]
	v_pk_mul_f32 v[50:51], v[116:117], v[56:57] op_sel_hi:[1,0]
	v_pk_fma_f32 v[54:55], v[22:23], v[54:55], v[30:31]
	v_pk_fma_f32 v[52:53], v[18:19], v[50:51], v[26:27]
	v_pk_fma_f32 v[50:51], v[16:17], v[48:49], v[24:25]
	v_pk_mul_f32 v[48:49], v[114:115], v[56:57] op_sel_hi:[1,0]
	s_nop 0
	v_pk_fma_f32 v[48:49], v[20:21], v[48:49], v[28:29]
	s_nop 0
	v_cvt_pk_bf16_f32 v48, v48, v49
	v_cvt_pk_bf16_f32 v49, v54, v55
	v_cvt_pk_bf16_f32 v50, v50, v51
	v_cvt_pk_bf16_f32 v51, v52, v53
	global_store_dwordx4 v[64:65], v[48:51], off sc1
	s_cbranch_vccnz .LBB0_994

.LBB0_1871:
	s_waitcnt vmcnt(0)
	v_lshlrev_b32_e32 v62, 2, v44
	v_add_co_u32_e32 v44, vcc, s19, v82
	v_ashrrev_i32_e32 v55, 31, v45
	v_mov_b32_e32 v54, v45
	v_addc_co_u32_e32 v45, vcc, -1, v83, vcc
	v_lshlrev_b32_e32 v64, 2, v40
	v_add_co_u32_e32 v40, vcc, s20, v82
	s_add_i32 s5, s38, s30
	v_lshlrev_b32_e32 v63, 2, v46
	v_ashrrev_i32_e32 v57, 31, v47
	v_mov_b32_e32 v56, v47
	v_ashrrev_i32_e32 v47, 31, v41
	v_mov_b32_e32 v46, v41
	v_lshlrev_b32_e32 v65, 2, v42
	v_ashrrev_i32_e32 v59, 31, v43
	v_mov_b32_e32 v58, v43
	v_addc_co_u32_e32 v41, vcc, -1, v83, vcc
	v_lshlrev_b32_e32 v66, 2, v36
	v_ashrrev_i32_e32 v43, 31, v37
	v_mov_b32_e32 v42, v37
	v_lshlrev_b32_e32 v67, 2, v38
	v_ashrrev_i32_e32 v37, 31, v39
	v_mov_b32_e32 v36, v39
	v_lshlrev_b32_e32 v85, 2, v32
	v_ashrrev_i32_e32 v39, 31, v33
	v_mov_b32_e32 v38, v33
	v_lshlrev_b32_e32 v34, 2, v34
	v_ashrrev_i32_e32 v33, 31, v35
	v_mov_b32_e32 v32, v35
	v_add_u32_e32 v35, s18, v62
	s_cmp_lt_i32 s5, 0x8000
	v_mul_f32_e32 v84, 0x3d000000, v60
	v_mul_f32_e32 v86, 0x3d000000, v61
	v_mul_f32_e32 v88, 0x3d000000, v52
	v_mul_f32_e32 v90, 0x3d000000, v53
	v_mul_f32_e32 v92, 0x3d000000, v50
	v_mul_f32_e32 v94, 0x3d000000, v51
	v_mul_f32_e32 v98, 0x3d000000, v48
	v_mul_f32_e32 v100, 0x3d000000, v49
	v_lshlrev_b64 v[102:103], 10, v[54:55]
	v_add_u32_e32 v87, s18, v63
	v_lshlrev_b64 v[104:105], 10, v[56:57]
	global_load_dwordx4 v[76:79], v[44:45], off offset:-3072
	global_load_dwordx4 v[72:75], v[44:45], off offset:-2048
	v_add_u32_e32 v89, s18, v64
	v_lshlrev_b64 v[106:107], 10, v[46:47]
	v_add_u32_e32 v47, s18, v65
	v_lshlrev_b64 v[108:109], 10, v[58:59]
	global_load_dwordx4 v[68:71], v[44:45], off offset:-1024
	v_add_u32_e32 v45, s18, v66
	v_lshlrev_b64 v[110:111], 10, v[42:43]
	v_add_u32_e32 v43, s18, v67
	v_lshlrev_b64 v[112:113], 10, v[36:37]
	global_load_dwordx4 v[64:67], v[40:41], off offset:-4096
	global_load_dwordx4 v[60:63], v[40:41], off offset:-3072
	v_add_u32_e32 v37, s18, v85
	v_lshlrev_b64 v[114:115], 10, v[38:39]
	v_add_u32_e32 v39, s18, v34
	v_lshlrev_b64 v[116:117], 10, v[32:33]
	global_load_dwordx4 v[56:59], v[40:41], off offset:-2048
	global_load_dwordx4 v[52:55], v[40:41], off offset:-1024
	global_load_dwordx4 v[48:51], v[40:41], off
	ds_read_b32 v46, v35
	ds_read_b32 v44, v87
	ds_read_b32 v42, v89
	ds_read_b32 v40, v47
	ds_read_b32 v38, v45
	ds_read_b32 v36, v43
	ds_read_b32 v34, v37
	ds_read_b32 v32, v39
	s_cselect_b64 s[0:1], -1, 0
	s_and_b64 s[6:7], s[0:1], exec
	s_cselect_b32 s4, s5, s38
	s_mov_b32 s38, s5
	s_ashr_i32 s5, s4, 31
	s_lshl_b64 s[4:5], s[4:5], 5
	s_waitcnt lgkmcnt(7)
	v_ashrrev_i32_e32 v47, 31, v46
	s_waitcnt lgkmcnt(6)
	v_ashrrev_i32_e32 v45, 31, v44
	s_waitcnt lgkmcnt(5)
	v_ashrrev_i32_e32 v43, 31, v42
	s_waitcnt lgkmcnt(4)
	v_ashrrev_i32_e32 v41, 31, v40
	s_waitcnt lgkmcnt(3)
	v_ashrrev_i32_e32 v39, 31, v38
	s_waitcnt lgkmcnt(2)
	v_ashrrev_i32_e32 v37, 31, v36
	s_waitcnt lgkmcnt(1)
	v_ashrrev_i32_e32 v35, 31, v34
	s_waitcnt lgkmcnt(0)
	v_ashrrev_i32_e32 v33, 31, v32
	s_add_u32 s6, s42, s4
	v_lshlrev_b64 v[46:47], 18, v[46:47]
	v_lshlrev_b64 v[44:45], 18, v[44:45]
	v_lshlrev_b64 v[42:43], 18, v[42:43]
	v_lshlrev_b64 v[40:41], 18, v[40:41]
	v_lshlrev_b64 v[38:39], 18, v[38:39]
	v_lshlrev_b64 v[36:37], 18, v[36:37]
	v_lshlrev_b64 v[34:35], 18, v[34:35]
	v_lshlrev_b64 v[32:33], 18, v[32:33]
	s_addc_u32 s7, s43, s5
	v_lshl_add_u64 v[118:119], s[40:41], 0, v[46:47]
	v_lshl_add_u64 v[120:121], s[40:41], 0, v[44:45]
	v_lshl_add_u64 v[122:123], s[40:41], 0, v[42:43]
	v_lshl_add_u64 v[124:125], s[40:41], 0, v[40:41]
	v_lshl_add_u64 v[136:137], s[40:41], 0, v[38:39]
	v_lshl_add_u64 v[138:139], s[40:41], 0, v[36:37]
	v_lshl_add_u64 v[140:141], s[40:41], 0, v[34:35]
	v_lshl_add_u64 v[142:143], s[40:41], 0, v[32:33]
	global_load_dwordx2 v[144:145], v126, s[6:7] offset:16
	global_load_dwordx4 v[44:47], v126, s[6:7]
	global_load_dwordx2 v[146:147], v126, s[6:7] offset:48
	global_load_dwordx4 v[40:43], v126, s[6:7] offset:32
	global_load_dwordx2 v[148:149], v126, s[6:7] offset:80
	global_load_dwordx4 v[36:39], v126, s[6:7] offset:64
	global_load_dwordx2 v[150:151], v126, s[6:7] offset:112
	global_load_dwordx4 v[32:35], v126, s[6:7] offset:96
	v_lshl_add_u64 v[102:103], v[118:119], 0, v[102:103]
	v_lshl_add_u64 v[104:105], v[120:121], 0, v[104:105]
	v_lshl_add_u64 v[106:107], v[122:123], 0, v[106:107]
	v_lshl_add_u64 v[108:109], v[124:125], 0, v[108:109]
	v_lshl_add_u64 v[110:111], v[136:137], 0, v[110:111]
	v_lshl_add_u64 v[112:113], v[138:139], 0, v[112:113]
	v_lshl_add_u64 v[114:115], v[140:141], 0, v[114:115]
	v_lshl_add_u64 v[116:117], v[142:143], 0, v[116:117]
	v_lshl_add_u64 v[102:103], v[102:103], 0, v[80:81]
	v_lshl_add_u64 v[104:105], v[104:105], 0, v[80:81]
	v_lshl_add_u64 v[106:107], v[106:107], 0, v[80:81]
	v_lshl_add_u64 v[108:109], v[108:109], 0, v[80:81]
	v_lshl_add_u64 v[110:111], v[110:111], 0, v[80:81]
	v_lshl_add_u64 v[112:113], v[112:113], 0, v[80:81]
	v_lshl_add_u64 v[114:115], v[114:115], 0, v[80:81]
	v_lshl_add_u64 v[116:117], v[116:117], 0, v[80:81]
	global_load_dwordx2 v[118:119], v[102:103], off nt
	global_load_dwordx2 v[120:121], v[104:105], off nt
	s_nop 0
	global_load_dwordx2 v[104:105], v[104:105], off offset:512 nt
	s_nop 0
	global_load_dwordx2 v[102:103], v[102:103], off offset:512 nt
	s_nop 0
	global_load_dwordx2 v[122:123], v[106:107], off nt
	global_load_dwordx2 v[124:125], v[108:109], off nt
	s_nop 0
	global_load_dwordx2 v[108:109], v[108:109], off offset:512 nt
	s_nop 0
	global_load_dwordx2 v[106:107], v[106:107], off offset:512 nt
	s_nop 0
	global_load_dwordx2 v[136:137], v[110:111], off nt
	global_load_dwordx2 v[138:139], v[112:113], off nt
	s_nop 0
	global_load_dwordx2 v[112:113], v[112:113], off offset:512 nt
	s_nop 0
	global_load_dwordx2 v[110:111], v[110:111], off offset:512 nt
	s_nop 0
	global_load_dwordx2 v[140:141], v[114:115], off nt
	global_load_dwordx2 v[142:143], v[116:117], off nt
	s_nop 0
	global_load_dwordx2 v[116:117], v[116:117], off offset:512 nt
	s_nop 0
	global_load_dwordx2 v[114:115], v[114:115], off offset:512 nt
	v_add_co_u32_e32 v96, vcc, s22, v82
	s_and_b64 s[4:5], s[0:1], exec
	s_nop 0
	v_addc_co_u32_e32 v97, vcc, -1, v83, vcc
	s_waitcnt vmcnt(31)
	v_lshlrev_b32_e32 v152, 16, v76
	v_and_b32_e32 v153, 0xffff0000, v76
	v_lshlrev_b32_e32 v76, 16, v77
	v_and_b32_e32 v77, 0xffff0000, v77
	v_lshlrev_b32_e32 v154, 16, v78
	v_and_b32_e32 v155, 0xffff0000, v78
	v_lshlrev_b32_e32 v78, 16, v79
	v_and_b32_e32 v79, 0xffff0000, v79
	s_waitcnt vmcnt(30)
	v_lshlrev_b32_e32 v156, 16, v72
	v_and_b32_e32 v157, 0xffff0000, v72
	v_lshlrev_b32_e32 v72, 16, v73
	s_waitcnt vmcnt(27)
	v_lshlrev_b32_e32 v168, 16, v60
	v_and_b32_e32 v169, 0xffff0000, v60
	v_lshlrev_b32_e32 v170, 16, v61
	v_and_b32_e32 v171, 0xffff0000, v61
	s_waitcnt vmcnt(25)
	v_lshlrev_b32_e32 v178, 16, v52
	s_waitcnt vmcnt(24)
	v_lshlrev_b32_e32 v184, 16, v48
	v_and_b32_e32 v185, 0xffff0000, v48
	v_lshlrev_b32_e32 v186, 16, v49
	v_and_b32_e32 v187, 0xffff0000, v49
	v_and_b32_e32 v179, 0xffff0000, v52
	v_lshlrev_b32_e32 v180, 16, v53
	v_and_b32_e32 v181, 0xffff0000, v53
	v_lshlrev_b32_e32 v188, 16, v50
	v_and_b32_e32 v189, 0xffff0000, v50
	v_lshlrev_b32_e32 v190, 16, v51
	v_and_b32_e32 v191, 0xffff0000, v51
	v_and_b32_e32 v73, 0xffff0000, v73
	v_lshlrev_b32_e32 v158, 16, v74
	v_and_b32_e32 v159, 0xffff0000, v74
	v_lshlrev_b32_e32 v74, 16, v75
	v_and_b32_e32 v75, 0xffff0000, v75
	v_lshlrev_b32_e32 v160, 16, v68
	v_and_b32_e32 v161, 0xffff0000, v68
	v_lshlrev_b32_e32 v68, 16, v69
	v_and_b32_e32 v69, 0xffff0000, v69
	v_lshlrev_b32_e32 v162, 16, v70
	v_and_b32_e32 v163, 0xffff0000, v70
	v_lshlrev_b32_e32 v70, 16, v71
	v_and_b32_e32 v71, 0xffff0000, v71
	v_lshlrev_b32_e32 v164, 16, v64
	v_and_b32_e32 v165, 0xffff0000, v64
	v_lshlrev_b32_e32 v64, 16, v65
	s_waitcnt vmcnt(23)
	v_mov_b64_e32 v[60:61], v[144:145]
	v_and_b32_e32 v65, 0xffff0000, v65
	s_waitcnt vmcnt(21)
	v_mov_b64_e32 v[52:53], v[146:147]
	v_lshlrev_b32_e32 v166, 16, v66
	s_waitcnt vmcnt(19)
	v_mov_b64_e32 v[50:51], v[148:149]
	v_and_b32_e32 v167, 0xffff0000, v66
	s_waitcnt vmcnt(17)
	v_mov_b64_e32 v[48:49], v[150:151]
	v_lshlrev_b32_e32 v66, 16, v67
	v_and_b32_e32 v67, 0xffff0000, v67
	s_waitcnt vmcnt(15)
	v_cvt_pk_f32_fp8_e32 v[144:145], v118
	s_waitcnt vmcnt(14)
	v_cvt_pk_f32_fp8_e32 v[150:151], v120
	v_cvt_pk_f32_fp8_sdwa v[192:193], v120 src0_sel:WORD_1
	v_cvt_pk_f32_fp8_e32 v[194:195], v121
	v_cvt_pk_f32_fp8_sdwa v[120:121], v121 src0_sel:WORD_1
	s_waitcnt vmcnt(13)
	v_cvt_pk_f32_fp8_e32 v[202:203], v104
	v_cvt_pk_f32_fp8_sdwa v[204:205], v104 src0_sel:WORD_1
	v_cvt_pk_f32_fp8_e32 v[206:207], v105
	v_cvt_pk_f32_fp8_sdwa v[104:105], v105 src0_sel:WORD_1
	v_pk_mul_f32 v[150:151], v[86:87], v[150:151] op_sel_hi:[0,1]
	v_cvt_pk_f32_fp8_sdwa v[146:147], v118 src0_sel:WORD_1
	v_cvt_pk_f32_fp8_e32 v[148:149], v119
	v_cvt_pk_f32_fp8_sdwa v[118:119], v119 src0_sel:WORD_1
	s_waitcnt vmcnt(12)
	v_cvt_pk_f32_fp8_e32 v[196:197], v102
	v_cvt_pk_f32_fp8_sdwa v[198:199], v102 src0_sel:WORD_1
	v_cvt_pk_f32_fp8_e32 v[200:201], v103
	v_cvt_pk_f32_fp8_sdwa v[102:103], v103 src0_sel:WORD_1
	s_waitcnt vmcnt(10)
	v_cvt_pk_f32_fp8_e32 v[214:215], v124
	v_cvt_pk_f32_fp8_sdwa v[216:217], v124 src0_sel:WORD_1
	v_cvt_pk_f32_fp8_e32 v[218:219], v125
	v_cvt_pk_f32_fp8_sdwa v[124:125], v125 src0_sel:WORD_1
	s_waitcnt vmcnt(9)
	v_cvt_pk_f32_fp8_e32 v[226:227], v108
	v_cvt_pk_f32_fp8_sdwa v[228:229], v108 src0_sel:WORD_1
	v_cvt_pk_f32_fp8_e32 v[230:231], v109
	v_cvt_pk_f32_fp8_sdwa v[108:109], v109 src0_sel:WORD_1
	s_waitcnt vmcnt(6)
	v_cvt_pk_f32_fp8_e32 v[238:239], v138
	v_cvt_pk_f32_fp8_sdwa v[240:241], v138 src0_sel:WORD_1
	v_cvt_pk_f32_fp8_e32 v[242:243], v139
	v_cvt_pk_f32_fp8_sdwa v[138:139], v139 src0_sel:WORD_1
	s_waitcnt vmcnt(5)
	v_cvt_pk_f32_fp8_e32 v[250:251], v112
	v_pk_mul_f32 v[192:193], v[86:87], v[192:193] op_sel_hi:[0,1]
	v_pk_mul_f32 v[120:121], v[86:87], v[120:121] op_sel_hi:[0,1]
	v_pk_mul_f32 v[194:195], v[86:87], v[194:195] op_sel_hi:[0,1]
	v_pk_mul_f32 v[204:205], v[86:87], v[204:205] op_sel_hi:[0,1]
	v_pk_mul_f32 v[202:203], v[86:87], v[202:203] op_sel_hi:[0,1]
	v_pk_mul_f32 v[104:105], v[86:87], v[104:105] op_sel_hi:[0,1]
	v_pk_mul_f32 v[86:87], v[86:87], v[206:207] op_sel_hi:[0,1]
	v_cvt_pk_f32_fp8_sdwa v[206:207], v112 src0_sel:WORD_1
	v_pk_fma_f32 v[144:145], v[84:85], v[144:145], v[150:151] op_sel_hi:[0,1,1]
	v_cvt_pk_f32_fp8_e32 v[150:151], v113
	v_cvt_pk_f32_fp8_sdwa v[112:113], v113 src0_sel:WORD_1
	v_cvt_pk_f32_fp8_e32 v[208:209], v122
	v_pk_fma_f32 v[146:147], v[84:85], v[146:147], v[192:193] op_sel_hi:[0,1,1]
	v_pk_fma_f32 v[148:149], v[84:85], v[148:149], v[194:195] op_sel_hi:[0,1,1]
	v_pk_fma_f32 v[118:119], v[84:85], v[118:119], v[120:121] op_sel_hi:[0,1,1]
	v_pk_fma_f32 v[196:197], v[84:85], v[196:197], v[202:203] op_sel_hi:[0,1,1]
	s_waitcnt vmcnt(2)
	v_cvt_pk_f32_fp8_e32 v[202:203], v142
	v_pk_fma_f32 v[198:199], v[84:85], v[198:199], v[204:205] op_sel_hi:[0,1,1]
	v_cvt_pk_f32_fp8_sdwa v[204:205], v142 src0_sel:WORD_1
	v_pk_fma_f32 v[86:87], v[84:85], v[200:201], v[86:87] op_sel_hi:[0,1,1]
	v_cvt_pk_f32_fp8_e32 v[200:201], v143
	v_cvt_pk_f32_fp8_sdwa v[142:143], v143 src0_sel:WORD_1
	v_pk_fma_f32 v[84:85], v[84:85], v[102:103], v[104:105] op_sel_hi:[0,1,1]
	s_waitcnt vmcnt(1)
	v_cvt_pk_f32_fp8_e32 v[104:105], v116
	v_pk_mul_f32 v[216:217], v[90:91], v[216:217] op_sel_hi:[0,1]
	v_pk_mul_f32 v[214:215], v[90:91], v[214:215] op_sel_hi:[0,1]
	v_pk_mul_f32 v[124:125], v[90:91], v[124:125] op_sel_hi:[0,1]
	v_pk_mul_f32 v[218:219], v[90:91], v[218:219] op_sel_hi:[0,1]
	v_pk_mul_f32 v[228:229], v[90:91], v[228:229] op_sel_hi:[0,1]
	v_pk_mul_f32 v[226:227], v[90:91], v[226:227] op_sel_hi:[0,1]
	v_pk_mul_f32 v[108:109], v[90:91], v[108:109] op_sel_hi:[0,1]
	v_pk_mul_f32 v[90:91], v[90:91], v[230:231] op_sel_hi:[0,1]
	v_cvt_pk_f32_fp8_sdwa v[230:231], v116 src0_sel:WORD_1
	v_pk_mul_f32 v[240:241], v[94:95], v[240:241] op_sel_hi:[0,1]
	v_pk_mul_f32 v[238:239], v[94:95], v[238:239] op_sel_hi:[0,1]
	v_pk_mul_f32 v[138:139], v[94:95], v[138:139] op_sel_hi:[0,1]
	v_pk_mul_f32 v[242:243], v[94:95], v[242:243] op_sel_hi:[0,1]
	v_pk_mul_f32 v[206:207], v[94:95], v[206:207] op_sel_hi:[0,1]
	v_pk_mul_f32 v[250:251], v[94:95], v[250:251] op_sel_hi:[0,1]
	v_pk_mul_f32 v[112:113], v[94:95], v[112:113] op_sel_hi:[0,1]
	v_pk_mul_f32 v[94:95], v[94:95], v[150:151] op_sel_hi:[0,1]
	v_cvt_pk_f32_fp8_e32 v[150:151], v117
	v_cvt_pk_f32_fp8_sdwa v[116:117], v117 src0_sel:WORD_1
	v_cvt_pk_f32_fp8_sdwa v[210:211], v122 src0_sel:WORD_1
	v_cvt_pk_f32_fp8_e32 v[212:213], v123
	v_cvt_pk_f32_fp8_sdwa v[122:123], v123 src0_sel:WORD_1
	v_cvt_pk_f32_fp8_e32 v[220:221], v106
	v_cvt_pk_f32_fp8_sdwa v[222:223], v106 src0_sel:WORD_1
	v_cvt_pk_f32_fp8_e32 v[224:225], v107
	v_cvt_pk_f32_fp8_sdwa v[106:107], v107 src0_sel:WORD_1
	v_cvt_pk_f32_fp8_e32 v[232:233], v136
	v_cvt_pk_f32_fp8_sdwa v[234:235], v136 src0_sel:WORD_1
	v_cvt_pk_f32_fp8_e32 v[236:237], v137
	v_cvt_pk_f32_fp8_sdwa v[136:137], v137 src0_sel:WORD_1
	v_cvt_pk_f32_fp8_e32 v[244:245], v110
	v_cvt_pk_f32_fp8_sdwa v[246:247], v110 src0_sel:WORD_1
	v_cvt_pk_f32_fp8_e32 v[248:249], v111
	v_cvt_pk_f32_fp8_sdwa v[110:111], v111 src0_sel:WORD_1
	v_cvt_pk_f32_fp8_e32 v[192:193], v140
	v_cvt_pk_f32_fp8_sdwa v[194:195], v140 src0_sel:WORD_1
	v_cvt_pk_f32_fp8_e32 v[120:121], v141
	v_cvt_pk_f32_fp8_sdwa v[140:141], v141 src0_sel:WORD_1
	s_waitcnt vmcnt(0)
	v_cvt_pk_f32_fp8_e32 v[102:103], v114
	v_pk_mul_f32 v[204:205], v[100:101], v[204:205] op_sel_hi:[0,1]
	v_pk_mul_f32 v[202:203], v[100:101], v[202:203] op_sel_hi:[0,1]
	v_pk_mul_f32 v[142:143], v[100:101], v[142:143] op_sel_hi:[0,1]
	v_pk_mul_f32 v[200:201], v[100:101], v[200:201] op_sel_hi:[0,1]
	v_pk_mul_f32 v[230:231], v[100:101], v[230:231] op_sel_hi:[0,1]
	v_pk_mul_f32 v[104:105], v[100:101], v[104:105] op_sel_hi:[0,1]
	v_pk_mul_f32 v[116:117], v[100:101], v[116:117] op_sel_hi:[0,1]
	v_pk_mul_f32 v[100:101], v[100:101], v[150:151] op_sel_hi:[0,1]
	v_cvt_pk_f32_fp8_sdwa v[150:151], v114 src0_sel:WORD_1
	v_pk_fma_f32 v[208:209], v[88:89], v[208:209], v[214:215] op_sel_hi:[0,1,1]
	v_cvt_pk_f32_fp8_e32 v[214:215], v115
	v_cvt_pk_f32_fp8_sdwa v[114:115], v115 src0_sel:WORD_1
	v_lshlrev_b32_e32 v172, 16, v62
	v_and_b32_e32 v173, 0xffff0000, v62
	v_lshlrev_b32_e32 v62, 16, v63
	v_and_b32_e32 v63, 0xffff0000, v63
	v_lshlrev_b32_e32 v174, 16, v56
	v_and_b32_e32 v175, 0xffff0000, v56
	v_lshlrev_b32_e32 v56, 16, v57
	v_and_b32_e32 v57, 0xffff0000, v57
	v_lshlrev_b32_e32 v176, 16, v58
	v_and_b32_e32 v177, 0xffff0000, v58
	v_lshlrev_b32_e32 v58, 16, v59
	v_and_b32_e32 v59, 0xffff0000, v59
	v_lshlrev_b32_e32 v182, 16, v54
	v_and_b32_e32 v183, 0xffff0000, v54
	v_lshlrev_b32_e32 v54, 16, v55
	v_and_b32_e32 v55, 0xffff0000, v55
	v_pk_fma_f32 v[210:211], v[88:89], v[210:211], v[216:217] op_sel_hi:[0,1,1]
	v_pk_fma_f32 v[212:213], v[88:89], v[212:213], v[218:219] op_sel_hi:[0,1,1]
	v_pk_fma_f32 v[216:217], v[88:89], v[122:123], v[124:125] op_sel_hi:[0,1,1]
	v_pk_fma_f32 v[218:219], v[88:89], v[220:221], v[226:227] op_sel_hi:[0,1,1]
	v_pk_fma_f32 v[220:221], v[88:89], v[222:223], v[228:229] op_sel_hi:[0,1,1]
	v_pk_fma_f32 v[90:91], v[88:89], v[224:225], v[90:91] op_sel_hi:[0,1,1]
	v_pk_fma_f32 v[88:89], v[88:89], v[106:107], v[108:109] op_sel_hi:[0,1,1]
	v_pk_fma_f32 v[222:223], v[92:93], v[232:233], v[238:239] op_sel_hi:[0,1,1]
	v_pk_fma_f32 v[224:225], v[92:93], v[234:235], v[240:241] op_sel_hi:[0,1,1]
	v_pk_fma_f32 v[226:227], v[92:93], v[236:237], v[242:243] op_sel_hi:[0,1,1]
	v_pk_fma_f32 v[136:137], v[92:93], v[136:137], v[138:139] op_sel_hi:[0,1,1]
	v_pk_fma_f32 v[138:139], v[92:93], v[244:245], v[250:251] op_sel_hi:[0,1,1]
	v_pk_fma_f32 v[206:207], v[92:93], v[246:247], v[206:207] op_sel_hi:[0,1,1]
	v_pk_fma_f32 v[228:229], v[92:93], v[248:249], v[94:95] op_sel_hi:[0,1,1]
	v_pk_fma_f32 v[232:233], v[92:93], v[110:111], v[112:113] op_sel_hi:[0,1,1]
	v_pk_fma_f32 v[192:193], v[98:99], v[192:193], v[202:203] op_sel_hi:[0,1,1]
	v_pk_fma_f32 v[194:195], v[98:99], v[194:195], v[204:205] op_sel_hi:[0,1,1]
	v_pk_fma_f32 v[200:201], v[98:99], v[120:121], v[200:201] op_sel_hi:[0,1,1]
	v_pk_fma_f32 v[140:141], v[98:99], v[140:141], v[142:143] op_sel_hi:[0,1,1]
	v_pk_fma_f32 v[142:143], v[98:99], v[102:103], v[104:105] op_sel_hi:[0,1,1]
	v_pk_fma_f32 v[150:151], v[98:99], v[150:151], v[230:231] op_sel_hi:[0,1,1]
	v_pk_fma_f32 v[202:203], v[98:99], v[214:215], v[100:101] op_sel_hi:[0,1,1]
	v_pk_fma_f32 v[204:205], v[98:99], v[114:115], v[116:117] op_sel_hi:[0,1,1]
	v_pk_fma_f32 v[112:113], v[76:77], s[36:37], v[146:147] op_sel_hi:[1,0,1]
	v_pk_fma_f32 v[116:117], v[152:153], s[36:37], v[144:145] op_sel_hi:[1,0,1]
	v_pk_fma_f32 v[120:121], v[78:79], s[36:37], v[118:119] op_sel_hi:[1,0,1]
	v_pk_fma_f32 v[124:125], v[154:155], s[36:37], v[148:149] op_sel_hi:[1,0,1]
	v_pk_fma_f32 v[110:111], v[72:73], s[36:37], v[198:199] op_sel_hi:[1,0,1]
	v_pk_fma_f32 v[114:115], v[156:157], s[36:37], v[196:197] op_sel_hi:[1,0,1]
	v_pk_fma_f32 v[118:119], v[74:75], s[36:37], v[84:85] op_sel_hi:[1,0,1]
	v_pk_fma_f32 v[122:123], v[158:159], s[36:37], v[86:87] op_sel_hi:[1,0,1]
	v_pk_fma_f32 v[94:95], v[68:69], s[36:37], v[210:211] op_sel_hi:[1,0,1]
	v_pk_fma_f32 v[100:101], v[160:161], s[36:37], v[208:209] op_sel_hi:[1,0,1]
	v_pk_fma_f32 v[104:105], v[70:71], s[36:37], v[216:217] op_sel_hi:[1,0,1]
	v_pk_fma_f32 v[108:109], v[162:163], s[36:37], v[212:213] op_sel_hi:[1,0,1]
	v_pk_fma_f32 v[92:93], v[64:65], s[36:37], v[220:221] op_sel_hi:[1,0,1]
	v_pk_fma_f32 v[98:99], v[164:165], s[36:37], v[218:219] op_sel_hi:[1,0,1]
	v_pk_fma_f32 v[102:103], v[66:67], s[36:37], v[88:89] op_sel_hi:[1,0,1]
	v_pk_fma_f32 v[106:107], v[166:167], s[36:37], v[90:91] op_sel_hi:[1,0,1]
	v_pk_fma_f32 v[74:75], v[170:171], s[36:37], v[224:225] op_sel_hi:[1,0,1]
	v_pk_fma_f32 v[78:79], v[168:169], s[36:37], v[222:223] op_sel_hi:[1,0,1]
	v_pk_fma_f32 v[86:87], v[62:63], s[36:37], v[136:137] op_sel_hi:[1,0,1]
	v_pk_fma_f32 v[90:91], v[172:173], s[36:37], v[226:227] op_sel_hi:[1,0,1]
	v_pk_fma_f32 v[72:73], v[56:57], s[36:37], v[206:207] op_sel_hi:[1,0,1]
	v_pk_fma_f32 v[76:77], v[174:175], s[36:37], v[138:139] op_sel_hi:[1,0,1]
	v_pk_fma_f32 v[84:85], v[58:59], s[36:37], v[232:233] op_sel_hi:[1,0,1]
	v_pk_fma_f32 v[88:89], v[176:177], s[36:37], v[228:229] op_sel_hi:[1,0,1]
	v_pk_fma_f32 v[56:57], v[180:181], s[36:37], v[194:195] op_sel_hi:[1,0,1]
	v_pk_fma_f32 v[62:63], v[178:179], s[36:37], v[192:193] op_sel_hi:[1,0,1]
	v_pk_fma_f32 v[66:67], v[54:55], s[36:37], v[140:141] op_sel_hi:[1,0,1]
	v_pk_fma_f32 v[70:71], v[182:183], s[36:37], v[200:201] op_sel_hi:[1,0,1]
	v_pk_fma_f32 v[54:55], v[186:187], s[36:37], v[150:151] op_sel_hi:[1,0,1]
	v_pk_fma_f32 v[58:59], v[184:185], s[36:37], v[142:143] op_sel_hi:[1,0,1]
	v_pk_fma_f32 v[64:65], v[190:191], s[36:37], v[204:205] op_sel_hi:[1,0,1]
	v_pk_fma_f32 v[68:69], v[188:189], s[36:37], v[202:203] op_sel_hi:[1,0,1]
	v_mov_b32_e32 v136, v116
	v_mov_b32_e32 v137, v114
	v_mov_b32_e32 v138, v117
	v_mov_b32_e32 v139, v115
	v_mov_b32_e32 v140, v112
	v_mov_b32_e32 v141, v110
	v_mov_b32_e32 v142, v113
	v_mov_b32_e32 v143, v111
	v_mov_b32_e32 v144, v124
	v_mov_b32_e32 v145, v122
	v_mov_b32_e32 v146, v125
	v_mov_b32_e32 v147, v123
	v_mov_b32_e32 v148, v120
	v_mov_b32_e32 v149, v118
	v_mov_b32_e32 v150, v121
	v_mov_b32_e32 v151, v119
	v_mov_b32_e32 v152, v100
	v_mov_b32_e32 v153, v98
	v_mov_b32_e32 v154, v101
	v_mov_b32_e32 v155, v99
	v_mov_b32_e32 v156, v94
	v_mov_b32_e32 v157, v92
	v_mov_b32_e32 v158, v95
	v_mov_b32_e32 v159, v93
	v_mov_b32_e32 v160, v108
	v_mov_b32_e32 v161, v106
	v_mov_b32_e32 v162, v109
	v_mov_b32_e32 v163, v107
	v_mov_b32_e32 v164, v104
	v_mov_b32_e32 v165, v102
	v_mov_b32_e32 v166, v105
	v_mov_b32_e32 v167, v103
	v_mov_b32_e32 v168, v78
	v_mov_b32_e32 v169, v76
	v_mov_b32_e32 v170, v79
	v_mov_b32_e32 v171, v77
	v_mov_b32_e32 v172, v74
	v_mov_b32_e32 v173, v72
	v_mov_b32_e32 v174, v75
	v_mov_b32_e32 v175, v73
	v_mov_b32_e32 v176, v90
	v_mov_b32_e32 v177, v88
	v_mov_b32_e32 v178, v91
	v_mov_b32_e32 v179, v89
	v_mov_b32_e32 v180, v86
	v_mov_b32_e32 v181, v84
	v_mov_b32_e32 v182, v87
	v_mov_b32_e32 v183, v85
	v_mov_b32_e32 v184, v62
	v_mov_b32_e32 v185, v58
	v_mov_b32_e32 v186, v63
	v_mov_b32_e32 v187, v59
	v_mov_b32_e32 v188, v56
	v_mov_b32_e32 v189, v54
	v_mov_b32_e32 v190, v57
	v_mov_b32_e32 v191, v55
	v_mov_b32_e32 v192, v70
	v_mov_b32_e32 v193, v68
	v_mov_b32_e32 v194, v71
	v_mov_b32_e32 v195, v69
	v_mov_b32_e32 v196, v66
	v_mov_b32_e32 v197, v64
	v_mov_b32_e32 v198, v67
	v_mov_b32_e32 v199, v65
	v_pk_add_f32 v[136:137], v[136:137], v[138:139]
	v_pk_add_f32 v[138:139], v[140:141], v[142:143]
	v_pk_add_f32 v[140:141], v[144:145], v[146:147]
	v_pk_add_f32 v[142:143], v[148:149], v[150:151]
	v_pk_add_f32 v[144:145], v[152:153], v[154:155]
	v_pk_add_f32 v[146:147], v[156:157], v[158:159]
	v_pk_add_f32 v[148:149], v[160:161], v[162:163]
	v_pk_add_f32 v[150:151], v[164:165], v[166:167]
	v_pk_add_f32 v[152:153], v[168:169], v[170:171]
	v_pk_add_f32 v[154:155], v[172:173], v[174:175]
	v_pk_add_f32 v[156:157], v[176:177], v[178:179]
	v_pk_add_f32 v[158:159], v[180:181], v[182:183]
	v_pk_add_f32 v[160:161], v[184:185], v[186:187]
	v_pk_add_f32 v[162:163], v[188:189], v[190:191]
	v_pk_add_f32 v[164:165], v[192:193], v[194:195]
	v_pk_add_f32 v[166:167], v[196:197], v[198:199]
	v_pk_add_f32 v[136:137], v[136:137], v[138:139]
	v_pk_add_f32 v[138:139], v[140:141], v[142:143]
	v_pk_add_f32 v[140:141], v[144:145], v[146:147]
	v_pk_add_f32 v[142:143], v[148:149], v[150:151]
	v_pk_add_f32 v[144:145], v[152:153], v[154:155]
	v_pk_add_f32 v[146:147], v[156:157], v[158:159]
	v_pk_add_f32 v[148:149], v[160:161], v[162:163]
	v_pk_add_f32 v[150:151], v[164:165], v[166:167]
	v_pk_add_f32 v[136:137], v[136:137], v[138:139]
	v_pk_add_f32 v[138:139], v[140:141], v[142:143]
	v_pk_add_f32 v[140:141], v[144:145], v[146:147]
	v_pk_add_f32 v[142:143], v[148:149], v[150:151]
	v_add_f32_e32 v135, 0, v136
	v_add_f32_e32 v136, 0, v138
	v_add_f32_e32 v138, 0, v140
	v_add_f32_e32 v140, 0, v142
	v_add_f32_e32 v135, v135, v137
	v_add_f32_e32 v136, v136, v139
	v_add_f32_e32 v137, v138, v141
	v_add_f32_e32 v138, v140, v143
	ds_bpermute_b32 v139, v127, v135
	ds_bpermute_b32 v140, v127, v136
	ds_bpermute_b32 v141, v127, v137
	ds_bpermute_b32 v142, v127, v138
	s_waitcnt lgkmcnt(3)
	v_add_f32_e32 v135, v135, v139
	s_waitcnt lgkmcnt(2)
	v_add_f32_e32 v136, v136, v140
	s_waitcnt lgkmcnt(1)
	v_add_f32_e32 v137, v137, v141
	s_waitcnt lgkmcnt(0)
	v_add_f32_e32 v138, v138, v142
	ds_bpermute_b32 v139, v128, v135
	ds_bpermute_b32 v140, v128, v136
	ds_bpermute_b32 v141, v128, v137
	ds_bpermute_b32 v142, v128, v138
	s_waitcnt lgkmcnt(3)
	v_add_f32_e32 v135, v135, v139
	s_waitcnt lgkmcnt(2)
	v_add_f32_e32 v136, v136, v140
	s_waitcnt lgkmcnt(1)
	v_add_f32_e32 v137, v137, v141
	s_waitcnt lgkmcnt(0)
	v_add_f32_e32 v138, v138, v142
	ds_bpermute_b32 v139, v129, v135
	ds_bpermute_b32 v140, v129, v136
	ds_bpermute_b32 v141, v129, v137
	ds_bpermute_b32 v142, v129, v138
	s_waitcnt lgkmcnt(3)
	v_add_f32_e32 v135, v135, v139
	s_waitcnt lgkmcnt(2)
	v_add_f32_e32 v136, v136, v140
	s_waitcnt lgkmcnt(1)
	v_add_f32_e32 v137, v137, v141
	s_waitcnt lgkmcnt(0)
	v_add_f32_e32 v138, v138, v142
	ds_bpermute_b32 v139, v130, v135
	ds_bpermute_b32 v140, v130, v136
	ds_bpermute_b32 v141, v130, v137
	ds_bpermute_b32 v142, v130, v138
	s_waitcnt lgkmcnt(3)
	v_add_f32_e32 v135, v135, v139
	s_waitcnt lgkmcnt(2)
	v_add_f32_e32 v136, v136, v140
	s_waitcnt lgkmcnt(1)
	v_add_f32_e32 v137, v137, v141
	s_waitcnt lgkmcnt(0)
	v_add_f32_e32 v138, v138, v142
	ds_bpermute_b32 v139, v131, v135
	ds_bpermute_b32 v140, v131, v136
	ds_bpermute_b32 v141, v131, v137
	ds_bpermute_b32 v142, v131, v138
	s_waitcnt lgkmcnt(3)
	v_add_f32_e32 v135, v135, v139
	s_waitcnt lgkmcnt(2)
	v_add_f32_e32 v136, v136, v140
	s_waitcnt lgkmcnt(1)
	v_add_f32_e32 v137, v137, v141
	s_waitcnt lgkmcnt(0)
	v_add_f32_e32 v138, v138, v142
	ds_bpermute_b32 v139, v132, v135
	ds_bpermute_b32 v140, v132, v136
	ds_bpermute_b32 v141, v132, v137
	ds_bpermute_b32 v142, v132, v138
	s_waitcnt lgkmcnt(3)
	v_add_f32_e32 v135, v135, v139
	s_waitcnt lgkmcnt(2)
	v_add_f32_e32 v136, v136, v140
	s_waitcnt lgkmcnt(1)
	v_add_f32_e32 v137, v137, v141
	s_waitcnt lgkmcnt(0)
	v_add_f32_e32 v138, v138, v142
	v_fmamk_f32 v117, v135, 0xba800000, v117
	v_fmac_f32_e32 v116, 0xba800000, v135
	v_fmamk_f32 v113, v135, 0xba800000, v113
	v_fmac_f32_e32 v112, 0xba800000, v135
	v_fmamk_f32 v125, v135, 0xba800000, v125
	v_fmac_f32_e32 v124, 0xba800000, v135
	v_fmamk_f32 v121, v135, 0xba800000, v121
	v_fmac_f32_e32 v120, 0xba800000, v135
	v_fmac_f32_e32 v114, 0xba800000, v135
	v_fmac_f32_e32 v110, 0xba800000, v135
	v_fmamk_f32 v101, v136, 0xba800000, v101
	v_fmac_f32_e32 v100, 0xba800000, v136
	v_fmamk_f32 v95, v136, 0xba800000, v95
	v_fmac_f32_e32 v94, 0xba800000, v136
	v_fmamk_f32 v109, v136, 0xba800000, v109
	v_fmac_f32_e32 v108, 0xba800000, v136
	v_fmamk_f32 v105, v136, 0xba800000, v105
	v_fmac_f32_e32 v104, 0xba800000, v136
	v_fmamk_f32 v99, v136, 0xba800000, v99
	v_fmac_f32_e32 v98, 0xba800000, v136
	v_fmamk_f32 v93, v136, 0xba800000, v93
	v_fmac_f32_e32 v92, 0xba800000, v136
	v_fmamk_f32 v103, v136, 0xba800000, v103
	v_fmac_f32_e32 v102, 0xba800000, v136
	v_fmamk_f32 v107, v136, 0xba800000, v107
	v_fmac_f32_e32 v106, 0xba800000, v136
	v_fmamk_f32 v79, v137, 0xba800000, v79
	v_fmac_f32_e32 v78, 0xba800000, v137
	v_fmamk_f32 v75, v137, 0xba800000, v75
	v_fmac_f32_e32 v74, 0xba800000, v137
	v_fmamk_f32 v91, v137, 0xba800000, v91
	v_fmac_f32_e32 v90, 0xba800000, v137
	v_fmamk_f32 v87, v137, 0xba800000, v87
	v_fmac_f32_e32 v86, 0xba800000, v137
	v_fmamk_f32 v77, v137, 0xba800000, v77
	v_fmac_f32_e32 v76, 0xba800000, v137
	v_fmamk_f32 v73, v137, 0xba800000, v73
	v_fmac_f32_e32 v72, 0xba800000, v137
	v_fmamk_f32 v85, v137, 0xba800000, v85
	v_fmac_f32_e32 v84, 0xba800000, v137
	v_fmamk_f32 v89, v137, 0xba800000, v89
	v_fmac_f32_e32 v88, 0xba800000, v137
	v_fmamk_f32 v63, v138, 0xba800000, v63
	v_fmac_f32_e32 v62, 0xba800000, v138
	v_fmamk_f32 v57, v138, 0xba800000, v57
	v_fmac_f32_e32 v56, 0xba800000, v138
	v_fmamk_f32 v71, v138, 0xba800000, v71
	v_fmac_f32_e32 v70, 0xba800000, v138
	v_fmamk_f32 v67, v138, 0xba800000, v67
	v_fmac_f32_e32 v66, 0xba800000, v138
	v_fmamk_f32 v59, v138, 0xba800000, v59
	v_fmac_f32_e32 v58, 0xba800000, v138
	v_fmamk_f32 v55, v138, 0xba800000, v55
	v_fmac_f32_e32 v54, 0xba800000, v138
	v_fmamk_f32 v65, v138, 0xba800000, v65
	v_fmac_f32_e32 v64, 0xba800000, v138
	v_fmamk_f32 v69, v138, 0xba800000, v69
	v_fmac_f32_e32 v68, 0xba800000, v138
	v_pk_mul_f32 v[136:137], v[112:113], v[112:113]
	v_pk_mul_f32 v[138:139], v[116:117], v[116:117]
	v_pk_mul_f32 v[140:141], v[120:121], v[120:121]
	v_pk_mul_f32 v[142:143], v[124:125], v[124:125]
	v_fmamk_f32 v115, v135, 0xba800000, v115
	v_fmamk_f32 v111, v135, 0xba800000, v111
	v_mul_f32_e32 v144, v114, v114
	v_mul_f32_e32 v146, v110, v110
	v_pk_mul_f32 v[148:149], v[94:95], v[94:95]
	v_pk_mul_f32 v[150:151], v[100:101], v[100:101]
	v_pk_mul_f32 v[152:153], v[104:105], v[104:105]
	v_pk_mul_f32 v[154:155], v[108:109], v[108:109]
	v_mul_f32_e32 v156, v98, v98
	v_mul_f32_e32 v158, v92, v92
	v_pk_mul_f32 v[160:161], v[74:75], v[74:75]
	v_pk_mul_f32 v[162:163], v[78:79], v[78:79]
	v_pk_mul_f32 v[164:165], v[86:87], v[86:87]
	v_pk_mul_f32 v[166:167], v[90:91], v[90:91]
	v_pk_mov_b32 v[184:185], v[138:139], v[136:137] op_sel:[1,0]
	v_mov_b32_e32 v139, v137
	v_pk_mov_b32 v[136:137], v[142:143], v[140:141] op_sel:[1,0]
	v_mov_b32_e32 v143, v141
	v_fmamk_f32 v123, v135, 0xba800000, v123
	v_fmac_f32_e32 v122, 0xba800000, v135
	v_mul_f32_e32 v168, v76, v76
	v_mul_f32_e32 v170, v72, v72
	v_pk_mul_f32 v[172:173], v[56:57], v[56:57]
	v_pk_mul_f32 v[174:175], v[62:63], v[62:63]
	v_pk_mul_f32 v[176:177], v[66:67], v[66:67]
	v_pk_mul_f32 v[178:179], v[70:71], v[70:71]
	v_pk_fma_f32 v[140:141], v[114:115], v[114:115], v[144:145] op_sel_hi:[1,1,0]
	v_pk_fma_f32 v[144:145], v[110:111], v[110:111], v[146:147] op_sel_hi:[1,1,0]
	v_pk_mov_b32 v[146:147], v[150:151], v[148:149] op_sel:[1,0]
	v_mov_b32_e32 v151, v149
	v_pk_mov_b32 v[148:149], v[154:155], v[152:153] op_sel:[1,0]
	v_mov_b32_e32 v155, v153
	v_pk_fma_f32 v[152:153], v[98:99], v[98:99], v[156:157] op_sel_hi:[1,1,0]
	v_pk_fma_f32 v[156:157], v[92:93], v[92:93], v[158:159] op_sel_hi:[1,1,0]
	v_pk_mov_b32 v[158:159], v[162:163], v[160:161] op_sel:[1,0]
	v_mov_b32_e32 v163, v161
	v_pk_mov_b32 v[160:161], v[166:167], v[164:165] op_sel:[1,0]
	v_mov_b32_e32 v167, v165
	v_pk_add_f32 v[138:139], v[184:185], v[138:139]
	v_pk_add_f32 v[136:137], v[136:137], v[142:143]
	v_fmamk_f32 v119, v135, 0xba800000, v119
	v_fmac_f32_e32 v118, 0xba800000, v135
	v_pk_fma_f32 v[164:165], v[76:77], v[76:77], v[168:169] op_sel_hi:[1,1,0]
	v_pk_fma_f32 v[168:169], v[72:73], v[72:73], v[170:171] op_sel_hi:[1,1,0]
	v_pk_mov_b32 v[170:171], v[174:175], v[172:173] op_sel:[1,0]
	v_mov_b32_e32 v175, v173
	v_pk_mov_b32 v[172:173], v[178:179], v[176:177] op_sel:[1,0]
	v_mov_b32_e32 v179, v177
	v_mul_f32_e32 v140, v122, v122
	v_mul_f32_e32 v144, v123, v123
	v_pk_add_f32 v[142:143], v[146:147], v[150:151]
	v_pk_add_f32 v[146:147], v[148:149], v[154:155]
	v_pk_add_f32 v[148:149], v[158:159], v[162:163]
	v_pk_add_f32 v[150:151], v[160:161], v[166:167]
	v_pk_add_f32 v[138:139], v[138:139], v[138:139] op_sel_hi:[0,1]
	v_pk_add_f32 v[136:137], v[136:137], v[136:137] op_sel_hi:[0,1]
	v_mul_f32_e32 v180, v58, v58
	v_mul_f32_e32 v182, v54, v54
	v_mul_f32_e32 v152, v106, v106
	v_mul_f32_e32 v156, v107, v107
	v_pk_add_f32 v[154:155], v[170:171], v[174:175]
	v_pk_add_f32 v[158:159], v[172:173], v[178:179]
	v_pk_add_f32 v[140:141], v[140:141], v[144:145]
	v_pk_add_f32 v[142:143], v[142:143], v[142:143] op_sel_hi:[0,1]
	v_pk_add_f32 v[144:145], v[146:147], v[146:147] op_sel_hi:[0,1]
	v_pk_add_f32 v[148:149], v[148:149], v[148:149] op_sel_hi:[0,1]
	v_pk_add_f32 v[150:151], v[150:151], v[150:151] op_sel_hi:[0,1]
	v_mul_f32_e32 v138, v118, v118
	v_mul_f32_e32 v136, v119, v119
	v_pk_fma_f32 v[176:177], v[58:59], v[58:59], v[180:181] op_sel_hi:[1,1,0]
	v_pk_fma_f32 v[180:181], v[54:55], v[54:55], v[182:183] op_sel_hi:[1,1,0]
	v_mul_f32_e32 v164, v88, v88
	v_mul_f32_e32 v168, v89, v89
	v_pk_add_f32 v[146:147], v[152:153], v[156:157]
	v_pk_add_f32 v[154:155], v[154:155], v[154:155] op_sel_hi:[0,1]
	v_pk_add_f32 v[156:157], v[158:159], v[158:159] op_sel_hi:[0,1]
	v_mul_f32_e32 v142, v102, v102
	v_mul_f32_e32 v144, v103, v103
	v_mul_f32_e32 v148, v84, v84
	v_mul_f32_e32 v150, v85, v85
	v_pk_add_f32 v[136:137], v[138:139], v[136:137]
	v_mul_f32_e32 v176, v68, v68
	v_mul_f32_e32 v180, v69, v69
	v_pk_add_f32 v[152:153], v[164:165], v[168:169]
	v_mul_f32_e32 v154, v64, v64
	v_mul_f32_e32 v156, v65, v65
	v_pk_add_f32 v[138:139], v[142:143], v[144:145]
	v_pk_add_f32 v[142:143], v[148:149], v[150:151]
	v_pk_add_f32 v[136:137], v[140:141], v[136:137]
	v_pk_add_f32 v[158:159], v[176:177], v[180:181]
	v_pk_add_f32 v[144:145], v[154:155], v[156:157]
	v_pk_add_f32 v[138:139], v[146:147], v[138:139]
	v_pk_add_f32 v[140:141], v[152:153], v[142:143]
	v_add_f32_e32 v135, v136, v137
	v_pk_add_f32 v[142:143], v[158:159], v[144:145]
	v_add_f32_e32 v136, v138, v139
	v_add_f32_e32 v137, v140, v141
	ds_bpermute_b32 v139, v127, v135
	v_add_f32_e32 v138, v142, v143
	ds_bpermute_b32 v140, v127, v136
	ds_bpermute_b32 v141, v127, v137
	ds_bpermute_b32 v142, v127, v138
	s_waitcnt lgkmcnt(3)
	v_add_f32_e32 v135, v135, v139
	ds_bpermute_b32 v139, v128, v135
	s_waitcnt lgkmcnt(3)
	v_add_f32_e32 v136, v136, v140
	s_waitcnt lgkmcnt(2)
	v_add_f32_e32 v137, v137, v141
	s_waitcnt lgkmcnt(1)
	v_add_f32_e32 v138, v138, v142
	ds_bpermute_b32 v140, v128, v136
	ds_bpermute_b32 v141, v128, v137
	ds_bpermute_b32 v142, v128, v138
	s_waitcnt lgkmcnt(3)
	v_add_f32_e32 v135, v135, v139
	ds_bpermute_b32 v139, v129, v135
	s_waitcnt lgkmcnt(3)
	v_add_f32_e32 v136, v136, v140
	s_waitcnt lgkmcnt(2)
	v_add_f32_e32 v137, v137, v141
	s_waitcnt lgkmcnt(1)
	v_add_f32_e32 v138, v138, v142
	ds_bpermute_b32 v140, v129, v136
	ds_bpermute_b32 v141, v129, v137
	ds_bpermute_b32 v142, v129, v138
	s_waitcnt lgkmcnt(3)
	v_add_f32_e32 v135, v135, v139
	ds_bpermute_b32 v139, v130, v135
	s_waitcnt lgkmcnt(3)
	v_add_f32_e32 v136, v136, v140
	s_waitcnt lgkmcnt(2)
	v_add_f32_e32 v137, v137, v141
	s_waitcnt lgkmcnt(1)
	v_add_f32_e32 v138, v138, v142
	ds_bpermute_b32 v140, v130, v136
	ds_bpermute_b32 v141, v130, v137
	ds_bpermute_b32 v142, v130, v138
	s_waitcnt lgkmcnt(3)
	v_add_f32_e32 v135, v135, v139
	ds_bpermute_b32 v139, v131, v135
	s_waitcnt lgkmcnt(3)
	v_add_f32_e32 v136, v136, v140
	s_waitcnt lgkmcnt(2)
	v_add_f32_e32 v137, v137, v141
	s_waitcnt lgkmcnt(1)
	v_add_f32_e32 v138, v138, v142
	ds_bpermute_b32 v140, v131, v136
	ds_bpermute_b32 v141, v131, v137
	ds_bpermute_b32 v142, v131, v138
	s_waitcnt lgkmcnt(3)
	v_add_f32_e32 v135, v135, v139
	ds_bpermute_b32 v139, v132, v135
	s_waitcnt lgkmcnt(3)
	v_add_f32_e32 v136, v136, v140
	s_waitcnt lgkmcnt(2)
	v_add_f32_e32 v137, v137, v141
	s_waitcnt lgkmcnt(1)
	v_add_f32_e32 v138, v138, v142
	ds_bpermute_b32 v140, v132, v136
	ds_bpermute_b32 v141, v132, v137
	ds_bpermute_b32 v142, v132, v138
	s_waitcnt lgkmcnt(3)
	v_add_f32_e32 v135, v135, v139
	v_fmamk_f32 v135, v135, 0x3a800000, v133
	s_waitcnt lgkmcnt(2)
	v_add_f32_e32 v136, v136, v140
	s_waitcnt lgkmcnt(1)
	v_add_f32_e32 v137, v137, v141
	s_waitcnt lgkmcnt(0)
	v_add_f32_e32 v138, v138, v142
	v_fmamk_f32 v136, v136, 0x3a800000, v133
	v_fmamk_f32 v137, v137, 0x3a800000, v133
	v_mul_f32_e32 v139, 0x4f800000, v135
	v_cmp_gt_f32_e64 s[8:9], s21, v135
	v_fmamk_f32 v138, v138, 0x3a800000, v133
	v_mul_f32_e32 v140, 0x4f800000, v136
	v_cmp_gt_f32_e32 vcc, s21, v136
	v_mul_f32_e32 v141, 0x4f800000, v137
	v_cmp_gt_f32_e64 s[0:1], s21, v137
	v_cndmask_b32_e64 v135, v135, v139, s[8:9]
	v_mul_f32_e32 v142, 0x4f800000, v138
	v_cmp_gt_f32_e64 s[6:7], s21, v138
	v_cndmask_b32_e32 v136, v136, v140, vcc
	v_cndmask_b32_e64 v137, v137, v141, s[0:1]
	v_sqrt_f32_e32 v139, v135
	v_cndmask_b32_e64 v138, v138, v142, s[6:7]
	v_sqrt_f32_e32 v140, v136
	v_sqrt_f32_e32 v141, v137
	v_sqrt_f32_e32 v142, v138
	v_add_u32_e32 v143, -1, v139
	v_add_u32_e32 v144, 1, v139
	v_add_u32_e32 v145, -1, v140
	v_add_u32_e32 v147, -1, v141
	v_fma_f32 v151, -v143, v139, v135
	v_add_u32_e32 v146, 1, v140
	v_add_u32_e32 v148, 1, v141
	v_add_u32_e32 v149, -1, v142
	v_fma_f32 v152, -v144, v139, v135
	v_fma_f32 v153, -v145, v140, v136
	v_fma_f32 v155, -v147, v141, v137
	v_cmp_ge_f32_e64 s[10:11], 0, v151
	v_add_u32_e32 v150, 1, v142
	v_fma_f32 v154, -v146, v140, v136
	v_fma_f32 v156, -v148, v141, v137
	v_fma_f32 v157, -v149, v142, v138
	v_cndmask_b32_e64 v139, v139, v143, s[10:11]
	v_cmp_ge_f32_e64 s[10:11], 0, v153
	v_cmp_ge_f32_e64 s[12:13], 0, v155
	v_cmp_lt_f32_e64 s[16:17], 0, v152
	v_fma_f32 v158, -v150, v142, v138
	v_cndmask_b32_e64 v140, v140, v145, s[10:11]
	v_cmp_lt_f32_e64 s[10:11], 0, v154
	v_cndmask_b32_e64 v141, v141, v147, s[12:13]
	v_cmp_lt_f32_e64 s[12:13], 0, v156
	v_cmp_ge_f32_e64 s[14:15], 0, v157
	v_cndmask_b32_e64 v139, v139, v144, s[16:17]
	v_cndmask_b32_e64 v140, v140, v146, s[10:11]
	v_cndmask_b32_e64 v142, v142, v149, s[14:15]
	v_cmp_lt_f32_e64 s[14:15], 0, v158
	v_cndmask_b32_e64 v141, v141, v148, s[12:13]
	v_mul_f32_e32 v143, 0x37800000, v139
	v_cndmask_b32_e64 v142, v142, v150, s[14:15]
	v_mul_f32_e32 v144, 0x37800000, v140
	v_mul_f32_e32 v145, 0x37800000, v141
	v_cndmask_b32_e64 v139, v139, v143, s[8:9]
	v_cmp_class_f32_e64 s[8:9], v135, v134
	v_mul_f32_e32 v146, 0x37800000, v142
	v_cndmask_b32_e32 v140, v140, v144, vcc
	v_cmp_class_f32_e32 vcc, v136, v134
	v_cndmask_b32_e64 v141, v141, v145, s[0:1]
	v_cmp_class_f32_e64 s[0:1], v137, v134
	v_cndmask_b32_e64 v135, v139, v135, s[8:9]
	v_cndmask_b32_e64 v142, v142, v146, s[6:7]
	v_cmp_class_f32_e64 s[6:7], v138, v134
	v_cndmask_b32_e32 v139, v140, v136, vcc
	v_cndmask_b32_e64 v140, v141, v137, s[0:1]
	v_div_scale_f32 v136, s[0:1], v135, v135, 1.0
	v_cndmask_b32_e64 v141, v142, v138, s[6:7]
	v_div_scale_f32 v138, s[0:1], v139, v139, 1.0
	v_rcp_f32_e32 v147, v136
	v_div_scale_f32 v143, s[6:7], v140, v140, 1.0
	v_rcp_f32_e32 v148, v138
	v_div_scale_f32 v145, s[8:9], v141, v141, 1.0
	v_rcp_f32_e32 v149, v143
	v_rcp_f32_e32 v150, v145
	v_fma_f32 v151, -v136, v147, 1.0
	v_div_scale_f32 v137, vcc, 1.0, v135, 1.0
	v_fma_f32 v152, -v138, v148, 1.0
	v_fmac_f32_e32 v147, v151, v147
	v_div_scale_f32 v142, s[0:1], 1.0, v139, 1.0
	v_fma_f32 v153, -v143, v149, 1.0
	v_fmac_f32_e32 v148, v152, v148
	v_mul_f32_e32 v151, v137, v147
	v_div_scale_f32 v144, s[6:7], 1.0, v140, 1.0
	v_fma_f32 v154, -v145, v150, 1.0
	v_fmac_f32_e32 v149, v153, v149
	v_mul_f32_e32 v152, v142, v148
	v_fma_f32 v155, -v136, v151, v137
	v_div_scale_f32 v146, s[8:9], 1.0, v141, 1.0
	v_fmac_f32_e32 v150, v154, v150
	v_mul_f32_e32 v153, v144, v149
	v_fma_f32 v156, -v138, v152, v142
	v_fmac_f32_e32 v151, v155, v147
	v_mul_f32_e32 v154, v146, v150
	v_fma_f32 v157, -v143, v153, v144
	v_fmac_f32_e32 v152, v156, v148
	v_fma_f32 v136, -v136, v151, v137
	v_fma_f32 v158, -v145, v154, v146
	v_fmac_f32_e32 v153, v157, v149
	v_fma_f32 v137, -v138, v152, v142
	v_div_fmas_f32 v136, v136, v147, v151
	s_mov_b64 vcc, s[0:1]
	v_fmac_f32_e32 v154, v158, v150
	v_fma_f32 v138, -v143, v153, v144
	v_div_fixup_f32 v136, v136, v135, 1.0
	v_div_fmas_f32 v135, v137, v148, v152
	s_mov_b64 vcc, s[6:7]
	v_fma_f32 v142, -v145, v154, v146
	v_pk_mul_f32 v[124:125], v[124:125], v[136:137] op_sel_hi:[1,0]
	v_pk_mul_f32 v[120:121], v[120:121], v[136:137] op_sel_hi:[1,0]
	v_pk_mul_f32 v[116:117], v[116:117], v[136:137] op_sel_hi:[1,0]
	v_pk_mul_f32 v[112:113], v[112:113], v[136:137] op_sel_hi:[1,0]
	v_pk_mul_f32 v[122:123], v[122:123], v[136:137] op_sel_hi:[1,0]
	v_pk_mul_f32 v[118:119], v[118:119], v[136:137] op_sel_hi:[1,0]
	v_pk_mul_f32 v[114:115], v[114:115], v[136:137] op_sel_hi:[1,0]
	v_pk_mul_f32 v[110:111], v[110:111], v[136:137] op_sel_hi:[1,0]
	v_div_fixup_f32 v136, v135, v139, 1.0
	v_div_fmas_f32 v135, v138, v149, v153
	s_mov_b64 vcc, s[8:9]
	v_pk_fma_f32 v[116:117], v[4:5], v[116:117], v[12:13]
	v_pk_mul_f32 v[108:109], v[108:109], v[136:137] op_sel_hi:[1,0]
	v_pk_mul_f32 v[104:105], v[104:105], v[136:137] op_sel_hi:[1,0]
	v_pk_mul_f32 v[100:101], v[100:101], v[136:137] op_sel_hi:[1,0]
	v_pk_mul_f32 v[138:139], v[94:95], v[136:137] op_sel_hi:[1,0]
	v_pk_mul_f32 v[106:107], v[106:107], v[136:137] op_sel_hi:[1,0]
	v_pk_mul_f32 v[102:103], v[102:103], v[136:137] op_sel_hi:[1,0]
	v_pk_mul_f32 v[98:99], v[98:99], v[136:137] op_sel_hi:[1,0]
	v_pk_mul_f32 v[136:137], v[92:93], v[136:137] op_sel_hi:[1,0]
	v_div_fixup_f32 v140, v135, v140, 1.0
	v_div_fmas_f32 v135, v142, v150, v154
	v_pk_fma_f32 v[120:121], v[2:3], v[120:121], v[10:11]
	v_pk_fma_f32 v[124:125], v[0:1], v[124:125], v[8:9]
	v_pk_fma_f32 v[112:113], v[6:7], v[112:113], v[14:15]
	v_pk_fma_f32 v[110:111], v[22:23], v[110:111], v[30:31]
	v_pk_fma_f32 v[114:115], v[20:21], v[114:115], v[28:29]
	v_cvt_pk_bf16_f32 v92, v116, v117
	v_pk_fma_f32 v[116:117], v[22:23], v[136:137], v[30:31]
	v_div_fixup_f32 v136, v135, v141, 1.0
	v_pk_fma_f32 v[118:119], v[18:19], v[118:119], v[26:27]
	v_pk_fma_f32 v[122:123], v[16:17], v[122:123], v[24:25]
	v_cvt_pk_bf16_f32 v93, v112, v113
	v_cvt_pk_bf16_f32 v94, v124, v125
	v_cvt_pk_bf16_f32 v95, v120, v121
	v_pk_fma_f32 v[104:105], v[2:3], v[104:105], v[10:11]
	v_pk_fma_f32 v[108:109], v[0:1], v[108:109], v[8:9]
	v_pk_fma_f32 v[112:113], v[6:7], v[138:139], v[14:15]
	v_pk_fma_f32 v[100:101], v[4:5], v[100:101], v[12:13]
	v_pk_mul_f32 v[120:121], v[74:75], v[140:141] op_sel_hi:[1,0]
	v_pk_mul_f32 v[124:125], v[72:73], v[140:141] op_sel_hi:[1,0]
	global_store_dwordx4 v[96:97], v[92:95], off offset:-3072 sc1
	v_cvt_pk_bf16_f32 v72, v114, v115
	v_cvt_pk_bf16_f32 v73, v110, v111
	v_cvt_pk_bf16_f32 v74, v122, v123
	v_cvt_pk_bf16_f32 v75, v118, v119
	v_pk_mul_f32 v[110:111], v[56:57], v[136:137] op_sel_hi:[1,0]
	v_pk_mul_f32 v[114:115], v[54:55], v[136:137] op_sel_hi:[1,0]
	global_store_dwordx4 v[96:97], v[72:75], off offset:-2048 sc1
	v_cvt_pk_bf16_f32 v54, v100, v101
	v_cvt_pk_bf16_f32 v55, v112, v113
	v_cvt_pk_bf16_f32 v56, v108, v109
	v_cvt_pk_bf16_f32 v57, v104, v105
	v_pk_fma_f32 v[102:103], v[18:19], v[102:103], v[26:27]
	v_pk_fma_f32 v[106:107], v[16:17], v[106:107], v[24:25]
	v_pk_fma_f32 v[98:99], v[20:21], v[98:99], v[28:29]
	v_pk_mul_f32 v[90:91], v[90:91], v[140:141] op_sel_hi:[1,0]
	v_pk_mul_f32 v[86:87], v[86:87], v[140:141] op_sel_hi:[1,0]
	v_pk_mul_f32 v[78:79], v[78:79], v[140:141] op_sel_hi:[1,0]
	global_store_dwordx4 v[96:97], v[54:57], off offset:-1024 sc1
	v_pk_mul_f32 v[88:89], v[88:89], v[140:141] op_sel_hi:[1,0]
	v_pk_mul_f32 v[84:85], v[84:85], v[140:141] op_sel_hi:[1,0]
	v_cvt_pk_bf16_f32 v54, v98, v99
	v_cvt_pk_bf16_f32 v55, v116, v117
	v_cvt_pk_bf16_f32 v56, v106, v107
	v_cvt_pk_bf16_f32 v57, v102, v103
	v_pk_mul_f32 v[76:77], v[76:77], v[140:141] op_sel_hi:[1,0]
	v_pk_fma_f32 v[86:87], v[2:3], v[86:87], v[10:11]
	v_pk_fma_f32 v[90:91], v[0:1], v[90:91], v[8:9]
	v_pk_fma_f32 v[92:93], v[6:7], v[120:121], v[14:15]
	v_pk_fma_f32 v[78:79], v[4:5], v[78:79], v[12:13]
	global_store_dwordx4 v[82:83], v[54:57], off offset:-4096 sc1
	v_pk_fma_f32 v[84:85], v[18:19], v[84:85], v[26:27]
	v_pk_fma_f32 v[88:89], v[16:17], v[88:89], v[24:25]
	v_cvt_pk_bf16_f32 v54, v78, v79
	v_cvt_pk_bf16_f32 v55, v92, v93
	v_cvt_pk_bf16_f32 v56, v90, v91
	v_cvt_pk_bf16_f32 v57, v86, v87
	v_pk_fma_f32 v[94:95], v[22:23], v[124:125], v[30:31]
	v_pk_fma_f32 v[76:77], v[20:21], v[76:77], v[28:29]
	v_pk_mul_f32 v[70:71], v[70:71], v[136:137] op_sel_hi:[1,0]
	v_pk_mul_f32 v[66:67], v[66:67], v[136:137] op_sel_hi:[1,0]
	v_pk_mul_f32 v[62:63], v[62:63], v[136:137] op_sel_hi:[1,0]
	global_store_dwordx4 v[82:83], v[54:57], off offset:-3072 sc1
	v_pk_mul_f32 v[68:69], v[68:69], v[136:137] op_sel_hi:[1,0]
	v_pk_mul_f32 v[64:65], v[64:65], v[136:137] op_sel_hi:[1,0]
	v_cvt_pk_bf16_f32 v54, v76, v77
	v_cvt_pk_bf16_f32 v55, v94, v95
	v_cvt_pk_bf16_f32 v56, v88, v89
	v_cvt_pk_bf16_f32 v57, v84, v85
	v_pk_mul_f32 v[58:59], v[58:59], v[136:137] op_sel_hi:[1,0]
	v_pk_fma_f32 v[66:67], v[2:3], v[66:67], v[10:11]
	v_pk_fma_f32 v[70:71], v[0:1], v[70:71], v[8:9]
	v_pk_fma_f32 v[72:73], v[6:7], v[110:111], v[14:15]
	v_pk_fma_f32 v[62:63], v[4:5], v[62:63], v[12:13]
	global_store_dwordx4 v[82:83], v[54:57], off offset:-2048 sc1
	v_pk_fma_f32 v[64:65], v[18:19], v[64:65], v[26:27]
	v_pk_fma_f32 v[68:69], v[16:17], v[68:69], v[24:25]
	v_cvt_pk_bf16_f32 v54, v62, v63
	v_cvt_pk_bf16_f32 v55, v72, v73
	v_cvt_pk_bf16_f32 v56, v70, v71
	v_cvt_pk_bf16_f32 v57, v66, v67
	v_pk_fma_f32 v[74:75], v[22:23], v[114:115], v[30:31]
	v_pk_fma_f32 v[58:59], v[20:21], v[58:59], v[28:29]
	global_store_dwordx4 v[82:83], v[54:57], off offset:-1024 sc1
	s_mov_b64 vcc, s[4:5]
	s_nop 0
	v_cvt_pk_bf16_f32 v54, v58, v59
	v_cvt_pk_bf16_f32 v55, v74, v75
	v_cvt_pk_bf16_f32 v56, v68, v69
	v_cvt_pk_bf16_f32 v57, v64, v65
	global_store_dwordx4 v[82:83], v[54:57], off sc1
	v_lshl_add_u64 v[82:83], v[82:83], 0, s[34:35]
	s_cbranch_vccnz .LBB0_1871

.LBB0_2750:
	s_waitcnt vmcnt(0)
	v_lshlrev_b32_e32 v73, 2, v64
	v_lshlrev_b32_e32 v75, 2, v66
	v_ashrrev_i32_e32 v79, 31, v67
	v_mov_b32_e32 v78, v67
	v_add_co_u32_e32 v64, vcc, s27, v70
	v_lshlrev_b32_e32 v83, 2, v60
	v_ashrrev_i32_e32 v67, 31, v61
	v_mov_b32_e32 v66, v61
	v_lshlrev_b32_e32 v85, 2, v62
	v_ashrrev_i32_e32 v61, 31, v63
	v_mov_b32_e32 v60, v63
	v_lshlrev_b32_e32 v87, 2, v56
	s_add_i32 s0, s26, s24
	v_ashrrev_i32_e32 v77, 31, v65
	v_mov_b32_e32 v76, v65
	v_addc_co_u32_e32 v65, vcc, -1, v71, vcc
	v_ashrrev_i32_e32 v63, 31, v57
	v_mov_b32_e32 v62, v57
	v_lshlrev_b32_e32 v91, 2, v58
	v_ashrrev_i32_e32 v57, 31, v59
	v_mov_b32_e32 v56, v59
	v_lshlrev_b32_e32 v95, 2, v52
	v_ashrrev_i32_e32 v59, 31, v53
	v_mov_b32_e32 v58, v53
	v_lshlrev_b32_e32 v54, 2, v54
	v_ashrrev_i32_e32 v53, 31, v55
	v_mov_b32_e32 v52, v55
	v_mul_f32_e32 v82, 0x3d000000, v96
	v_mul_f32_e32 v84, 0x3d000000, v97
	v_add_u32_e32 v55, s25, v73
	v_lshlrev_b64 v[96:97], 10, v[66:67]
	v_add_u32_e32 v66, s25, v85
	v_lshlrev_b64 v[110:111], 10, v[60:61]
	v_add_u32_e32 v60, s25, v87
	s_cmp_lt_i32 s0, 0x8000
	global_load_dwordx4 v[36:39], v[70:71], off offset:-4096
	global_load_dwordx4 v[32:35], v[70:71], off offset:-3072
	global_load_dwordx4 v[48:51], v[70:71], off offset:-2048
	global_load_dwordx4 v[44:47], v[70:71], off offset:-1024
	global_load_dwordx4 v[40:43], v[70:71], off
	v_mul_f32_e32 v72, 0x3d000000, v102
	v_mul_f32_e32 v74, 0x3d000000, v103
	v_mul_f32_e32 v86, 0x3d000000, v88
	v_mul_f32_e32 v90, 0x3d000000, v89
	v_mul_f32_e32 v94, 0x3d000000, v80
	v_mul_f32_e32 v98, 0x3d000000, v81
	v_lshlrev_b64 v[80:81], 10, v[76:77]
	v_add_u32_e32 v73, s25, v75
	v_lshlrev_b64 v[88:89], 10, v[78:79]
	global_load_dwordx4 v[76:79], v[64:65], off offset:-3072
	global_load_dwordx4 v[102:105], v[64:65], off offset:-2048
	v_add_u32_e32 v75, s25, v83
	global_load_dwordx4 v[106:109], v[64:65], off offset:-1024
	v_lshlrev_b64 v[112:113], 10, v[62:63]
	v_add_u32_e32 v61, s25, v91
	v_lshlrev_b64 v[114:115], 10, v[56:57]
	v_add_u32_e32 v57, s25, v95
	v_lshlrev_b64 v[116:117], 10, v[58:59]
	v_add_u32_e32 v59, s25, v54
	v_lshlrev_b64 v[118:119], 10, v[52:53]
	ds_read_b32 v52, v55
	ds_read_b32 v54, v73
	ds_read_b32 v56, v75
	ds_read_b32 v58, v66
	ds_read_b32 v60, v60
	ds_read_b32 v62, v61
	ds_read_b32 v64, v57
	ds_read_b32 v66, v59
	s_cselect_b64 s[4:5], -1, 0
	s_and_b64 s[6:7], s[4:5], exec
	s_cselect_b32 s6, s0, s26
	s_ashr_i32 s7, s6, 31
	s_mov_b32 s26, s0
	s_lshl_b64 s[0:1], s[6:7], 5
	s_waitcnt lgkmcnt(7)
	v_ashrrev_i32_e32 v53, 31, v52
	s_waitcnt lgkmcnt(6)
	v_ashrrev_i32_e32 v55, 31, v54
	s_waitcnt lgkmcnt(5)
	v_ashrrev_i32_e32 v57, 31, v56
	s_waitcnt lgkmcnt(4)
	v_ashrrev_i32_e32 v59, 31, v58
	s_waitcnt lgkmcnt(3)
	v_ashrrev_i32_e32 v61, 31, v60
	s_waitcnt lgkmcnt(2)
	v_ashrrev_i32_e32 v63, 31, v62
	s_waitcnt lgkmcnt(1)
	v_ashrrev_i32_e32 v65, 31, v64
	s_waitcnt lgkmcnt(0)
	v_ashrrev_i32_e32 v67, 31, v66
	s_add_u32 s0, s38, s0
	v_lshlrev_b64 v[52:53], 18, v[52:53]
	v_lshlrev_b64 v[54:55], 18, v[54:55]
	v_lshlrev_b64 v[56:57], 18, v[56:57]
	v_lshlrev_b64 v[58:59], 18, v[58:59]
	v_lshlrev_b64 v[60:61], 18, v[60:61]
	v_lshlrev_b64 v[62:63], 18, v[62:63]
	v_lshlrev_b64 v[64:65], 18, v[64:65]
	v_lshlrev_b64 v[66:67], 18, v[66:67]
	s_addc_u32 s1, s39, s1
	v_lshl_add_u64 v[120:121], s[36:37], 0, v[52:53]
	v_lshl_add_u64 v[122:123], s[36:37], 0, v[54:55]
	v_lshl_add_u64 v[124:125], s[36:37], 0, v[56:57]
	v_lshl_add_u64 v[126:127], s[36:37], 0, v[58:59]
	v_lshl_add_u64 v[138:139], s[36:37], 0, v[60:61]
	v_lshl_add_u64 v[140:141], s[36:37], 0, v[62:63]
	v_lshl_add_u64 v[142:143], s[36:37], 0, v[64:65]
	v_lshl_add_u64 v[144:145], s[36:37], 0, v[66:67]
	global_load_dwordx2 v[146:147], v128, s[0:1] offset:16
	global_load_dwordx4 v[64:67], v128, s[0:1]
	global_load_dwordx2 v[148:149], v128, s[0:1] offset:48
	global_load_dwordx4 v[60:63], v128, s[0:1] offset:32
	global_load_dwordx2 v[150:151], v128, s[0:1] offset:80
	global_load_dwordx4 v[56:59], v128, s[0:1] offset:64
	global_load_dwordx2 v[152:153], v128, s[0:1] offset:112
	global_load_dwordx4 v[52:55], v128, s[0:1] offset:96
	v_lshl_add_u64 v[80:81], v[120:121], 0, v[80:81]
	v_lshl_add_u64 v[110:111], v[126:127], 0, v[110:111]
	v_lshl_add_u64 v[112:113], v[138:139], 0, v[112:113]
	v_lshl_add_u64 v[114:115], v[140:141], 0, v[114:115]
	v_lshl_add_u64 v[116:117], v[142:143], 0, v[116:117]
	v_lshl_add_u64 v[118:119], v[144:145], 0, v[118:119]
	v_lshl_add_u64 v[88:89], v[122:123], 0, v[88:89]
	v_lshl_add_u64 v[96:97], v[124:125], 0, v[96:97]
	v_lshl_add_u64 v[80:81], v[80:81], 0, v[68:69]
	v_lshl_add_u64 v[110:111], v[110:111], 0, v[68:69]
	v_lshl_add_u64 v[112:113], v[112:113], 0, v[68:69]
	v_lshl_add_u64 v[114:115], v[114:115], 0, v[68:69]
	v_lshl_add_u64 v[116:117], v[116:117], 0, v[68:69]
	v_lshl_add_u64 v[118:119], v[118:119], 0, v[68:69]
	v_lshl_add_u64 v[88:89], v[88:89], 0, v[68:69]
	v_lshl_add_u64 v[96:97], v[96:97], 0, v[68:69]
	global_load_dwordx2 v[120:121], v[80:81], off nt
	global_load_dwordx2 v[122:123], v[88:89], off nt
	global_load_dwordx2 v[124:125], v[88:89], off offset:512 nt
	global_load_dwordx2 v[126:127], v[80:81], off offset:512 nt
	global_load_dwordx2 v[138:139], v[96:97], off nt
	global_load_dwordx2 v[140:141], v[110:111], off nt
	s_nop 0
	global_load_dwordx2 v[110:111], v[110:111], off offset:512 nt
	s_nop 0
	global_load_dwordx2 v[142:143], v[96:97], off offset:512 nt
	global_load_dwordx2 v[144:145], v[112:113], off nt
	global_load_dwordx2 v[154:155], v[114:115], off nt
	s_nop 0
	global_load_dwordx2 v[114:115], v[114:115], off offset:512 nt
	s_nop 0
	global_load_dwordx2 v[112:113], v[112:113], off offset:512 nt
	s_nop 0
	global_load_dwordx2 v[156:157], v[116:117], off nt
	global_load_dwordx2 v[158:159], v[118:119], off nt
	s_nop 0
	global_load_dwordx2 v[118:119], v[118:119], off offset:512 nt
	s_nop 0
	global_load_dwordx2 v[116:117], v[116:117], off offset:512 nt
	v_add_co_u32_e32 v92, vcc, s33, v70
	s_and_b64 s[4:5], s[4:5], exec
	s_nop 0
	v_addc_co_u32_e32 v93, vcc, -1, v71, vcc
	v_add_co_u32_e32 v100, vcc, s34, v70
	s_waitcnt vmcnt(29)
	v_lshlrev_b32_e32 v170, 16, v50
	v_and_b32_e32 v171, 0xffff0000, v50
	v_lshlrev_b32_e32 v172, 16, v51
	v_and_b32_e32 v173, 0xffff0000, v51
	s_waitcnt vmcnt(27)
	v_lshlrev_b32_e32 v180, 16, v42
	v_and_b32_e32 v181, 0xffff0000, v42
	v_lshlrev_b32_e32 v182, 16, v43
	v_and_b32_e32 v183, 0xffff0000, v43
	v_lshlrev_b32_e32 v160, 16, v36
	v_and_b32_e32 v161, 0xffff0000, v36
	v_lshlrev_b32_e32 v36, 16, v37
	s_waitcnt vmcnt(26)
	v_lshlrev_b32_e32 v42, 16, v76
	s_waitcnt vmcnt(25)
	v_lshlrev_b32_e32 v184, 16, v102
	v_and_b32_e32 v185, 0xffff0000, v102
	v_lshlrev_b32_e32 v186, 16, v103
	v_and_b32_e32 v187, 0xffff0000, v103
	v_and_b32_e32 v43, 0xffff0000, v76
	v_lshlrev_b32_e32 v50, 16, v77
	v_and_b32_e32 v51, 0xffff0000, v77
	v_lshlrev_b32_e32 v76, 16, v78
	v_and_b32_e32 v77, 0xffff0000, v78
	v_lshlrev_b32_e32 v78, 16, v79
	v_and_b32_e32 v79, 0xffff0000, v79
	v_lshlrev_b32_e32 v188, 16, v104
	v_and_b32_e32 v189, 0xffff0000, v104
	v_lshlrev_b32_e32 v104, 16, v105
	v_and_b32_e32 v105, 0xffff0000, v105
	v_and_b32_e32 v37, 0xffff0000, v37
	v_lshlrev_b32_e32 v162, 16, v38
	v_and_b32_e32 v163, 0xffff0000, v38
	v_lshlrev_b32_e32 v38, 16, v39
	v_and_b32_e32 v39, 0xffff0000, v39
	v_lshlrev_b32_e32 v164, 16, v32
	v_and_b32_e32 v165, 0xffff0000, v32
	v_lshlrev_b32_e32 v32, 16, v33
	v_and_b32_e32 v33, 0xffff0000, v33
	v_lshlrev_b32_e32 v166, 16, v34
	v_and_b32_e32 v167, 0xffff0000, v34
	v_lshlrev_b32_e32 v34, 16, v35
	v_and_b32_e32 v35, 0xffff0000, v35
	v_lshlrev_b32_e32 v168, 16, v48
	v_and_b32_e32 v169, 0xffff0000, v48
	v_lshlrev_b32_e32 v48, 16, v49
	v_and_b32_e32 v49, 0xffff0000, v49
	v_lshlrev_b32_e32 v174, 16, v44
	v_and_b32_e32 v175, 0xffff0000, v44
	v_lshlrev_b32_e32 v44, 16, v45
	v_and_b32_e32 v45, 0xffff0000, v45
	s_waitcnt vmcnt(23)
	v_mov_b64_e32 v[102:103], v[146:147]
	v_lshlrev_b32_e32 v176, 16, v46
	s_waitcnt vmcnt(21)
	v_mov_b64_e32 v[96:97], v[148:149]
	v_and_b32_e32 v177, 0xffff0000, v46
	s_waitcnt vmcnt(19)
	v_mov_b64_e32 v[88:89], v[150:151]
	v_lshlrev_b32_e32 v46, 16, v47
	s_waitcnt vmcnt(17)
	v_mov_b64_e32 v[80:81], v[152:153]
	v_and_b32_e32 v47, 0xffff0000, v47
	v_lshlrev_b32_e32 v178, 16, v40
	s_waitcnt vmcnt(15)
	v_cvt_pk_f32_fp8_e32 v[146:147], v120
	s_waitcnt vmcnt(14)
	v_cvt_pk_f32_fp8_e32 v[152:153], v122
	v_cvt_pk_f32_fp8_sdwa v[194:195], v122 src0_sel:WORD_1
	v_cvt_pk_f32_fp8_sdwa v[148:149], v120 src0_sel:WORD_1
	v_cvt_pk_f32_fp8_e32 v[196:197], v123
	v_cvt_pk_f32_fp8_sdwa v[122:123], v123 src0_sel:WORD_1
	s_waitcnt vmcnt(13)
	v_cvt_pk_f32_fp8_e32 v[204:205], v124
	v_cvt_pk_f32_fp8_sdwa v[206:207], v124 src0_sel:WORD_1
	v_cvt_pk_f32_fp8_e32 v[208:209], v125
	v_cvt_pk_f32_fp8_sdwa v[124:125], v125 src0_sel:WORD_1
	v_pk_mul_f32 v[194:195], v[74:75], v[194:195] op_sel_hi:[0,1]
	v_pk_mul_f32 v[152:153], v[74:75], v[152:153] op_sel_hi:[0,1]
	v_cvt_pk_f32_fp8_e32 v[150:151], v121
	v_cvt_pk_f32_fp8_sdwa v[120:121], v121 src0_sel:WORD_1
	s_waitcnt vmcnt(12)
	v_cvt_pk_f32_fp8_e32 v[198:199], v126
	v_cvt_pk_f32_fp8_sdwa v[200:201], v126 src0_sel:WORD_1
	v_cvt_pk_f32_fp8_e32 v[202:203], v127
	v_cvt_pk_f32_fp8_sdwa v[126:127], v127 src0_sel:WORD_1
	s_waitcnt vmcnt(10)
	v_cvt_pk_f32_fp8_e32 v[216:217], v140
	v_cvt_pk_f32_fp8_sdwa v[218:219], v140 src0_sel:WORD_1
	v_cvt_pk_f32_fp8_e32 v[220:221], v141
	v_cvt_pk_f32_fp8_sdwa v[140:141], v141 src0_sel:WORD_1
	s_waitcnt vmcnt(9)
	v_cvt_pk_f32_fp8_e32 v[228:229], v110
	v_cvt_pk_f32_fp8_sdwa v[230:231], v110 src0_sel:WORD_1
	v_cvt_pk_f32_fp8_e32 v[232:233], v111
	v_cvt_pk_f32_fp8_sdwa v[110:111], v111 src0_sel:WORD_1
	s_waitcnt vmcnt(6)
	v_cvt_pk_f32_fp8_e32 v[240:241], v154
	v_cvt_pk_f32_fp8_sdwa v[242:243], v154 src0_sel:WORD_1
	v_cvt_pk_f32_fp8_e32 v[244:245], v155
	v_cvt_pk_f32_fp8_sdwa v[154:155], v155 src0_sel:WORD_1
	v_pk_mul_f32 v[122:123], v[74:75], v[122:123] op_sel_hi:[0,1]
	v_pk_mul_f32 v[196:197], v[74:75], v[196:197] op_sel_hi:[0,1]
	v_pk_mul_f32 v[206:207], v[74:75], v[206:207] op_sel_hi:[0,1]
	v_pk_mul_f32 v[204:205], v[74:75], v[204:205] op_sel_hi:[0,1]
	v_pk_mul_f32 v[124:125], v[74:75], v[124:125] op_sel_hi:[0,1]
	v_pk_mul_f32 v[74:75], v[74:75], v[208:209] op_sel_hi:[0,1]
	s_waitcnt vmcnt(5)
	v_cvt_pk_f32_fp8_e32 v[208:209], v114
	v_pk_fma_f32 v[146:147], v[72:73], v[146:147], v[152:153] op_sel_hi:[0,1,1]
	v_cvt_pk_f32_fp8_sdwa v[152:153], v114 src0_sel:WORD_1
	v_pk_fma_f32 v[148:149], v[72:73], v[148:149], v[194:195] op_sel_hi:[0,1,1]
	v_cvt_pk_f32_fp8_e32 v[194:195], v115
	v_cvt_pk_f32_fp8_sdwa v[114:115], v115 src0_sel:WORD_1
	v_cvt_pk_f32_fp8_e32 v[210:211], v138
	v_cvt_pk_f32_fp8_sdwa v[212:213], v138 src0_sel:WORD_1
	v_pk_fma_f32 v[150:151], v[72:73], v[150:151], v[196:197] op_sel_hi:[0,1,1]
	v_pk_fma_f32 v[120:121], v[72:73], v[120:121], v[122:123] op_sel_hi:[0,1,1]
	v_pk_fma_f32 v[198:199], v[72:73], v[198:199], v[204:205] op_sel_hi:[0,1,1]
	v_pk_fma_f32 v[200:201], v[72:73], v[200:201], v[206:207] op_sel_hi:[0,1,1]
	s_waitcnt vmcnt(2)
	v_cvt_pk_f32_fp8_e32 v[206:207], v158
	v_pk_fma_f32 v[74:75], v[72:73], v[202:203], v[74:75] op_sel_hi:[0,1,1]
	v_cvt_pk_f32_fp8_sdwa v[202:203], v158 src0_sel:WORD_1
	v_pk_fma_f32 v[72:73], v[72:73], v[126:127], v[124:125] op_sel_hi:[0,1,1]
	v_cvt_pk_f32_fp8_e32 v[124:125], v159
	v_cvt_pk_f32_fp8_sdwa v[126:127], v159 src0_sel:WORD_1
	s_waitcnt vmcnt(1)
	v_cvt_pk_f32_fp8_e32 v[158:159], v118
	v_pk_mul_f32 v[218:219], v[84:85], v[218:219] op_sel_hi:[0,1]
	v_pk_mul_f32 v[216:217], v[84:85], v[216:217] op_sel_hi:[0,1]
	v_pk_mul_f32 v[140:141], v[84:85], v[140:141] op_sel_hi:[0,1]
	v_pk_mul_f32 v[220:221], v[84:85], v[220:221] op_sel_hi:[0,1]
	v_pk_mul_f32 v[230:231], v[84:85], v[230:231] op_sel_hi:[0,1]
	v_pk_mul_f32 v[228:229], v[84:85], v[228:229] op_sel_hi:[0,1]
	v_pk_mul_f32 v[110:111], v[84:85], v[110:111] op_sel_hi:[0,1]
	v_pk_mul_f32 v[84:85], v[84:85], v[232:233] op_sel_hi:[0,1]
	v_cvt_pk_f32_fp8_sdwa v[232:233], v118 src0_sel:WORD_1
	v_pk_mul_f32 v[242:243], v[90:91], v[242:243] op_sel_hi:[0,1]
	v_pk_mul_f32 v[240:241], v[90:91], v[240:241] op_sel_hi:[0,1]
	v_pk_mul_f32 v[154:155], v[90:91], v[154:155] op_sel_hi:[0,1]
	v_pk_mul_f32 v[244:245], v[90:91], v[244:245] op_sel_hi:[0,1]
	v_pk_mul_f32 v[152:153], v[90:91], v[152:153] op_sel_hi:[0,1]
	v_pk_mul_f32 v[208:209], v[90:91], v[208:209] op_sel_hi:[0,1]
	v_pk_mul_f32 v[114:115], v[90:91], v[114:115] op_sel_hi:[0,1]
	v_pk_mul_f32 v[90:91], v[90:91], v[194:195] op_sel_hi:[0,1]
	v_cvt_pk_f32_fp8_e32 v[194:195], v119
	v_cvt_pk_f32_fp8_sdwa v[118:119], v119 src0_sel:WORD_1
	v_cvt_pk_f32_fp8_e32 v[214:215], v139
	v_cvt_pk_f32_fp8_sdwa v[138:139], v139 src0_sel:WORD_1
	v_cvt_pk_f32_fp8_e32 v[222:223], v142
	v_cvt_pk_f32_fp8_sdwa v[224:225], v142 src0_sel:WORD_1
	v_cvt_pk_f32_fp8_e32 v[226:227], v143
	v_cvt_pk_f32_fp8_sdwa v[142:143], v143 src0_sel:WORD_1
	v_cvt_pk_f32_fp8_e32 v[234:235], v144
	v_cvt_pk_f32_fp8_sdwa v[236:237], v144 src0_sel:WORD_1
	v_cvt_pk_f32_fp8_e32 v[238:239], v145
	v_cvt_pk_f32_fp8_sdwa v[144:145], v145 src0_sel:WORD_1
	v_cvt_pk_f32_fp8_e32 v[246:247], v112
	v_cvt_pk_f32_fp8_sdwa v[248:249], v112 src0_sel:WORD_1
	v_cvt_pk_f32_fp8_e32 v[250:251], v113
	v_cvt_pk_f32_fp8_sdwa v[112:113], v113 src0_sel:WORD_1
	v_cvt_pk_f32_fp8_e32 v[196:197], v156
	v_cvt_pk_f32_fp8_sdwa v[122:123], v156 src0_sel:WORD_1
	v_cvt_pk_f32_fp8_e32 v[204:205], v157
	v_cvt_pk_f32_fp8_sdwa v[156:157], v157 src0_sel:WORD_1
	v_pk_mul_f32 v[202:203], v[98:99], v[202:203] op_sel_hi:[0,1]
	v_pk_mul_f32 v[206:207], v[98:99], v[206:207] op_sel_hi:[0,1]
	v_pk_mul_f32 v[126:127], v[98:99], v[126:127] op_sel_hi:[0,1]
	v_pk_mul_f32 v[124:125], v[98:99], v[124:125] op_sel_hi:[0,1]
	v_pk_mul_f32 v[232:233], v[98:99], v[232:233] op_sel_hi:[0,1]
	v_pk_mul_f32 v[158:159], v[98:99], v[158:159] op_sel_hi:[0,1]
	v_pk_mul_f32 v[118:119], v[98:99], v[118:119] op_sel_hi:[0,1]
	v_pk_mul_f32 v[98:99], v[98:99], v[194:195] op_sel_hi:[0,1]
	s_waitcnt vmcnt(0)
	v_cvt_pk_f32_fp8_e32 v[194:195], v116
	v_pk_fma_f32 v[210:211], v[82:83], v[210:211], v[216:217] op_sel_hi:[0,1,1]
	v_cvt_pk_f32_fp8_sdwa v[216:217], v116 src0_sel:WORD_1
	v_pk_fma_f32 v[212:213], v[82:83], v[212:213], v[218:219] op_sel_hi:[0,1,1]
	v_cvt_pk_f32_fp8_e32 v[218:219], v117
	v_cvt_pk_f32_fp8_sdwa v[116:117], v117 src0_sel:WORD_1
	v_and_b32_e32 v179, 0xffff0000, v40
	v_lshlrev_b32_e32 v40, 16, v41
	v_and_b32_e32 v41, 0xffff0000, v41
	v_lshlrev_b32_e32 v190, 16, v106
	v_and_b32_e32 v191, 0xffff0000, v106
	v_lshlrev_b32_e32 v106, 16, v107
	v_and_b32_e32 v107, 0xffff0000, v107
	v_lshlrev_b32_e32 v192, 16, v108
	v_and_b32_e32 v193, 0xffff0000, v108
	v_lshlrev_b32_e32 v108, 16, v109
	v_and_b32_e32 v109, 0xffff0000, v109
	v_pk_fma_f32 v[214:215], v[82:83], v[214:215], v[220:221] op_sel_hi:[0,1,1]
	v_pk_fma_f32 v[138:139], v[82:83], v[138:139], v[140:141] op_sel_hi:[0,1,1]
	v_pk_fma_f32 v[140:141], v[82:83], v[222:223], v[228:229] op_sel_hi:[0,1,1]
	v_pk_fma_f32 v[220:221], v[82:83], v[224:225], v[230:231] op_sel_hi:[0,1,1]
	v_pk_fma_f32 v[84:85], v[82:83], v[226:227], v[84:85] op_sel_hi:[0,1,1]
	v_pk_fma_f32 v[82:83], v[82:83], v[142:143], v[110:111] op_sel_hi:[0,1,1]
	v_pk_fma_f32 v[142:143], v[86:87], v[234:235], v[240:241] op_sel_hi:[0,1,1]
	v_pk_fma_f32 v[222:223], v[86:87], v[236:237], v[242:243] op_sel_hi:[0,1,1]
	v_pk_fma_f32 v[224:225], v[86:87], v[238:239], v[244:245] op_sel_hi:[0,1,1]
	v_pk_fma_f32 v[144:145], v[86:87], v[144:145], v[154:155] op_sel_hi:[0,1,1]
	v_pk_fma_f32 v[154:155], v[86:87], v[246:247], v[208:209] op_sel_hi:[0,1,1]
	v_pk_fma_f32 v[152:153], v[86:87], v[248:249], v[152:153] op_sel_hi:[0,1,1]
	v_pk_fma_f32 v[208:209], v[86:87], v[250:251], v[90:91] op_sel_hi:[0,1,1]
	v_pk_fma_f32 v[226:227], v[86:87], v[112:113], v[114:115] op_sel_hi:[0,1,1]
	v_pk_fma_f32 v[196:197], v[94:95], v[196:197], v[206:207] op_sel_hi:[0,1,1]
	v_pk_fma_f32 v[202:203], v[94:95], v[122:123], v[202:203] op_sel_hi:[0,1,1]
	v_pk_fma_f32 v[204:205], v[94:95], v[204:205], v[124:125] op_sel_hi:[0,1,1]
	v_pk_fma_f32 v[156:157], v[94:95], v[156:157], v[126:127] op_sel_hi:[0,1,1]
	v_pk_fma_f32 v[158:159], v[94:95], v[194:195], v[158:159] op_sel_hi:[0,1,1]
	v_pk_fma_f32 v[194:195], v[94:95], v[216:217], v[232:233] op_sel_hi:[0,1,1]
	v_pk_fma_f32 v[206:207], v[94:95], v[218:219], v[98:99] op_sel_hi:[0,1,1]
	v_pk_fma_f32 v[216:217], v[94:95], v[116:117], v[118:119] op_sel_hi:[0,1,1]
	v_pk_fma_f32 v[114:115], v[50:51], s[30:31], v[148:149] op_sel_hi:[1,0,1]
	v_pk_fma_f32 v[118:119], v[42:43], s[30:31], v[146:147] op_sel_hi:[1,0,1]
	v_pk_fma_f32 v[122:123], v[78:79], s[30:31], v[120:121] op_sel_hi:[1,0,1]
	v_pk_fma_f32 v[126:127], v[76:77], s[30:31], v[150:151] op_sel_hi:[1,0,1]
	v_pk_fma_f32 v[112:113], v[186:187], s[30:31], v[200:201] op_sel_hi:[1,0,1]
	v_pk_fma_f32 v[116:117], v[184:185], s[30:31], v[198:199] op_sel_hi:[1,0,1]
	v_pk_fma_f32 v[120:121], v[104:105], s[30:31], v[72:73] op_sel_hi:[1,0,1]
	v_pk_fma_f32 v[124:125], v[188:189], s[30:31], v[74:75] op_sel_hi:[1,0,1]
	v_pk_fma_f32 v[90:91], v[106:107], s[30:31], v[212:213] op_sel_hi:[1,0,1]
	v_pk_fma_f32 v[98:99], v[190:191], s[30:31], v[210:211] op_sel_hi:[1,0,1]
	v_pk_fma_f32 v[106:107], v[108:109], s[30:31], v[138:139] op_sel_hi:[1,0,1]
	v_pk_fma_f32 v[110:111], v[192:193], s[30:31], v[214:215] op_sel_hi:[1,0,1]
	v_pk_fma_f32 v[86:87], v[36:37], s[30:31], v[220:221] op_sel_hi:[1,0,1]
	v_pk_fma_f32 v[94:95], v[160:161], s[30:31], v[140:141] op_sel_hi:[1,0,1]
	v_pk_fma_f32 v[104:105], v[38:39], s[30:31], v[82:83] op_sel_hi:[1,0,1]
	v_pk_fma_f32 v[108:109], v[162:163], s[30:31], v[84:85] op_sel_hi:[1,0,1]
	v_pk_fma_f32 v[50:51], v[32:33], s[30:31], v[222:223] op_sel_hi:[1,0,1]
	v_pk_fma_f32 v[74:75], v[164:165], s[30:31], v[142:143] op_sel_hi:[1,0,1]
	v_pk_fma_f32 v[78:79], v[34:35], s[30:31], v[144:145] op_sel_hi:[1,0,1]
	v_pk_fma_f32 v[84:85], v[166:167], s[30:31], v[224:225] op_sel_hi:[1,0,1]
	v_pk_fma_f32 v[48:49], v[48:49], s[30:31], v[152:153] op_sel_hi:[1,0,1]
	v_pk_fma_f32 v[72:73], v[168:169], s[30:31], v[154:155] op_sel_hi:[1,0,1]
	v_pk_fma_f32 v[76:77], v[172:173], s[30:31], v[226:227] op_sel_hi:[1,0,1]
	v_pk_fma_f32 v[82:83], v[170:171], s[30:31], v[208:209] op_sel_hi:[1,0,1]
	v_pk_fma_f32 v[34:35], v[44:45], s[30:31], v[202:203] op_sel_hi:[1,0,1]
	v_pk_fma_f32 v[38:39], v[174:175], s[30:31], v[196:197] op_sel_hi:[1,0,1]
	v_pk_fma_f32 v[42:43], v[46:47], s[30:31], v[156:157] op_sel_hi:[1,0,1]
	v_pk_fma_f32 v[46:47], v[176:177], s[30:31], v[204:205] op_sel_hi:[1,0,1]
	v_pk_fma_f32 v[32:33], v[40:41], s[30:31], v[194:195] op_sel_hi:[1,0,1]
	v_pk_fma_f32 v[36:37], v[178:179], s[30:31], v[158:159] op_sel_hi:[1,0,1]
	v_pk_fma_f32 v[40:41], v[182:183], s[30:31], v[216:217] op_sel_hi:[1,0,1]
	v_pk_fma_f32 v[44:45], v[180:181], s[30:31], v[206:207] op_sel_hi:[1,0,1]
	v_mov_b32_e32 v138, v118
	v_mov_b32_e32 v139, v116
	v_mov_b32_e32 v140, v119
	v_mov_b32_e32 v141, v117
	v_mov_b32_e32 v142, v114
	v_mov_b32_e32 v143, v112
	v_mov_b32_e32 v144, v115
	v_mov_b32_e32 v145, v113
	v_mov_b32_e32 v146, v126
	v_mov_b32_e32 v147, v124
	v_mov_b32_e32 v148, v127
	v_mov_b32_e32 v149, v125
	v_mov_b32_e32 v150, v122
	v_mov_b32_e32 v151, v120
	v_mov_b32_e32 v152, v123
	v_mov_b32_e32 v153, v121
	v_mov_b32_e32 v154, v98
	v_mov_b32_e32 v155, v94
	v_mov_b32_e32 v156, v99
	v_mov_b32_e32 v157, v95
	v_mov_b32_e32 v158, v90
	v_mov_b32_e32 v159, v86
	v_mov_b32_e32 v160, v91
	v_mov_b32_e32 v161, v87
	v_mov_b32_e32 v162, v110
	v_mov_b32_e32 v163, v108
	v_mov_b32_e32 v164, v111
	v_mov_b32_e32 v165, v109
	v_mov_b32_e32 v166, v106
	v_mov_b32_e32 v167, v104
	v_mov_b32_e32 v168, v107
	v_mov_b32_e32 v169, v105
	v_mov_b32_e32 v170, v74
	v_mov_b32_e32 v171, v72
	v_mov_b32_e32 v172, v75
	v_mov_b32_e32 v173, v73
	v_mov_b32_e32 v174, v50
	v_mov_b32_e32 v175, v48
	v_mov_b32_e32 v176, v51
	v_mov_b32_e32 v177, v49
	v_mov_b32_e32 v178, v84
	v_mov_b32_e32 v179, v82
	v_mov_b32_e32 v180, v85
	v_mov_b32_e32 v181, v83
	v_mov_b32_e32 v182, v78
	v_mov_b32_e32 v183, v76
	v_mov_b32_e32 v184, v79
	v_mov_b32_e32 v185, v77
	v_mov_b32_e32 v186, v38
	v_mov_b32_e32 v187, v36
	v_mov_b32_e32 v188, v39
	v_mov_b32_e32 v189, v37
	v_mov_b32_e32 v190, v34
	v_mov_b32_e32 v191, v32
	v_mov_b32_e32 v192, v35
	v_mov_b32_e32 v193, v33
	v_mov_b32_e32 v194, v46
	v_mov_b32_e32 v195, v44
	v_mov_b32_e32 v196, v47
	v_mov_b32_e32 v197, v45
	v_mov_b32_e32 v198, v42
	v_mov_b32_e32 v199, v40
	v_mov_b32_e32 v200, v43
	v_mov_b32_e32 v201, v41
	v_pk_add_f32 v[138:139], v[138:139], v[140:141]
	v_pk_add_f32 v[140:141], v[142:143], v[144:145]
	v_pk_add_f32 v[142:143], v[146:147], v[148:149]
	v_pk_add_f32 v[144:145], v[150:151], v[152:153]
	v_pk_add_f32 v[146:147], v[154:155], v[156:157]
	v_pk_add_f32 v[148:149], v[158:159], v[160:161]
	v_pk_add_f32 v[150:151], v[162:163], v[164:165]
	v_pk_add_f32 v[152:153], v[166:167], v[168:169]
	v_pk_add_f32 v[154:155], v[170:171], v[172:173]
	v_pk_add_f32 v[156:157], v[174:175], v[176:177]
	v_pk_add_f32 v[158:159], v[178:179], v[180:181]
	v_pk_add_f32 v[160:161], v[182:183], v[184:185]
	v_pk_add_f32 v[162:163], v[186:187], v[188:189]
	v_pk_add_f32 v[164:165], v[190:191], v[192:193]
	v_pk_add_f32 v[166:167], v[194:195], v[196:197]
	v_pk_add_f32 v[168:169], v[198:199], v[200:201]
	v_pk_add_f32 v[138:139], v[138:139], v[140:141]
	v_pk_add_f32 v[140:141], v[142:143], v[144:145]
	v_pk_add_f32 v[142:143], v[146:147], v[148:149]
	v_pk_add_f32 v[144:145], v[150:151], v[152:153]
	v_pk_add_f32 v[146:147], v[154:155], v[156:157]
	v_pk_add_f32 v[148:149], v[158:159], v[160:161]
	v_pk_add_f32 v[150:151], v[162:163], v[164:165]
	v_pk_add_f32 v[152:153], v[166:167], v[168:169]
	v_pk_add_f32 v[138:139], v[138:139], v[140:141]
	v_pk_add_f32 v[140:141], v[142:143], v[144:145]
	v_pk_add_f32 v[142:143], v[146:147], v[148:149]
	v_pk_add_f32 v[144:145], v[150:151], v[152:153]
	v_add_f32_e32 v137, 0, v138
	v_add_f32_e32 v138, 0, v140
	v_add_f32_e32 v140, 0, v142
	v_add_f32_e32 v142, 0, v144
	v_add_f32_e32 v137, v137, v139
	v_add_f32_e32 v138, v138, v141
	v_add_f32_e32 v139, v140, v143
	v_add_f32_e32 v140, v142, v145
	ds_bpermute_b32 v141, v129, v137
	ds_bpermute_b32 v142, v129, v138
	ds_bpermute_b32 v143, v129, v139
	ds_bpermute_b32 v144, v129, v140
	v_addc_co_u32_e32 v101, vcc, -1, v71, vcc
	s_waitcnt lgkmcnt(3)
	v_add_f32_e32 v137, v137, v141
	s_waitcnt lgkmcnt(2)
	v_add_f32_e32 v138, v138, v142
	s_waitcnt lgkmcnt(1)
	v_add_f32_e32 v139, v139, v143
	s_waitcnt lgkmcnt(0)
	v_add_f32_e32 v140, v140, v144
	ds_bpermute_b32 v141, v130, v137
	ds_bpermute_b32 v142, v130, v138
	ds_bpermute_b32 v143, v130, v139
	ds_bpermute_b32 v144, v130, v140
	v_lshl_add_u64 v[70:71], v[70:71], 0, s[28:29]
	s_waitcnt lgkmcnt(3)
	v_add_f32_e32 v137, v137, v141
	s_waitcnt lgkmcnt(2)
	v_add_f32_e32 v138, v138, v142
	s_waitcnt lgkmcnt(1)
	v_add_f32_e32 v139, v139, v143
	s_waitcnt lgkmcnt(0)
	v_add_f32_e32 v140, v140, v144
	ds_bpermute_b32 v141, v131, v137
	ds_bpermute_b32 v142, v131, v138
	ds_bpermute_b32 v143, v131, v139
	ds_bpermute_b32 v144, v131, v140
	s_waitcnt lgkmcnt(3)
	v_add_f32_e32 v137, v137, v141
	s_waitcnt lgkmcnt(2)
	v_add_f32_e32 v138, v138, v142
	s_waitcnt lgkmcnt(1)
	v_add_f32_e32 v139, v139, v143
	s_waitcnt lgkmcnt(0)
	v_add_f32_e32 v140, v140, v144
	ds_bpermute_b32 v141, v132, v137
	ds_bpermute_b32 v142, v132, v138
	ds_bpermute_b32 v143, v132, v139
	ds_bpermute_b32 v144, v132, v140
	s_waitcnt lgkmcnt(3)
	v_add_f32_e32 v137, v137, v141
	s_waitcnt lgkmcnt(2)
	v_add_f32_e32 v138, v138, v142
	s_waitcnt lgkmcnt(1)
	v_add_f32_e32 v139, v139, v143
	s_waitcnt lgkmcnt(0)
	v_add_f32_e32 v140, v140, v144
	ds_bpermute_b32 v141, v133, v137
	ds_bpermute_b32 v142, v133, v138
	ds_bpermute_b32 v143, v133, v139
	ds_bpermute_b32 v144, v133, v140
	s_waitcnt lgkmcnt(3)
	v_add_f32_e32 v137, v137, v141
	s_waitcnt lgkmcnt(2)
	v_add_f32_e32 v138, v138, v142
	s_waitcnt lgkmcnt(1)
	v_add_f32_e32 v139, v139, v143
	s_waitcnt lgkmcnt(0)
	v_add_f32_e32 v140, v140, v144
	ds_bpermute_b32 v141, v134, v137
	ds_bpermute_b32 v142, v134, v138
	ds_bpermute_b32 v143, v134, v139
	ds_bpermute_b32 v144, v134, v140
	s_waitcnt lgkmcnt(3)
	v_add_f32_e32 v137, v137, v141
	s_waitcnt lgkmcnt(2)
	v_add_f32_e32 v138, v138, v142
	s_waitcnt lgkmcnt(1)
	v_add_f32_e32 v139, v139, v143
	s_waitcnt lgkmcnt(0)
	v_add_f32_e32 v140, v140, v144
	v_fmamk_f32 v119, v137, 0xba800000, v119
	v_fmac_f32_e32 v118, 0xba800000, v137
	v_fmamk_f32 v115, v137, 0xba800000, v115
	v_fmac_f32_e32 v114, 0xba800000, v137
	v_fmamk_f32 v127, v137, 0xba800000, v127
	v_fmac_f32_e32 v126, 0xba800000, v137
	v_fmamk_f32 v123, v137, 0xba800000, v123
	v_fmac_f32_e32 v122, 0xba800000, v137
	v_fmac_f32_e32 v116, 0xba800000, v137
	v_fmac_f32_e32 v112, 0xba800000, v137
	v_fmamk_f32 v99, v138, 0xba800000, v99
	v_fmac_f32_e32 v98, 0xba800000, v138
	v_fmamk_f32 v91, v138, 0xba800000, v91
	v_fmac_f32_e32 v90, 0xba800000, v138
	v_fmamk_f32 v111, v138, 0xba800000, v111
	v_fmac_f32_e32 v110, 0xba800000, v138
	v_fmamk_f32 v107, v138, 0xba800000, v107
	v_fmac_f32_e32 v106, 0xba800000, v138
	v_fmamk_f32 v95, v138, 0xba800000, v95
	v_fmac_f32_e32 v94, 0xba800000, v138
	v_fmamk_f32 v87, v138, 0xba800000, v87
	v_fmac_f32_e32 v86, 0xba800000, v138
	v_fmamk_f32 v105, v138, 0xba800000, v105
	v_fmac_f32_e32 v104, 0xba800000, v138
	v_fmamk_f32 v109, v138, 0xba800000, v109
	v_fmac_f32_e32 v108, 0xba800000, v138
	v_fmamk_f32 v75, v139, 0xba800000, v75
	v_fmac_f32_e32 v74, 0xba800000, v139
	v_fmamk_f32 v51, v139, 0xba800000, v51
	v_fmac_f32_e32 v50, 0xba800000, v139
	v_fmamk_f32 v85, v139, 0xba800000, v85
	v_fmac_f32_e32 v84, 0xba800000, v139
	v_fmamk_f32 v79, v139, 0xba800000, v79
	v_fmac_f32_e32 v78, 0xba800000, v139
	v_fmamk_f32 v73, v139, 0xba800000, v73
	v_fmac_f32_e32 v72, 0xba800000, v139
	v_fmamk_f32 v49, v139, 0xba800000, v49
	v_fmac_f32_e32 v48, 0xba800000, v139
	v_fmamk_f32 v77, v139, 0xba800000, v77
	v_fmac_f32_e32 v76, 0xba800000, v139
	v_fmamk_f32 v83, v139, 0xba800000, v83
	v_fmac_f32_e32 v82, 0xba800000, v139
	v_fmamk_f32 v39, v140, 0xba800000, v39
	v_fmac_f32_e32 v38, 0xba800000, v140
	v_fmamk_f32 v35, v140, 0xba800000, v35
	v_fmac_f32_e32 v34, 0xba800000, v140
	v_fmamk_f32 v47, v140, 0xba800000, v47
	v_fmac_f32_e32 v46, 0xba800000, v140
	v_fmamk_f32 v43, v140, 0xba800000, v43
	v_fmac_f32_e32 v42, 0xba800000, v140
	v_fmamk_f32 v37, v140, 0xba800000, v37
	v_fmac_f32_e32 v36, 0xba800000, v140
	v_fmamk_f32 v33, v140, 0xba800000, v33
	v_fmac_f32_e32 v32, 0xba800000, v140
	v_fmamk_f32 v41, v140, 0xba800000, v41
	v_fmac_f32_e32 v40, 0xba800000, v140
	v_fmamk_f32 v45, v140, 0xba800000, v45
	v_fmac_f32_e32 v44, 0xba800000, v140
	v_pk_mul_f32 v[138:139], v[114:115], v[114:115]
	v_pk_mul_f32 v[140:141], v[118:119], v[118:119]
	v_pk_mul_f32 v[142:143], v[122:123], v[122:123]
	v_pk_mul_f32 v[144:145], v[126:127], v[126:127]
	v_fmamk_f32 v117, v137, 0xba800000, v117
	v_fmamk_f32 v113, v137, 0xba800000, v113
	v_mul_f32_e32 v146, v116, v116
	v_mul_f32_e32 v148, v112, v112
	v_pk_mul_f32 v[150:151], v[90:91], v[90:91]
	v_pk_mul_f32 v[152:153], v[98:99], v[98:99]
	v_pk_mul_f32 v[154:155], v[106:107], v[106:107]
	v_pk_mul_f32 v[156:157], v[110:111], v[110:111]
	v_mul_f32_e32 v158, v94, v94
	v_mul_f32_e32 v160, v86, v86
	v_pk_mul_f32 v[162:163], v[50:51], v[50:51]
	v_pk_mul_f32 v[164:165], v[74:75], v[74:75]
	v_pk_mul_f32 v[166:167], v[78:79], v[78:79]
	v_pk_mul_f32 v[168:169], v[84:85], v[84:85]
	v_pk_mov_b32 v[186:187], v[140:141], v[138:139] op_sel:[1,0]
	v_mov_b32_e32 v141, v139
	v_pk_mov_b32 v[138:139], v[144:145], v[142:143] op_sel:[1,0]
	v_mov_b32_e32 v145, v143
	v_fmamk_f32 v125, v137, 0xba800000, v125
	v_fmac_f32_e32 v124, 0xba800000, v137
	v_pk_fma_f32 v[142:143], v[116:117], v[116:117], v[146:147] op_sel_hi:[1,1,0]
	v_pk_fma_f32 v[146:147], v[112:113], v[112:113], v[148:149] op_sel_hi:[1,1,0]
	v_pk_mov_b32 v[148:149], v[152:153], v[150:151] op_sel:[1,0]
	v_mov_b32_e32 v153, v151
	v_pk_mov_b32 v[150:151], v[156:157], v[154:155] op_sel:[1,0]
	v_mov_b32_e32 v157, v155
	v_pk_fma_f32 v[154:155], v[94:95], v[94:95], v[158:159] op_sel_hi:[1,1,0]
	v_pk_fma_f32 v[158:159], v[86:87], v[86:87], v[160:161] op_sel_hi:[1,1,0]
	v_pk_mov_b32 v[160:161], v[164:165], v[162:163] op_sel:[1,0]
	v_mov_b32_e32 v165, v163
	v_pk_mov_b32 v[162:163], v[168:169], v[166:167] op_sel:[1,0]
	v_mov_b32_e32 v169, v167
	v_pk_add_f32 v[140:141], v[186:187], v[140:141]
	v_pk_add_f32 v[138:139], v[138:139], v[144:145]
	v_fmamk_f32 v121, v137, 0xba800000, v121
	v_fmac_f32_e32 v120, 0xba800000, v137
	v_mul_f32_e32 v170, v72, v72
	v_mul_f32_e32 v172, v48, v48
	v_pk_mul_f32 v[174:175], v[34:35], v[34:35]
	v_pk_mul_f32 v[176:177], v[38:39], v[38:39]
	v_pk_mul_f32 v[178:179], v[42:43], v[42:43]
	v_pk_mul_f32 v[180:181], v[46:47], v[46:47]
	v_mul_f32_e32 v142, v124, v124
	v_mul_f32_e32 v146, v125, v125
	v_pk_add_f32 v[144:145], v[148:149], v[152:153]
	v_pk_add_f32 v[148:149], v[150:151], v[156:157]
	v_pk_add_f32 v[150:151], v[160:161], v[164:165]
	v_pk_add_f32 v[152:153], v[162:163], v[168:169]
	v_pk_add_f32 v[140:141], v[140:141], v[140:141] op_sel_hi:[0,1]
	v_pk_add_f32 v[138:139], v[138:139], v[138:139] op_sel_hi:[0,1]
	v_pk_fma_f32 v[166:167], v[72:73], v[72:73], v[170:171] op_sel_hi:[1,1,0]
	v_pk_fma_f32 v[170:171], v[48:49], v[48:49], v[172:173] op_sel_hi:[1,1,0]
	v_pk_mov_b32 v[172:173], v[176:177], v[174:175] op_sel:[1,0]
	v_mov_b32_e32 v177, v175
	v_pk_mov_b32 v[174:175], v[180:181], v[178:179] op_sel:[1,0]
	v_mov_b32_e32 v181, v179
	v_pk_add_f32 v[142:143], v[142:143], v[146:147]
	v_pk_add_f32 v[144:145], v[144:145], v[144:145] op_sel_hi:[0,1]
	v_pk_add_f32 v[146:147], v[148:149], v[148:149] op_sel_hi:[0,1]
	v_pk_add_f32 v[150:151], v[150:151], v[150:151] op_sel_hi:[0,1]
	v_pk_add_f32 v[152:153], v[152:153], v[152:153] op_sel_hi:[0,1]
	v_mul_f32_e32 v140, v120, v120
	v_mul_f32_e32 v138, v121, v121
	v_mul_f32_e32 v182, v36, v36
	v_mul_f32_e32 v184, v32, v32
	v_mul_f32_e32 v154, v108, v108
	v_mul_f32_e32 v158, v109, v109
	v_mul_f32_e32 v166, v82, v82
	v_mul_f32_e32 v170, v83, v83
	v_pk_add_f32 v[156:157], v[172:173], v[176:177]
	v_pk_add_f32 v[160:161], v[174:175], v[180:181]
	v_mul_f32_e32 v144, v104, v104
	v_mul_f32_e32 v146, v105, v105
	v_mul_f32_e32 v150, v76, v76
	v_mul_f32_e32 v152, v77, v77
	v_pk_add_f32 v[138:139], v[140:141], v[138:139]
	v_pk_fma_f32 v[178:179], v[36:37], v[36:37], v[182:183] op_sel_hi:[1,1,0]
	v_pk_fma_f32 v[182:183], v[32:33], v[32:33], v[184:185] op_sel_hi:[1,1,0]
	v_pk_add_f32 v[148:149], v[154:155], v[158:159]
	v_pk_add_f32 v[154:155], v[166:167], v[170:171]
	v_pk_add_f32 v[156:157], v[156:157], v[156:157] op_sel_hi:[0,1]
	v_pk_add_f32 v[158:159], v[160:161], v[160:161] op_sel_hi:[0,1]
	v_pk_add_f32 v[140:141], v[144:145], v[146:147]
	v_pk_add_f32 v[144:145], v[150:151], v[152:153]
	v_pk_add_f32 v[138:139], v[142:143], v[138:139]
	v_mul_f32_e32 v178, v44, v44
	v_mul_f32_e32 v182, v45, v45
	v_mul_f32_e32 v156, v40, v40
	v_mul_f32_e32 v158, v41, v41
	v_pk_add_f32 v[140:141], v[148:149], v[140:141]
	v_pk_add_f32 v[142:143], v[154:155], v[144:145]
	v_add_f32_e32 v137, v138, v139
	v_pk_add_f32 v[160:161], v[178:179], v[182:183]
	v_pk_add_f32 v[146:147], v[156:157], v[158:159]
	v_add_f32_e32 v138, v140, v141
	v_add_f32_e32 v139, v142, v143
	ds_bpermute_b32 v141, v129, v137
	v_pk_add_f32 v[144:145], v[160:161], v[146:147]
	ds_bpermute_b32 v142, v129, v138
	ds_bpermute_b32 v143, v129, v139
	v_add_f32_e32 v140, v144, v145
	ds_bpermute_b32 v144, v129, v140
	s_waitcnt lgkmcnt(3)
	v_add_f32_e32 v137, v137, v141
	s_waitcnt lgkmcnt(2)
	v_add_f32_e32 v138, v138, v142
	s_waitcnt lgkmcnt(1)
	v_add_f32_e32 v139, v139, v143
	ds_bpermute_b32 v141, v130, v137
	ds_bpermute_b32 v142, v130, v138
	ds_bpermute_b32 v143, v130, v139
	s_waitcnt lgkmcnt(3)
	v_add_f32_e32 v140, v140, v144
	ds_bpermute_b32 v144, v130, v140
	s_waitcnt lgkmcnt(3)
	v_add_f32_e32 v137, v137, v141
	s_waitcnt lgkmcnt(2)
	v_add_f32_e32 v138, v138, v142
	s_waitcnt lgkmcnt(1)
	v_add_f32_e32 v139, v139, v143
	ds_bpermute_b32 v141, v131, v137
	ds_bpermute_b32 v142, v131, v138
	ds_bpermute_b32 v143, v131, v139
	s_waitcnt lgkmcnt(3)
	v_add_f32_e32 v140, v140, v144
	ds_bpermute_b32 v144, v131, v140
	s_waitcnt lgkmcnt(3)
	v_add_f32_e32 v137, v137, v141
	s_waitcnt lgkmcnt(2)
	v_add_f32_e32 v138, v138, v142
	s_waitcnt lgkmcnt(1)
	v_add_f32_e32 v139, v139, v143
	ds_bpermute_b32 v141, v132, v137
	ds_bpermute_b32 v142, v132, v138
	ds_bpermute_b32 v143, v132, v139
	s_waitcnt lgkmcnt(3)
	v_add_f32_e32 v140, v140, v144
	ds_bpermute_b32 v144, v132, v140
	s_waitcnt lgkmcnt(3)
	v_add_f32_e32 v137, v137, v141
	s_waitcnt lgkmcnt(2)
	v_add_f32_e32 v138, v138, v142
	s_waitcnt lgkmcnt(1)
	v_add_f32_e32 v139, v139, v143
	ds_bpermute_b32 v141, v133, v137
	ds_bpermute_b32 v142, v133, v138
	ds_bpermute_b32 v143, v133, v139
	s_waitcnt lgkmcnt(3)
	v_add_f32_e32 v140, v140, v144
	ds_bpermute_b32 v144, v133, v140
	s_waitcnt lgkmcnt(3)
	v_add_f32_e32 v137, v137, v141
	s_waitcnt lgkmcnt(2)
	v_add_f32_e32 v138, v138, v142
	s_waitcnt lgkmcnt(1)
	v_add_f32_e32 v139, v139, v143
	ds_bpermute_b32 v141, v134, v137
	ds_bpermute_b32 v142, v134, v138
	ds_bpermute_b32 v143, v134, v139
	s_waitcnt lgkmcnt(3)
	v_add_f32_e32 v140, v140, v144
	ds_bpermute_b32 v144, v134, v140
	s_waitcnt lgkmcnt(3)
	v_add_f32_e32 v137, v137, v141
	s_waitcnt lgkmcnt(2)
	v_add_f32_e32 v138, v138, v142
	s_waitcnt lgkmcnt(1)
	v_add_f32_e32 v139, v139, v143
	v_fmamk_f32 v137, v137, 0x3a800000, v135
	v_fmamk_f32 v138, v138, 0x3a800000, v135
	v_fmamk_f32 v139, v139, 0x3a800000, v135
	v_mul_f32_e32 v141, 0x4f800000, v137
	v_cmp_gt_f32_e64 s[8:9], s31, v137
	s_waitcnt lgkmcnt(0)
	v_add_f32_e32 v140, v140, v144
	v_mul_f32_e32 v142, 0x4f800000, v138
	v_cmp_gt_f32_e32 vcc, s31, v138
	v_mul_f32_e32 v143, 0x4f800000, v139
	v_cmp_gt_f32_e64 s[0:1], s31, v139
	v_cndmask_b32_e64 v137, v137, v141, s[8:9]
	v_fmamk_f32 v140, v140, 0x3a800000, v135
	v_cndmask_b32_e32 v138, v138, v142, vcc
	v_cndmask_b32_e64 v139, v139, v143, s[0:1]
	v_sqrt_f32_e32 v141, v137
	v_mul_f32_e32 v144, 0x4f800000, v140
	v_cmp_gt_f32_e64 s[6:7], s31, v140
	v_sqrt_f32_e32 v142, v138
	v_sqrt_f32_e32 v143, v139
	v_cndmask_b32_e64 v140, v140, v144, s[6:7]
	v_sqrt_f32_e32 v144, v140
	v_add_u32_e32 v145, -1, v141
	v_add_u32_e32 v146, 1, v141
	v_add_u32_e32 v147, -1, v142
	v_add_u32_e32 v149, -1, v143
	v_fma_f32 v153, -v145, v141, v137
	v_add_u32_e32 v148, 1, v142
	v_add_u32_e32 v150, 1, v143
	v_fma_f32 v154, -v146, v141, v137
	v_fma_f32 v155, -v147, v142, v138
	v_fma_f32 v157, -v149, v143, v139
	v_cmp_ge_f32_e64 s[10:11], 0, v153
	v_add_u32_e32 v151, -1, v144
	v_fma_f32 v156, -v148, v142, v138
	v_fma_f32 v158, -v150, v143, v139
	v_cndmask_b32_e64 v141, v141, v145, s[10:11]
	v_cmp_ge_f32_e64 s[10:11], 0, v155
	v_cmp_ge_f32_e64 s[12:13], 0, v157
	v_cmp_lt_f32_e64 s[16:17], 0, v154
	v_add_u32_e32 v152, 1, v144
	v_fma_f32 v159, -v151, v144, v140
	v_cndmask_b32_e64 v142, v142, v147, s[10:11]
	v_cmp_lt_f32_e64 s[10:11], 0, v156
	v_cndmask_b32_e64 v143, v143, v149, s[12:13]
	v_cmp_lt_f32_e64 s[12:13], 0, v158
	v_cndmask_b32_e64 v141, v141, v146, s[16:17]
	v_fma_f32 v160, -v152, v144, v140
	v_cmp_ge_f32_e64 s[14:15], 0, v159
	v_cndmask_b32_e64 v142, v142, v148, s[10:11]
	v_cndmask_b32_e64 v143, v143, v150, s[12:13]
	v_mul_f32_e32 v145, 0x37800000, v141
	v_cndmask_b32_e64 v144, v144, v151, s[14:15]
	v_cmp_lt_f32_e64 s[14:15], 0, v160
	v_mul_f32_e32 v146, 0x37800000, v142
	v_mul_f32_e32 v147, 0x37800000, v143
	v_cndmask_b32_e64 v141, v141, v145, s[8:9]
	v_cmp_class_f32_e64 s[8:9], v137, v136
	v_cndmask_b32_e64 v144, v144, v152, s[14:15]
	v_cndmask_b32_e32 v142, v142, v146, vcc
	v_cmp_class_f32_e32 vcc, v138, v136
	v_cndmask_b32_e64 v143, v143, v147, s[0:1]
	v_cmp_class_f32_e64 s[0:1], v139, v136
	v_cndmask_b32_e64 v137, v141, v137, s[8:9]
	v_mul_f32_e32 v148, 0x37800000, v144
	v_cndmask_b32_e32 v141, v142, v138, vcc
	v_cndmask_b32_e64 v139, v143, v139, s[0:1]
	v_div_scale_f32 v138, s[0:1], v137, v137, 1.0
	v_cndmask_b32_e64 v144, v144, v148, s[6:7]
	v_cmp_class_f32_e64 s[6:7], v140, v136
	v_div_scale_f32 v142, s[0:1], v141, v141, 1.0
	v_rcp_f32_e32 v149, v138
	v_cndmask_b32_e64 v144, v144, v140, s[6:7]
	v_div_scale_f32 v145, s[6:7], v139, v139, 1.0
	v_rcp_f32_e32 v150, v142
	v_div_scale_f32 v147, s[8:9], v144, v144, 1.0
	v_rcp_f32_e32 v151, v145
	v_rcp_f32_e32 v152, v147
	v_fma_f32 v153, -v138, v149, 1.0
	v_div_scale_f32 v140, vcc, 1.0, v137, 1.0
	v_fma_f32 v154, -v142, v150, 1.0
	v_fmac_f32_e32 v149, v153, v149
	v_div_scale_f32 v143, s[0:1], 1.0, v141, 1.0
	v_fma_f32 v155, -v145, v151, 1.0
	v_fmac_f32_e32 v150, v154, v150
	v_mul_f32_e32 v153, v140, v149
	v_div_scale_f32 v146, s[6:7], 1.0, v139, 1.0
	v_fma_f32 v156, -v147, v152, 1.0
	v_fmac_f32_e32 v151, v155, v151
	v_mul_f32_e32 v154, v143, v150
	v_fma_f32 v157, -v138, v153, v140
	v_div_scale_f32 v148, s[8:9], 1.0, v144, 1.0
	v_fmac_f32_e32 v152, v156, v152
	v_mul_f32_e32 v155, v146, v151
	v_fma_f32 v158, -v142, v154, v143
	v_fmac_f32_e32 v153, v157, v149
	v_mul_f32_e32 v156, v148, v152
	v_fma_f32 v159, -v145, v155, v146
	v_fmac_f32_e32 v154, v158, v150
	v_fma_f32 v138, -v138, v153, v140
	v_fma_f32 v160, -v147, v156, v148
	v_fmac_f32_e32 v155, v159, v151
	v_fma_f32 v140, -v142, v154, v143
	v_div_fmas_f32 v138, v138, v149, v153
	s_mov_b64 vcc, s[0:1]
	v_fmac_f32_e32 v156, v160, v152
	v_fma_f32 v142, -v145, v155, v146
	v_div_fixup_f32 v138, v138, v137, 1.0
	v_div_fmas_f32 v137, v140, v150, v154
	s_mov_b64 vcc, s[6:7]
	v_fma_f32 v145, -v147, v156, v148
	v_pk_mul_f32 v[126:127], v[126:127], v[138:139] op_sel_hi:[1,0]
	v_pk_mul_f32 v[122:123], v[122:123], v[138:139] op_sel_hi:[1,0]
	v_pk_mul_f32 v[118:119], v[118:119], v[138:139] op_sel_hi:[1,0]
	v_pk_mul_f32 v[114:115], v[114:115], v[138:139] op_sel_hi:[1,0]
	v_pk_mul_f32 v[124:125], v[124:125], v[138:139] op_sel_hi:[1,0]
	v_pk_mul_f32 v[120:121], v[120:121], v[138:139] op_sel_hi:[1,0]
	v_pk_mul_f32 v[116:117], v[116:117], v[138:139] op_sel_hi:[1,0]
	v_pk_mul_f32 v[112:113], v[112:113], v[138:139] op_sel_hi:[1,0]
	v_div_fixup_f32 v138, v137, v141, 1.0
	v_div_fmas_f32 v137, v142, v151, v155
	s_mov_b64 vcc, s[8:9]
	v_pk_fma_f32 v[122:123], v[2:3], v[122:123], v[10:11]
	v_pk_fma_f32 v[126:127], v[0:1], v[126:127], v[8:9]
	v_pk_mul_f32 v[110:111], v[110:111], v[138:139] op_sel_hi:[1,0]
	v_pk_mul_f32 v[140:141], v[106:107], v[138:139] op_sel_hi:[1,0]
	v_pk_mul_f32 v[98:99], v[98:99], v[138:139] op_sel_hi:[1,0]
	v_pk_mul_f32 v[90:91], v[90:91], v[138:139] op_sel_hi:[1,0]
	v_pk_mul_f32 v[108:109], v[108:109], v[138:139] op_sel_hi:[1,0]
	v_pk_mul_f32 v[142:143], v[104:105], v[138:139] op_sel_hi:[1,0]
	v_pk_mul_f32 v[94:95], v[94:95], v[138:139] op_sel_hi:[1,0]
	v_pk_mul_f32 v[86:87], v[86:87], v[138:139] op_sel_hi:[1,0]
	v_div_fixup_f32 v138, v137, v139, 1.0
	v_div_fmas_f32 v137, v145, v152, v156
	v_pk_fma_f32 v[114:115], v[6:7], v[114:115], v[14:15]
	v_pk_fma_f32 v[118:119], v[4:5], v[118:119], v[12:13]
	v_pk_fma_f32 v[112:113], v[22:23], v[112:113], v[30:31]
	v_pk_fma_f32 v[116:117], v[20:21], v[116:117], v[28:29]
	v_cvt_pk_bf16_f32 v104, v118, v119
	v_cvt_pk_bf16_f32 v105, v114, v115
	v_cvt_pk_bf16_f32 v106, v126, v127
	v_cvt_pk_bf16_f32 v107, v122, v123
	v_pk_mul_f32 v[84:85], v[84:85], v[138:139] op_sel_hi:[1,0]
	v_pk_mul_f32 v[78:79], v[78:79], v[138:139] op_sel_hi:[1,0]
	v_pk_mul_f32 v[74:75], v[74:75], v[138:139] op_sel_hi:[1,0]
	v_pk_mul_f32 v[122:123], v[50:51], v[138:139] op_sel_hi:[1,0]
	v_pk_mul_f32 v[82:83], v[82:83], v[138:139] op_sel_hi:[1,0]
	v_pk_mul_f32 v[76:77], v[76:77], v[138:139] op_sel_hi:[1,0]
	v_pk_mul_f32 v[72:73], v[72:73], v[138:139] op_sel_hi:[1,0]
	v_pk_mul_f32 v[126:127], v[48:49], v[138:139] op_sel_hi:[1,0]
	v_div_fixup_f32 v138, v137, v144, 1.0
	v_pk_fma_f32 v[120:121], v[18:19], v[120:121], v[26:27]
	v_pk_fma_f32 v[124:125], v[16:17], v[124:125], v[24:25]
	v_pk_fma_f32 v[114:115], v[2:3], v[140:141], v[10:11]
	v_pk_fma_f32 v[110:111], v[0:1], v[110:111], v[8:9]
	v_pk_fma_f32 v[90:91], v[6:7], v[90:91], v[14:15]
	v_pk_fma_f32 v[98:99], v[4:5], v[98:99], v[12:13]
	global_store_dwordx4 v[92:93], v[104:107], off offset:-3072 sc1
	v_cvt_pk_bf16_f32 v48, v116, v117
	v_cvt_pk_bf16_f32 v49, v112, v113
	v_cvt_pk_bf16_f32 v50, v124, v125
	v_cvt_pk_bf16_f32 v51, v120, v121
	v_pk_mul_f32 v[112:113], v[34:35], v[138:139] op_sel_hi:[1,0]
	v_pk_mul_f32 v[116:117], v[32:33], v[138:139] op_sel_hi:[1,0]
	global_store_dwordx4 v[92:93], v[48:51], off offset:-2048 sc1
	v_cvt_pk_bf16_f32 v32, v98, v99
	v_cvt_pk_bf16_f32 v33, v90, v91
	v_cvt_pk_bf16_f32 v34, v110, v111
	v_cvt_pk_bf16_f32 v35, v114, v115
	v_pk_fma_f32 v[118:119], v[18:19], v[142:143], v[26:27]
	v_pk_fma_f32 v[108:109], v[16:17], v[108:109], v[24:25]
	v_pk_fma_f32 v[86:87], v[22:23], v[86:87], v[30:31]
	v_pk_fma_f32 v[94:95], v[20:21], v[94:95], v[28:29]
	global_store_dwordx4 v[92:93], v[32:35], off offset:-1024 sc1
	v_pk_fma_f32 v[78:79], v[2:3], v[78:79], v[10:11]
	v_pk_fma_f32 v[84:85], v[0:1], v[84:85], v[8:9]
	v_cvt_pk_bf16_f32 v32, v94, v95
	v_cvt_pk_bf16_f32 v33, v86, v87
	v_cvt_pk_bf16_f32 v34, v108, v109
	v_cvt_pk_bf16_f32 v35, v118, v119
	v_pk_fma_f32 v[104:105], v[6:7], v[122:123], v[14:15]
	v_pk_fma_f32 v[74:75], v[4:5], v[74:75], v[12:13]
	global_store_dwordx4 v[100:101], v[32:35], off offset:-4096 sc1
	v_pk_fma_f32 v[76:77], v[18:19], v[76:77], v[26:27]
	v_pk_fma_f32 v[82:83], v[16:17], v[82:83], v[24:25]
	v_cvt_pk_bf16_f32 v32, v74, v75
	v_cvt_pk_bf16_f32 v33, v104, v105
	v_cvt_pk_bf16_f32 v34, v84, v85
	v_cvt_pk_bf16_f32 v35, v78, v79
	v_pk_fma_f32 v[106:107], v[22:23], v[126:127], v[30:31]
	v_pk_fma_f32 v[72:73], v[20:21], v[72:73], v[28:29]
	v_pk_mul_f32 v[46:47], v[46:47], v[138:139] op_sel_hi:[1,0]
	v_pk_mul_f32 v[42:43], v[42:43], v[138:139] op_sel_hi:[1,0]
	v_pk_mul_f32 v[38:39], v[38:39], v[138:139] op_sel_hi:[1,0]
	global_store_dwordx4 v[100:101], v[32:35], off offset:-3072 sc1
	v_pk_mul_f32 v[44:45], v[44:45], v[138:139] op_sel_hi:[1,0]
	v_pk_mul_f32 v[40:41], v[40:41], v[138:139] op_sel_hi:[1,0]
	v_cvt_pk_bf16_f32 v32, v72, v73
	v_cvt_pk_bf16_f32 v33, v106, v107
	v_cvt_pk_bf16_f32 v34, v82, v83
	v_cvt_pk_bf16_f32 v35, v76, v77
	v_pk_mul_f32 v[36:37], v[36:37], v[138:139] op_sel_hi:[1,0]
	v_pk_fma_f32 v[42:43], v[2:3], v[42:43], v[10:11]
	v_pk_fma_f32 v[46:47], v[0:1], v[46:47], v[8:9]
	v_pk_fma_f32 v[48:49], v[6:7], v[112:113], v[14:15]
	v_pk_fma_f32 v[38:39], v[4:5], v[38:39], v[12:13]
	global_store_dwordx4 v[100:101], v[32:35], off offset:-2048 sc1
	s_mov_b64 vcc, s[4:5]
	v_pk_fma_f32 v[40:41], v[18:19], v[40:41], v[26:27]
	v_cvt_pk_bf16_f32 v32, v38, v39
	v_cvt_pk_bf16_f32 v33, v48, v49
	v_cvt_pk_bf16_f32 v34, v46, v47
	v_cvt_pk_bf16_f32 v35, v42, v43
	v_pk_fma_f32 v[44:45], v[16:17], v[44:45], v[24:25]
	v_pk_fma_f32 v[50:51], v[22:23], v[116:117], v[30:31]
	v_pk_fma_f32 v[36:37], v[20:21], v[36:37], v[28:29]
	global_store_dwordx4 v[100:101], v[32:35], off offset:-1024 sc1
	s_nop 1
	v_cvt_pk_bf16_f32 v32, v36, v37
	v_cvt_pk_bf16_f32 v33, v50, v51
	v_cvt_pk_bf16_f32 v34, v44, v45
	v_cvt_pk_bf16_f32 v35, v40, v41
	global_store_dwordx4 v[100:101], v[32:35], off sc1
	s_cbranch_vccnz .LBB0_2750

.LBB0_3498:
	s_waitcnt vmcnt(0)
	v_lshlrev_b32_e32 v62, 2, v44
	v_add_co_u32_e32 v44, vcc, s27, v82
	v_ashrrev_i32_e32 v55, 31, v45
	v_mov_b32_e32 v54, v45
	v_addc_co_u32_e32 v45, vcc, -1, v83, vcc
	v_lshlrev_b32_e32 v64, 2, v40
	v_add_co_u32_e32 v40, vcc, s29, v82
	s_add_i32 s5, s28, s22
	v_lshlrev_b32_e32 v63, 2, v46
	v_ashrrev_i32_e32 v57, 31, v47
	v_mov_b32_e32 v56, v47
	v_ashrrev_i32_e32 v47, 31, v41
	v_mov_b32_e32 v46, v41
	v_lshlrev_b32_e32 v65, 2, v42
	v_ashrrev_i32_e32 v59, 31, v43
	v_mov_b32_e32 v58, v43
	v_addc_co_u32_e32 v41, vcc, -1, v83, vcc
	v_lshlrev_b32_e32 v66, 2, v36
	v_ashrrev_i32_e32 v43, 31, v37
	v_mov_b32_e32 v42, v37
	v_lshlrev_b32_e32 v67, 2, v38
	v_ashrrev_i32_e32 v37, 31, v39
	v_mov_b32_e32 v36, v39
	v_lshlrev_b32_e32 v85, 2, v32
	v_ashrrev_i32_e32 v39, 31, v33
	v_mov_b32_e32 v38, v33
	v_lshlrev_b32_e32 v34, 2, v34
	v_ashrrev_i32_e32 v33, 31, v35
	v_mov_b32_e32 v32, v35
	v_add_u32_e32 v35, s23, v62
	s_cmp_lt_i32 s5, 0x8000
	v_mul_f32_e32 v84, 0x3d000000, v60
	v_mul_f32_e32 v86, 0x3d000000, v61
	v_mul_f32_e32 v88, 0x3d000000, v52
	v_mul_f32_e32 v90, 0x3d000000, v53
	v_mul_f32_e32 v92, 0x3d000000, v50
	v_mul_f32_e32 v94, 0x3d000000, v51
	v_mul_f32_e32 v98, 0x3d000000, v48
	v_mul_f32_e32 v100, 0x3d000000, v49
	v_lshlrev_b64 v[102:103], 10, v[54:55]
	v_add_u32_e32 v87, s23, v63
	v_lshlrev_b64 v[104:105], 10, v[56:57]
	global_load_dwordx4 v[76:79], v[44:45], off offset:-3072
	global_load_dwordx4 v[72:75], v[44:45], off offset:-2048
	v_add_u32_e32 v89, s23, v64
	v_lshlrev_b64 v[106:107], 10, v[46:47]
	v_add_u32_e32 v47, s23, v65
	v_lshlrev_b64 v[108:109], 10, v[58:59]
	global_load_dwordx4 v[68:71], v[44:45], off offset:-1024
	v_add_u32_e32 v45, s23, v66
	v_lshlrev_b64 v[110:111], 10, v[42:43]
	v_add_u32_e32 v43, s23, v67
	v_lshlrev_b64 v[112:113], 10, v[36:37]
	global_load_dwordx4 v[64:67], v[40:41], off offset:-4096
	global_load_dwordx4 v[60:63], v[40:41], off offset:-3072
	v_add_u32_e32 v37, s23, v85
	v_lshlrev_b64 v[114:115], 10, v[38:39]
	v_add_u32_e32 v39, s23, v34
	v_lshlrev_b64 v[116:117], 10, v[32:33]
	global_load_dwordx4 v[56:59], v[40:41], off offset:-2048
	global_load_dwordx4 v[52:55], v[40:41], off offset:-1024
	global_load_dwordx4 v[48:51], v[40:41], off
	ds_read_b32 v46, v35
	ds_read_b32 v44, v87
	ds_read_b32 v42, v89
	ds_read_b32 v40, v47
	ds_read_b32 v38, v45
	ds_read_b32 v36, v43
	ds_read_b32 v34, v37
	ds_read_b32 v32, v39
	s_cselect_b64 s[0:1], -1, 0
	s_and_b64 s[6:7], s[0:1], exec
	s_cselect_b32 s4, s5, s28
	s_mov_b32 s28, s5
	s_ashr_i32 s5, s4, 31
	s_lshl_b64 s[4:5], s[4:5], 5
	s_waitcnt lgkmcnt(7)
	v_ashrrev_i32_e32 v47, 31, v46
	s_waitcnt lgkmcnt(6)
	v_ashrrev_i32_e32 v45, 31, v44
	s_waitcnt lgkmcnt(5)
	v_ashrrev_i32_e32 v43, 31, v42
	s_waitcnt lgkmcnt(4)
	v_ashrrev_i32_e32 v41, 31, v40
	s_waitcnt lgkmcnt(3)
	v_ashrrev_i32_e32 v39, 31, v38
	s_waitcnt lgkmcnt(2)
	v_ashrrev_i32_e32 v37, 31, v36
	s_waitcnt lgkmcnt(1)
	v_ashrrev_i32_e32 v35, 31, v34
	s_waitcnt lgkmcnt(0)
	v_ashrrev_i32_e32 v33, 31, v32
	s_add_u32 s6, s34, s4
	v_lshlrev_b64 v[46:47], 18, v[46:47]
	v_lshlrev_b64 v[44:45], 18, v[44:45]
	v_lshlrev_b64 v[42:43], 18, v[42:43]
	v_lshlrev_b64 v[40:41], 18, v[40:41]
	v_lshlrev_b64 v[38:39], 18, v[38:39]
	v_lshlrev_b64 v[36:37], 18, v[36:37]
	v_lshlrev_b64 v[34:35], 18, v[34:35]
	v_lshlrev_b64 v[32:33], 18, v[32:33]
	s_addc_u32 s7, s35, s5
	v_lshl_add_u64 v[118:119], s[86:87], 0, v[46:47]
	v_lshl_add_u64 v[120:121], s[86:87], 0, v[44:45]
	v_lshl_add_u64 v[122:123], s[86:87], 0, v[42:43]
	v_lshl_add_u64 v[124:125], s[86:87], 0, v[40:41]
	v_lshl_add_u64 v[136:137], s[86:87], 0, v[38:39]
	v_lshl_add_u64 v[138:139], s[86:87], 0, v[36:37]
	v_lshl_add_u64 v[140:141], s[86:87], 0, v[34:35]
	v_lshl_add_u64 v[142:143], s[86:87], 0, v[32:33]
	global_load_dwordx2 v[144:145], v126, s[6:7] offset:16
	global_load_dwordx4 v[44:47], v126, s[6:7]
	global_load_dwordx2 v[146:147], v126, s[6:7] offset:48
	global_load_dwordx4 v[40:43], v126, s[6:7] offset:32
	global_load_dwordx2 v[148:149], v126, s[6:7] offset:80
	global_load_dwordx4 v[36:39], v126, s[6:7] offset:64
	global_load_dwordx2 v[150:151], v126, s[6:7] offset:112
	global_load_dwordx4 v[32:35], v126, s[6:7] offset:96
	v_lshl_add_u64 v[102:103], v[118:119], 0, v[102:103]
	v_lshl_add_u64 v[104:105], v[120:121], 0, v[104:105]
	v_lshl_add_u64 v[106:107], v[122:123], 0, v[106:107]
	v_lshl_add_u64 v[108:109], v[124:125], 0, v[108:109]
	v_lshl_add_u64 v[110:111], v[136:137], 0, v[110:111]
	v_lshl_add_u64 v[112:113], v[138:139], 0, v[112:113]
	v_lshl_add_u64 v[114:115], v[140:141], 0, v[114:115]
	v_lshl_add_u64 v[116:117], v[142:143], 0, v[116:117]
	v_lshl_add_u64 v[102:103], v[102:103], 0, v[80:81]
	v_lshl_add_u64 v[104:105], v[104:105], 0, v[80:81]
	v_lshl_add_u64 v[106:107], v[106:107], 0, v[80:81]
	v_lshl_add_u64 v[108:109], v[108:109], 0, v[80:81]
	v_lshl_add_u64 v[110:111], v[110:111], 0, v[80:81]
	v_lshl_add_u64 v[112:113], v[112:113], 0, v[80:81]
	v_lshl_add_u64 v[114:115], v[114:115], 0, v[80:81]
	v_lshl_add_u64 v[116:117], v[116:117], 0, v[80:81]
	global_load_dwordx2 v[118:119], v[102:103], off nt
	global_load_dwordx2 v[120:121], v[104:105], off nt
	s_nop 0
	global_load_dwordx2 v[104:105], v[104:105], off offset:512 nt
	s_nop 0
	global_load_dwordx2 v[102:103], v[102:103], off offset:512 nt
	s_nop 0
	global_load_dwordx2 v[122:123], v[106:107], off nt
	global_load_dwordx2 v[124:125], v[108:109], off nt
	s_nop 0
	global_load_dwordx2 v[108:109], v[108:109], off offset:512 nt
	s_nop 0
	global_load_dwordx2 v[106:107], v[106:107], off offset:512 nt
	s_nop 0
	global_load_dwordx2 v[136:137], v[110:111], off nt
	global_load_dwordx2 v[138:139], v[112:113], off nt
	s_nop 0
	global_load_dwordx2 v[112:113], v[112:113], off offset:512 nt
	s_nop 0
	global_load_dwordx2 v[110:111], v[110:111], off offset:512 nt
	s_nop 0
	global_load_dwordx2 v[140:141], v[114:115], off nt
	global_load_dwordx2 v[142:143], v[116:117], off nt
	s_nop 0
	global_load_dwordx2 v[116:117], v[116:117], off offset:512 nt
	s_nop 0
	global_load_dwordx2 v[114:115], v[114:115], off offset:512 nt
	v_add_co_u32_e32 v96, vcc, s31, v82
	s_and_b64 s[4:5], s[0:1], exec
	s_nop 0
	v_addc_co_u32_e32 v97, vcc, -1, v83, vcc
	s_waitcnt vmcnt(31)
	v_lshlrev_b32_e32 v152, 16, v76
	v_and_b32_e32 v153, 0xffff0000, v76
	v_lshlrev_b32_e32 v76, 16, v77
	v_and_b32_e32 v77, 0xffff0000, v77
	v_lshlrev_b32_e32 v154, 16, v78
	v_and_b32_e32 v155, 0xffff0000, v78
	v_lshlrev_b32_e32 v78, 16, v79
	v_and_b32_e32 v79, 0xffff0000, v79
	s_waitcnt vmcnt(30)
	v_lshlrev_b32_e32 v156, 16, v72
	v_and_b32_e32 v157, 0xffff0000, v72
	v_lshlrev_b32_e32 v72, 16, v73
	s_waitcnt vmcnt(27)
	v_lshlrev_b32_e32 v168, 16, v60
	v_and_b32_e32 v169, 0xffff0000, v60
	v_lshlrev_b32_e32 v170, 16, v61
	v_and_b32_e32 v171, 0xffff0000, v61
	s_waitcnt vmcnt(25)
	v_lshlrev_b32_e32 v178, 16, v52
	s_waitcnt vmcnt(24)
	v_lshlrev_b32_e32 v184, 16, v48
	v_and_b32_e32 v185, 0xffff0000, v48
	v_lshlrev_b32_e32 v186, 16, v49
	v_and_b32_e32 v187, 0xffff0000, v49
	v_and_b32_e32 v179, 0xffff0000, v52
	v_lshlrev_b32_e32 v180, 16, v53
	v_and_b32_e32 v181, 0xffff0000, v53
	v_lshlrev_b32_e32 v188, 16, v50
	v_and_b32_e32 v189, 0xffff0000, v50
	v_lshlrev_b32_e32 v190, 16, v51
	v_and_b32_e32 v191, 0xffff0000, v51
	v_and_b32_e32 v73, 0xffff0000, v73
	v_lshlrev_b32_e32 v158, 16, v74
	v_and_b32_e32 v159, 0xffff0000, v74
	v_lshlrev_b32_e32 v74, 16, v75
	v_and_b32_e32 v75, 0xffff0000, v75
	v_lshlrev_b32_e32 v160, 16, v68
	v_and_b32_e32 v161, 0xffff0000, v68
	v_lshlrev_b32_e32 v68, 16, v69
	v_and_b32_e32 v69, 0xffff0000, v69
	v_lshlrev_b32_e32 v162, 16, v70
	v_and_b32_e32 v163, 0xffff0000, v70
	v_lshlrev_b32_e32 v70, 16, v71
	v_and_b32_e32 v71, 0xffff0000, v71
	v_lshlrev_b32_e32 v164, 16, v64
	v_and_b32_e32 v165, 0xffff0000, v64
	v_lshlrev_b32_e32 v64, 16, v65
	s_waitcnt vmcnt(23)
	v_mov_b64_e32 v[60:61], v[144:145]
	v_and_b32_e32 v65, 0xffff0000, v65
	s_waitcnt vmcnt(21)
	v_mov_b64_e32 v[52:53], v[146:147]
	v_lshlrev_b32_e32 v166, 16, v66
	s_waitcnt vmcnt(19)
	v_mov_b64_e32 v[50:51], v[148:149]
	v_and_b32_e32 v167, 0xffff0000, v66
	s_waitcnt vmcnt(17)
	v_mov_b64_e32 v[48:49], v[150:151]
	v_lshlrev_b32_e32 v66, 16, v67
	v_and_b32_e32 v67, 0xffff0000, v67
	s_waitcnt vmcnt(15)
	v_cvt_pk_f32_fp8_e32 v[144:145], v118
	s_waitcnt vmcnt(14)
	v_cvt_pk_f32_fp8_e32 v[150:151], v120
	v_cvt_pk_f32_fp8_sdwa v[192:193], v120 src0_sel:WORD_1
	v_cvt_pk_f32_fp8_e32 v[194:195], v121
	v_cvt_pk_f32_fp8_sdwa v[120:121], v121 src0_sel:WORD_1
	s_waitcnt vmcnt(13)
	v_cvt_pk_f32_fp8_e32 v[202:203], v104
	v_cvt_pk_f32_fp8_sdwa v[204:205], v104 src0_sel:WORD_1
	v_cvt_pk_f32_fp8_e32 v[206:207], v105
	v_cvt_pk_f32_fp8_sdwa v[104:105], v105 src0_sel:WORD_1
	v_pk_mul_f32 v[150:151], v[86:87], v[150:151] op_sel_hi:[0,1]
	v_cvt_pk_f32_fp8_sdwa v[146:147], v118 src0_sel:WORD_1
	v_cvt_pk_f32_fp8_e32 v[148:149], v119
	v_cvt_pk_f32_fp8_sdwa v[118:119], v119 src0_sel:WORD_1
	s_waitcnt vmcnt(12)
	v_cvt_pk_f32_fp8_e32 v[196:197], v102
	v_cvt_pk_f32_fp8_sdwa v[198:199], v102 src0_sel:WORD_1
	v_cvt_pk_f32_fp8_e32 v[200:201], v103
	v_cvt_pk_f32_fp8_sdwa v[102:103], v103 src0_sel:WORD_1
	s_waitcnt vmcnt(10)
	v_cvt_pk_f32_fp8_e32 v[214:215], v124
	v_cvt_pk_f32_fp8_sdwa v[216:217], v124 src0_sel:WORD_1
	v_cvt_pk_f32_fp8_e32 v[218:219], v125
	v_cvt_pk_f32_fp8_sdwa v[124:125], v125 src0_sel:WORD_1
	s_waitcnt vmcnt(9)
	v_cvt_pk_f32_fp8_e32 v[226:227], v108
	v_cvt_pk_f32_fp8_sdwa v[228:229], v108 src0_sel:WORD_1
	v_cvt_pk_f32_fp8_e32 v[230:231], v109
	v_cvt_pk_f32_fp8_sdwa v[108:109], v109 src0_sel:WORD_1
	s_waitcnt vmcnt(6)
	v_cvt_pk_f32_fp8_e32 v[238:239], v138
	v_cvt_pk_f32_fp8_sdwa v[240:241], v138 src0_sel:WORD_1
	v_cvt_pk_f32_fp8_e32 v[242:243], v139
	v_cvt_pk_f32_fp8_sdwa v[138:139], v139 src0_sel:WORD_1
	s_waitcnt vmcnt(5)
	v_cvt_pk_f32_fp8_e32 v[250:251], v112
	v_pk_mul_f32 v[192:193], v[86:87], v[192:193] op_sel_hi:[0,1]
	v_pk_mul_f32 v[120:121], v[86:87], v[120:121] op_sel_hi:[0,1]
	v_pk_mul_f32 v[194:195], v[86:87], v[194:195] op_sel_hi:[0,1]
	v_pk_mul_f32 v[204:205], v[86:87], v[204:205] op_sel_hi:[0,1]
	v_pk_mul_f32 v[202:203], v[86:87], v[202:203] op_sel_hi:[0,1]
	v_pk_mul_f32 v[104:105], v[86:87], v[104:105] op_sel_hi:[0,1]
	v_pk_mul_f32 v[86:87], v[86:87], v[206:207] op_sel_hi:[0,1]
	v_cvt_pk_f32_fp8_sdwa v[206:207], v112 src0_sel:WORD_1
	v_pk_fma_f32 v[144:145], v[84:85], v[144:145], v[150:151] op_sel_hi:[0,1,1]
	v_cvt_pk_f32_fp8_e32 v[150:151], v113
	v_cvt_pk_f32_fp8_sdwa v[112:113], v113 src0_sel:WORD_1
	v_cvt_pk_f32_fp8_e32 v[208:209], v122
	v_pk_fma_f32 v[146:147], v[84:85], v[146:147], v[192:193] op_sel_hi:[0,1,1]
	v_pk_fma_f32 v[148:149], v[84:85], v[148:149], v[194:195] op_sel_hi:[0,1,1]
	v_pk_fma_f32 v[118:119], v[84:85], v[118:119], v[120:121] op_sel_hi:[0,1,1]
	v_pk_fma_f32 v[196:197], v[84:85], v[196:197], v[202:203] op_sel_hi:[0,1,1]
	s_waitcnt vmcnt(2)
	v_cvt_pk_f32_fp8_e32 v[202:203], v142
	v_pk_fma_f32 v[198:199], v[84:85], v[198:199], v[204:205] op_sel_hi:[0,1,1]
	v_cvt_pk_f32_fp8_sdwa v[204:205], v142 src0_sel:WORD_1
	v_pk_fma_f32 v[86:87], v[84:85], v[200:201], v[86:87] op_sel_hi:[0,1,1]
	v_cvt_pk_f32_fp8_e32 v[200:201], v143
	v_cvt_pk_f32_fp8_sdwa v[142:143], v143 src0_sel:WORD_1
	v_pk_fma_f32 v[84:85], v[84:85], v[102:103], v[104:105] op_sel_hi:[0,1,1]
	s_waitcnt vmcnt(1)
	v_cvt_pk_f32_fp8_e32 v[104:105], v116
	v_pk_mul_f32 v[216:217], v[90:91], v[216:217] op_sel_hi:[0,1]
	v_pk_mul_f32 v[214:215], v[90:91], v[214:215] op_sel_hi:[0,1]
	v_pk_mul_f32 v[124:125], v[90:91], v[124:125] op_sel_hi:[0,1]
	v_pk_mul_f32 v[218:219], v[90:91], v[218:219] op_sel_hi:[0,1]
	v_pk_mul_f32 v[228:229], v[90:91], v[228:229] op_sel_hi:[0,1]
	v_pk_mul_f32 v[226:227], v[90:91], v[226:227] op_sel_hi:[0,1]
	v_pk_mul_f32 v[108:109], v[90:91], v[108:109] op_sel_hi:[0,1]
	v_pk_mul_f32 v[90:91], v[90:91], v[230:231] op_sel_hi:[0,1]
	v_cvt_pk_f32_fp8_sdwa v[230:231], v116 src0_sel:WORD_1
	v_pk_mul_f32 v[240:241], v[94:95], v[240:241] op_sel_hi:[0,1]
	v_pk_mul_f32 v[238:239], v[94:95], v[238:239] op_sel_hi:[0,1]
	v_pk_mul_f32 v[138:139], v[94:95], v[138:139] op_sel_hi:[0,1]
	v_pk_mul_f32 v[242:243], v[94:95], v[242:243] op_sel_hi:[0,1]
	v_pk_mul_f32 v[206:207], v[94:95], v[206:207] op_sel_hi:[0,1]
	v_pk_mul_f32 v[250:251], v[94:95], v[250:251] op_sel_hi:[0,1]
	v_pk_mul_f32 v[112:113], v[94:95], v[112:113] op_sel_hi:[0,1]
	v_pk_mul_f32 v[94:95], v[94:95], v[150:151] op_sel_hi:[0,1]
	v_cvt_pk_f32_fp8_e32 v[150:151], v117
	v_cvt_pk_f32_fp8_sdwa v[116:117], v117 src0_sel:WORD_1
	v_cvt_pk_f32_fp8_sdwa v[210:211], v122 src0_sel:WORD_1
	v_cvt_pk_f32_fp8_e32 v[212:213], v123
	v_cvt_pk_f32_fp8_sdwa v[122:123], v123 src0_sel:WORD_1
	v_cvt_pk_f32_fp8_e32 v[220:221], v106
	v_cvt_pk_f32_fp8_sdwa v[222:223], v106 src0_sel:WORD_1
	v_cvt_pk_f32_fp8_e32 v[224:225], v107
	v_cvt_pk_f32_fp8_sdwa v[106:107], v107 src0_sel:WORD_1
	v_cvt_pk_f32_fp8_e32 v[232:233], v136
	v_cvt_pk_f32_fp8_sdwa v[234:235], v136 src0_sel:WORD_1
	v_cvt_pk_f32_fp8_e32 v[236:237], v137
	v_cvt_pk_f32_fp8_sdwa v[136:137], v137 src0_sel:WORD_1
	v_cvt_pk_f32_fp8_e32 v[244:245], v110
	v_cvt_pk_f32_fp8_sdwa v[246:247], v110 src0_sel:WORD_1
	v_cvt_pk_f32_fp8_e32 v[248:249], v111
	v_cvt_pk_f32_fp8_sdwa v[110:111], v111 src0_sel:WORD_1
	v_cvt_pk_f32_fp8_e32 v[192:193], v140
	v_cvt_pk_f32_fp8_sdwa v[194:195], v140 src0_sel:WORD_1
	v_cvt_pk_f32_fp8_e32 v[120:121], v141
	v_cvt_pk_f32_fp8_sdwa v[140:141], v141 src0_sel:WORD_1
	s_waitcnt vmcnt(0)
	v_cvt_pk_f32_fp8_e32 v[102:103], v114
	v_pk_mul_f32 v[204:205], v[100:101], v[204:205] op_sel_hi:[0,1]
	v_pk_mul_f32 v[202:203], v[100:101], v[202:203] op_sel_hi:[0,1]
	v_pk_mul_f32 v[142:143], v[100:101], v[142:143] op_sel_hi:[0,1]
	v_pk_mul_f32 v[200:201], v[100:101], v[200:201] op_sel_hi:[0,1]
	v_pk_mul_f32 v[230:231], v[100:101], v[230:231] op_sel_hi:[0,1]
	v_pk_mul_f32 v[104:105], v[100:101], v[104:105] op_sel_hi:[0,1]
	v_pk_mul_f32 v[116:117], v[100:101], v[116:117] op_sel_hi:[0,1]
	v_pk_mul_f32 v[100:101], v[100:101], v[150:151] op_sel_hi:[0,1]
	v_cvt_pk_f32_fp8_sdwa v[150:151], v114 src0_sel:WORD_1
	v_pk_fma_f32 v[208:209], v[88:89], v[208:209], v[214:215] op_sel_hi:[0,1,1]
	v_cvt_pk_f32_fp8_e32 v[214:215], v115
	v_cvt_pk_f32_fp8_sdwa v[114:115], v115 src0_sel:WORD_1
	v_lshlrev_b32_e32 v172, 16, v62
	v_and_b32_e32 v173, 0xffff0000, v62
	v_lshlrev_b32_e32 v62, 16, v63
	v_and_b32_e32 v63, 0xffff0000, v63
	v_lshlrev_b32_e32 v174, 16, v56
	v_and_b32_e32 v175, 0xffff0000, v56
	v_lshlrev_b32_e32 v56, 16, v57
	v_and_b32_e32 v57, 0xffff0000, v57
	v_lshlrev_b32_e32 v176, 16, v58
	v_and_b32_e32 v177, 0xffff0000, v58
	v_lshlrev_b32_e32 v58, 16, v59
	v_and_b32_e32 v59, 0xffff0000, v59
	v_lshlrev_b32_e32 v182, 16, v54
	v_and_b32_e32 v183, 0xffff0000, v54
	v_lshlrev_b32_e32 v54, 16, v55
	v_and_b32_e32 v55, 0xffff0000, v55
	v_pk_fma_f32 v[210:211], v[88:89], v[210:211], v[216:217] op_sel_hi:[0,1,1]
	v_pk_fma_f32 v[212:213], v[88:89], v[212:213], v[218:219] op_sel_hi:[0,1,1]
	v_pk_fma_f32 v[216:217], v[88:89], v[122:123], v[124:125] op_sel_hi:[0,1,1]
	v_pk_fma_f32 v[218:219], v[88:89], v[220:221], v[226:227] op_sel_hi:[0,1,1]
	v_pk_fma_f32 v[220:221], v[88:89], v[222:223], v[228:229] op_sel_hi:[0,1,1]
	v_pk_fma_f32 v[90:91], v[88:89], v[224:225], v[90:91] op_sel_hi:[0,1,1]
	v_pk_fma_f32 v[88:89], v[88:89], v[106:107], v[108:109] op_sel_hi:[0,1,1]
	v_pk_fma_f32 v[222:223], v[92:93], v[232:233], v[238:239] op_sel_hi:[0,1,1]
	v_pk_fma_f32 v[224:225], v[92:93], v[234:235], v[240:241] op_sel_hi:[0,1,1]
	v_pk_fma_f32 v[226:227], v[92:93], v[236:237], v[242:243] op_sel_hi:[0,1,1]
	v_pk_fma_f32 v[136:137], v[92:93], v[136:137], v[138:139] op_sel_hi:[0,1,1]
	v_pk_fma_f32 v[138:139], v[92:93], v[244:245], v[250:251] op_sel_hi:[0,1,1]
	v_pk_fma_f32 v[206:207], v[92:93], v[246:247], v[206:207] op_sel_hi:[0,1,1]
	v_pk_fma_f32 v[228:229], v[92:93], v[248:249], v[94:95] op_sel_hi:[0,1,1]
	v_pk_fma_f32 v[232:233], v[92:93], v[110:111], v[112:113] op_sel_hi:[0,1,1]
	v_pk_fma_f32 v[192:193], v[98:99], v[192:193], v[202:203] op_sel_hi:[0,1,1]
	v_pk_fma_f32 v[194:195], v[98:99], v[194:195], v[204:205] op_sel_hi:[0,1,1]
	v_pk_fma_f32 v[200:201], v[98:99], v[120:121], v[200:201] op_sel_hi:[0,1,1]
	v_pk_fma_f32 v[140:141], v[98:99], v[140:141], v[142:143] op_sel_hi:[0,1,1]
	v_pk_fma_f32 v[142:143], v[98:99], v[102:103], v[104:105] op_sel_hi:[0,1,1]
	v_pk_fma_f32 v[150:151], v[98:99], v[150:151], v[230:231] op_sel_hi:[0,1,1]
	v_pk_fma_f32 v[202:203], v[98:99], v[214:215], v[100:101] op_sel_hi:[0,1,1]
	v_pk_fma_f32 v[204:205], v[98:99], v[114:115], v[116:117] op_sel_hi:[0,1,1]
	v_pk_fma_f32 v[112:113], v[76:77], s[26:27], v[146:147] op_sel_hi:[1,0,1]
	v_pk_fma_f32 v[116:117], v[152:153], s[26:27], v[144:145] op_sel_hi:[1,0,1]
	v_pk_fma_f32 v[120:121], v[78:79], s[26:27], v[118:119] op_sel_hi:[1,0,1]
	v_pk_fma_f32 v[124:125], v[154:155], s[26:27], v[148:149] op_sel_hi:[1,0,1]
	v_pk_fma_f32 v[110:111], v[72:73], s[26:27], v[198:199] op_sel_hi:[1,0,1]
	v_pk_fma_f32 v[114:115], v[156:157], s[26:27], v[196:197] op_sel_hi:[1,0,1]
	v_pk_fma_f32 v[118:119], v[74:75], s[26:27], v[84:85] op_sel_hi:[1,0,1]
	v_pk_fma_f32 v[122:123], v[158:159], s[26:27], v[86:87] op_sel_hi:[1,0,1]
	v_pk_fma_f32 v[94:95], v[68:69], s[26:27], v[210:211] op_sel_hi:[1,0,1]
	v_pk_fma_f32 v[100:101], v[160:161], s[26:27], v[208:209] op_sel_hi:[1,0,1]
	v_pk_fma_f32 v[104:105], v[70:71], s[26:27], v[216:217] op_sel_hi:[1,0,1]
	v_pk_fma_f32 v[108:109], v[162:163], s[26:27], v[212:213] op_sel_hi:[1,0,1]
	v_pk_fma_f32 v[92:93], v[64:65], s[26:27], v[220:221] op_sel_hi:[1,0,1]
	v_pk_fma_f32 v[98:99], v[164:165], s[26:27], v[218:219] op_sel_hi:[1,0,1]
	v_pk_fma_f32 v[102:103], v[66:67], s[26:27], v[88:89] op_sel_hi:[1,0,1]
	v_pk_fma_f32 v[106:107], v[166:167], s[26:27], v[90:91] op_sel_hi:[1,0,1]
	v_pk_fma_f32 v[74:75], v[170:171], s[26:27], v[224:225] op_sel_hi:[1,0,1]
	v_pk_fma_f32 v[78:79], v[168:169], s[26:27], v[222:223] op_sel_hi:[1,0,1]
	v_pk_fma_f32 v[86:87], v[62:63], s[26:27], v[136:137] op_sel_hi:[1,0,1]
	v_pk_fma_f32 v[90:91], v[172:173], s[26:27], v[226:227] op_sel_hi:[1,0,1]
	v_pk_fma_f32 v[72:73], v[56:57], s[26:27], v[206:207] op_sel_hi:[1,0,1]
	v_pk_fma_f32 v[76:77], v[174:175], s[26:27], v[138:139] op_sel_hi:[1,0,1]
	v_pk_fma_f32 v[84:85], v[58:59], s[26:27], v[232:233] op_sel_hi:[1,0,1]
	v_pk_fma_f32 v[88:89], v[176:177], s[26:27], v[228:229] op_sel_hi:[1,0,1]
	v_pk_fma_f32 v[56:57], v[180:181], s[26:27], v[194:195] op_sel_hi:[1,0,1]
	v_pk_fma_f32 v[62:63], v[178:179], s[26:27], v[192:193] op_sel_hi:[1,0,1]
	v_pk_fma_f32 v[66:67], v[54:55], s[26:27], v[140:141] op_sel_hi:[1,0,1]
	v_pk_fma_f32 v[70:71], v[182:183], s[26:27], v[200:201] op_sel_hi:[1,0,1]
	v_pk_fma_f32 v[54:55], v[186:187], s[26:27], v[150:151] op_sel_hi:[1,0,1]
	v_pk_fma_f32 v[58:59], v[184:185], s[26:27], v[142:143] op_sel_hi:[1,0,1]
	v_pk_fma_f32 v[64:65], v[190:191], s[26:27], v[204:205] op_sel_hi:[1,0,1]
	v_pk_fma_f32 v[68:69], v[188:189], s[26:27], v[202:203] op_sel_hi:[1,0,1]
	v_mov_b32_e32 v136, v116
	v_mov_b32_e32 v137, v114
	v_mov_b32_e32 v138, v117
	v_mov_b32_e32 v139, v115
	v_mov_b32_e32 v140, v112
	v_mov_b32_e32 v141, v110
	v_mov_b32_e32 v142, v113
	v_mov_b32_e32 v143, v111
	v_mov_b32_e32 v144, v124
	v_mov_b32_e32 v145, v122
	v_mov_b32_e32 v146, v125
	v_mov_b32_e32 v147, v123
	v_mov_b32_e32 v148, v120
	v_mov_b32_e32 v149, v118
	v_mov_b32_e32 v150, v121
	v_mov_b32_e32 v151, v119
	v_mov_b32_e32 v152, v100
	v_mov_b32_e32 v153, v98
	v_mov_b32_e32 v154, v101
	v_mov_b32_e32 v155, v99
	v_mov_b32_e32 v156, v94
	v_mov_b32_e32 v157, v92
	v_mov_b32_e32 v158, v95
	v_mov_b32_e32 v159, v93
	v_mov_b32_e32 v160, v108
	v_mov_b32_e32 v161, v106
	v_mov_b32_e32 v162, v109
	v_mov_b32_e32 v163, v107
	v_mov_b32_e32 v164, v104
	v_mov_b32_e32 v165, v102
	v_mov_b32_e32 v166, v105
	v_mov_b32_e32 v167, v103
	v_mov_b32_e32 v168, v78
	v_mov_b32_e32 v169, v76
	v_mov_b32_e32 v170, v79
	v_mov_b32_e32 v171, v77
	v_mov_b32_e32 v172, v74
	v_mov_b32_e32 v173, v72
	v_mov_b32_e32 v174, v75
	v_mov_b32_e32 v175, v73
	v_mov_b32_e32 v176, v90
	v_mov_b32_e32 v177, v88
	v_mov_b32_e32 v178, v91
	v_mov_b32_e32 v179, v89
	v_mov_b32_e32 v180, v86
	v_mov_b32_e32 v181, v84
	v_mov_b32_e32 v182, v87
	v_mov_b32_e32 v183, v85
	v_mov_b32_e32 v184, v62
	v_mov_b32_e32 v185, v58
	v_mov_b32_e32 v186, v63
	v_mov_b32_e32 v187, v59
	v_mov_b32_e32 v188, v56
	v_mov_b32_e32 v189, v54
	v_mov_b32_e32 v190, v57
	v_mov_b32_e32 v191, v55
	v_mov_b32_e32 v192, v70
	v_mov_b32_e32 v193, v68
	v_mov_b32_e32 v194, v71
	v_mov_b32_e32 v195, v69
	v_mov_b32_e32 v196, v66
	v_mov_b32_e32 v197, v64
	v_mov_b32_e32 v198, v67
	v_mov_b32_e32 v199, v65
	v_pk_add_f32 v[136:137], v[136:137], v[138:139]
	v_pk_add_f32 v[138:139], v[140:141], v[142:143]
	v_pk_add_f32 v[140:141], v[144:145], v[146:147]
	v_pk_add_f32 v[142:143], v[148:149], v[150:151]
	v_pk_add_f32 v[144:145], v[152:153], v[154:155]
	v_pk_add_f32 v[146:147], v[156:157], v[158:159]
	v_pk_add_f32 v[148:149], v[160:161], v[162:163]
	v_pk_add_f32 v[150:151], v[164:165], v[166:167]
	v_pk_add_f32 v[152:153], v[168:169], v[170:171]
	v_pk_add_f32 v[154:155], v[172:173], v[174:175]
	v_pk_add_f32 v[156:157], v[176:177], v[178:179]
	v_pk_add_f32 v[158:159], v[180:181], v[182:183]
	v_pk_add_f32 v[160:161], v[184:185], v[186:187]
	v_pk_add_f32 v[162:163], v[188:189], v[190:191]
	v_pk_add_f32 v[164:165], v[192:193], v[194:195]
	v_pk_add_f32 v[166:167], v[196:197], v[198:199]
	v_pk_add_f32 v[136:137], v[136:137], v[138:139]
	v_pk_add_f32 v[138:139], v[140:141], v[142:143]
	v_pk_add_f32 v[140:141], v[144:145], v[146:147]
	v_pk_add_f32 v[142:143], v[148:149], v[150:151]
	v_pk_add_f32 v[144:145], v[152:153], v[154:155]
	v_pk_add_f32 v[146:147], v[156:157], v[158:159]
	v_pk_add_f32 v[148:149], v[160:161], v[162:163]
	v_pk_add_f32 v[150:151], v[164:165], v[166:167]
	v_pk_add_f32 v[136:137], v[136:137], v[138:139]
	v_pk_add_f32 v[138:139], v[140:141], v[142:143]
	v_pk_add_f32 v[140:141], v[144:145], v[146:147]
	v_pk_add_f32 v[142:143], v[148:149], v[150:151]
	v_add_f32_e32 v135, 0, v136
	v_add_f32_e32 v136, 0, v138
	v_add_f32_e32 v138, 0, v140
	v_add_f32_e32 v140, 0, v142
	v_add_f32_e32 v135, v135, v137
	v_add_f32_e32 v136, v136, v139
	v_add_f32_e32 v137, v138, v141
	v_add_f32_e32 v138, v140, v143
	ds_bpermute_b32 v139, v127, v135
	ds_bpermute_b32 v140, v127, v136
	ds_bpermute_b32 v141, v127, v137
	ds_bpermute_b32 v142, v127, v138
	s_waitcnt lgkmcnt(3)
	v_add_f32_e32 v135, v135, v139
	s_waitcnt lgkmcnt(2)
	v_add_f32_e32 v136, v136, v140
	s_waitcnt lgkmcnt(1)
	v_add_f32_e32 v137, v137, v141
	s_waitcnt lgkmcnt(0)
	v_add_f32_e32 v138, v138, v142
	ds_bpermute_b32 v139, v128, v135
	ds_bpermute_b32 v140, v128, v136
	ds_bpermute_b32 v141, v128, v137
	ds_bpermute_b32 v142, v128, v138
	s_waitcnt lgkmcnt(3)
	v_add_f32_e32 v135, v135, v139
	s_waitcnt lgkmcnt(2)
	v_add_f32_e32 v136, v136, v140
	s_waitcnt lgkmcnt(1)
	v_add_f32_e32 v137, v137, v141
	s_waitcnt lgkmcnt(0)
	v_add_f32_e32 v138, v138, v142
	ds_bpermute_b32 v139, v129, v135
	ds_bpermute_b32 v140, v129, v136
	ds_bpermute_b32 v141, v129, v137
	ds_bpermute_b32 v142, v129, v138
	s_waitcnt lgkmcnt(3)
	v_add_f32_e32 v135, v135, v139
	s_waitcnt lgkmcnt(2)
	v_add_f32_e32 v136, v136, v140
	s_waitcnt lgkmcnt(1)
	v_add_f32_e32 v137, v137, v141
	s_waitcnt lgkmcnt(0)
	v_add_f32_e32 v138, v138, v142
	ds_bpermute_b32 v139, v130, v135
	ds_bpermute_b32 v140, v130, v136
	ds_bpermute_b32 v141, v130, v137
	ds_bpermute_b32 v142, v130, v138
	s_waitcnt lgkmcnt(3)
	v_add_f32_e32 v135, v135, v139
	s_waitcnt lgkmcnt(2)
	v_add_f32_e32 v136, v136, v140
	s_waitcnt lgkmcnt(1)
	v_add_f32_e32 v137, v137, v141
	s_waitcnt lgkmcnt(0)
	v_add_f32_e32 v138, v138, v142
	ds_bpermute_b32 v139, v131, v135
	ds_bpermute_b32 v140, v131, v136
	ds_bpermute_b32 v141, v131, v137
	ds_bpermute_b32 v142, v131, v138
	s_waitcnt lgkmcnt(3)
	v_add_f32_e32 v135, v135, v139
	s_waitcnt lgkmcnt(2)
	v_add_f32_e32 v136, v136, v140
	s_waitcnt lgkmcnt(1)
	v_add_f32_e32 v137, v137, v141
	s_waitcnt lgkmcnt(0)
	v_add_f32_e32 v138, v138, v142
	ds_bpermute_b32 v139, v132, v135
	ds_bpermute_b32 v140, v132, v136
	ds_bpermute_b32 v141, v132, v137
	ds_bpermute_b32 v142, v132, v138
	s_waitcnt lgkmcnt(3)
	v_add_f32_e32 v135, v135, v139
	s_waitcnt lgkmcnt(2)
	v_add_f32_e32 v136, v136, v140
	s_waitcnt lgkmcnt(1)
	v_add_f32_e32 v137, v137, v141
	s_waitcnt lgkmcnt(0)
	v_add_f32_e32 v138, v138, v142
	v_fmamk_f32 v117, v135, 0xba800000, v117
	v_fmac_f32_e32 v116, 0xba800000, v135
	v_fmamk_f32 v113, v135, 0xba800000, v113
	v_fmac_f32_e32 v112, 0xba800000, v135
	v_fmamk_f32 v125, v135, 0xba800000, v125
	v_fmac_f32_e32 v124, 0xba800000, v135
	v_fmamk_f32 v121, v135, 0xba800000, v121
	v_fmac_f32_e32 v120, 0xba800000, v135
	v_fmac_f32_e32 v114, 0xba800000, v135
	v_fmac_f32_e32 v110, 0xba800000, v135
	v_fmamk_f32 v101, v136, 0xba800000, v101
	v_fmac_f32_e32 v100, 0xba800000, v136
	v_fmamk_f32 v95, v136, 0xba800000, v95
	v_fmac_f32_e32 v94, 0xba800000, v136
	v_fmamk_f32 v109, v136, 0xba800000, v109
	v_fmac_f32_e32 v108, 0xba800000, v136
	v_fmamk_f32 v105, v136, 0xba800000, v105
	v_fmac_f32_e32 v104, 0xba800000, v136
	v_fmamk_f32 v99, v136, 0xba800000, v99
	v_fmac_f32_e32 v98, 0xba800000, v136
	v_fmamk_f32 v93, v136, 0xba800000, v93
	v_fmac_f32_e32 v92, 0xba800000, v136
	v_fmamk_f32 v103, v136, 0xba800000, v103
	v_fmac_f32_e32 v102, 0xba800000, v136
	v_fmamk_f32 v107, v136, 0xba800000, v107
	v_fmac_f32_e32 v106, 0xba800000, v136
	v_fmamk_f32 v79, v137, 0xba800000, v79
	v_fmac_f32_e32 v78, 0xba800000, v137
	v_fmamk_f32 v75, v137, 0xba800000, v75
	v_fmac_f32_e32 v74, 0xba800000, v137
	v_fmamk_f32 v91, v137, 0xba800000, v91
	v_fmac_f32_e32 v90, 0xba800000, v137
	v_fmamk_f32 v87, v137, 0xba800000, v87
	v_fmac_f32_e32 v86, 0xba800000, v137
	v_fmamk_f32 v77, v137, 0xba800000, v77
	v_fmac_f32_e32 v76, 0xba800000, v137
	v_fmamk_f32 v73, v137, 0xba800000, v73
	v_fmac_f32_e32 v72, 0xba800000, v137
	v_fmamk_f32 v85, v137, 0xba800000, v85
	v_fmac_f32_e32 v84, 0xba800000, v137
	v_fmamk_f32 v89, v137, 0xba800000, v89
	v_fmac_f32_e32 v88, 0xba800000, v137
	v_fmamk_f32 v63, v138, 0xba800000, v63
	v_fmac_f32_e32 v62, 0xba800000, v138
	v_fmamk_f32 v57, v138, 0xba800000, v57
	v_fmac_f32_e32 v56, 0xba800000, v138
	v_fmamk_f32 v71, v138, 0xba800000, v71
	v_fmac_f32_e32 v70, 0xba800000, v138
	v_fmamk_f32 v67, v138, 0xba800000, v67
	v_fmac_f32_e32 v66, 0xba800000, v138
	v_fmamk_f32 v59, v138, 0xba800000, v59
	v_fmac_f32_e32 v58, 0xba800000, v138
	v_fmamk_f32 v55, v138, 0xba800000, v55
	v_fmac_f32_e32 v54, 0xba800000, v138
	v_fmamk_f32 v65, v138, 0xba800000, v65
	v_fmac_f32_e32 v64, 0xba800000, v138
	v_fmamk_f32 v69, v138, 0xba800000, v69
	v_fmac_f32_e32 v68, 0xba800000, v138
	v_pk_mul_f32 v[136:137], v[112:113], v[112:113]
	v_pk_mul_f32 v[138:139], v[116:117], v[116:117]
	v_pk_mul_f32 v[140:141], v[120:121], v[120:121]
	v_pk_mul_f32 v[142:143], v[124:125], v[124:125]
	v_fmamk_f32 v115, v135, 0xba800000, v115
	v_fmamk_f32 v111, v135, 0xba800000, v111
	v_mul_f32_e32 v144, v114, v114
	v_mul_f32_e32 v146, v110, v110
	v_pk_mul_f32 v[148:149], v[94:95], v[94:95]
	v_pk_mul_f32 v[150:151], v[100:101], v[100:101]
	v_pk_mul_f32 v[152:153], v[104:105], v[104:105]
	v_pk_mul_f32 v[154:155], v[108:109], v[108:109]
	v_mul_f32_e32 v156, v98, v98
	v_mul_f32_e32 v158, v92, v92
	v_pk_mul_f32 v[160:161], v[74:75], v[74:75]
	v_pk_mul_f32 v[162:163], v[78:79], v[78:79]
	v_pk_mul_f32 v[164:165], v[86:87], v[86:87]
	v_pk_mul_f32 v[166:167], v[90:91], v[90:91]
	v_pk_mov_b32 v[184:185], v[138:139], v[136:137] op_sel:[1,0]
	v_mov_b32_e32 v139, v137
	v_pk_mov_b32 v[136:137], v[142:143], v[140:141] op_sel:[1,0]
	v_mov_b32_e32 v143, v141
	v_fmamk_f32 v123, v135, 0xba800000, v123
	v_fmac_f32_e32 v122, 0xba800000, v135
	v_mul_f32_e32 v168, v76, v76
	v_mul_f32_e32 v170, v72, v72
	v_pk_mul_f32 v[172:173], v[56:57], v[56:57]
	v_pk_mul_f32 v[174:175], v[62:63], v[62:63]
	v_pk_mul_f32 v[176:177], v[66:67], v[66:67]
	v_pk_mul_f32 v[178:179], v[70:71], v[70:71]
	v_pk_fma_f32 v[140:141], v[114:115], v[114:115], v[144:145] op_sel_hi:[1,1,0]
	v_pk_fma_f32 v[144:145], v[110:111], v[110:111], v[146:147] op_sel_hi:[1,1,0]
	v_pk_mov_b32 v[146:147], v[150:151], v[148:149] op_sel:[1,0]
	v_mov_b32_e32 v151, v149
	v_pk_mov_b32 v[148:149], v[154:155], v[152:153] op_sel:[1,0]
	v_mov_b32_e32 v155, v153
	v_pk_fma_f32 v[152:153], v[98:99], v[98:99], v[156:157] op_sel_hi:[1,1,0]
	v_pk_fma_f32 v[156:157], v[92:93], v[92:93], v[158:159] op_sel_hi:[1,1,0]
	v_pk_mov_b32 v[158:159], v[162:163], v[160:161] op_sel:[1,0]
	v_mov_b32_e32 v163, v161
	v_pk_mov_b32 v[160:161], v[166:167], v[164:165] op_sel:[1,0]
	v_mov_b32_e32 v167, v165
	v_pk_add_f32 v[138:139], v[184:185], v[138:139]
	v_pk_add_f32 v[136:137], v[136:137], v[142:143]
	v_fmamk_f32 v119, v135, 0xba800000, v119
	v_fmac_f32_e32 v118, 0xba800000, v135
	v_pk_fma_f32 v[164:165], v[76:77], v[76:77], v[168:169] op_sel_hi:[1,1,0]
	v_pk_fma_f32 v[168:169], v[72:73], v[72:73], v[170:171] op_sel_hi:[1,1,0]
	v_pk_mov_b32 v[170:171], v[174:175], v[172:173] op_sel:[1,0]
	v_mov_b32_e32 v175, v173
	v_pk_mov_b32 v[172:173], v[178:179], v[176:177] op_sel:[1,0]
	v_mov_b32_e32 v179, v177
	v_mul_f32_e32 v140, v122, v122
	v_mul_f32_e32 v144, v123, v123
	v_pk_add_f32 v[142:143], v[146:147], v[150:151]
	v_pk_add_f32 v[146:147], v[148:149], v[154:155]
	v_pk_add_f32 v[148:149], v[158:159], v[162:163]
	v_pk_add_f32 v[150:151], v[160:161], v[166:167]
	v_pk_add_f32 v[138:139], v[138:139], v[138:139] op_sel_hi:[0,1]
	v_pk_add_f32 v[136:137], v[136:137], v[136:137] op_sel_hi:[0,1]
	v_mul_f32_e32 v180, v58, v58
	v_mul_f32_e32 v182, v54, v54
	v_mul_f32_e32 v152, v106, v106
	v_mul_f32_e32 v156, v107, v107
	v_pk_add_f32 v[154:155], v[170:171], v[174:175]
	v_pk_add_f32 v[158:159], v[172:173], v[178:179]
	v_pk_add_f32 v[140:141], v[140:141], v[144:145]
	v_pk_add_f32 v[142:143], v[142:143], v[142:143] op_sel_hi:[0,1]
	v_pk_add_f32 v[144:145], v[146:147], v[146:147] op_sel_hi:[0,1]
	v_pk_add_f32 v[148:149], v[148:149], v[148:149] op_sel_hi:[0,1]
	v_pk_add_f32 v[150:151], v[150:151], v[150:151] op_sel_hi:[0,1]
	v_mul_f32_e32 v138, v118, v118
	v_mul_f32_e32 v136, v119, v119
	v_pk_fma_f32 v[176:177], v[58:59], v[58:59], v[180:181] op_sel_hi:[1,1,0]
	v_pk_fma_f32 v[180:181], v[54:55], v[54:55], v[182:183] op_sel_hi:[1,1,0]
	v_mul_f32_e32 v164, v88, v88
	v_mul_f32_e32 v168, v89, v89
	v_pk_add_f32 v[146:147], v[152:153], v[156:157]
	v_pk_add_f32 v[154:155], v[154:155], v[154:155] op_sel_hi:[0,1]
	v_pk_add_f32 v[156:157], v[158:159], v[158:159] op_sel_hi:[0,1]
	v_mul_f32_e32 v142, v102, v102
	v_mul_f32_e32 v144, v103, v103
	v_mul_f32_e32 v148, v84, v84
	v_mul_f32_e32 v150, v85, v85
	v_pk_add_f32 v[136:137], v[138:139], v[136:137]
	v_mul_f32_e32 v176, v68, v68
	v_mul_f32_e32 v180, v69, v69
	v_pk_add_f32 v[152:153], v[164:165], v[168:169]
	v_mul_f32_e32 v154, v64, v64
	v_mul_f32_e32 v156, v65, v65
	v_pk_add_f32 v[138:139], v[142:143], v[144:145]
	v_pk_add_f32 v[142:143], v[148:149], v[150:151]
	v_pk_add_f32 v[136:137], v[140:141], v[136:137]
	v_pk_add_f32 v[158:159], v[176:177], v[180:181]
	v_pk_add_f32 v[144:145], v[154:155], v[156:157]
	v_pk_add_f32 v[138:139], v[146:147], v[138:139]
	v_pk_add_f32 v[140:141], v[152:153], v[142:143]
	v_add_f32_e32 v135, v136, v137
	v_pk_add_f32 v[142:143], v[158:159], v[144:145]
	v_add_f32_e32 v136, v138, v139
	v_add_f32_e32 v137, v140, v141
	ds_bpermute_b32 v139, v127, v135
	v_add_f32_e32 v138, v142, v143
	ds_bpermute_b32 v140, v127, v136
	ds_bpermute_b32 v141, v127, v137
	ds_bpermute_b32 v142, v127, v138
	s_waitcnt lgkmcnt(3)
	v_add_f32_e32 v135, v135, v139
	ds_bpermute_b32 v139, v128, v135
	s_waitcnt lgkmcnt(3)
	v_add_f32_e32 v136, v136, v140
	s_waitcnt lgkmcnt(2)
	v_add_f32_e32 v137, v137, v141
	s_waitcnt lgkmcnt(1)
	v_add_f32_e32 v138, v138, v142
	ds_bpermute_b32 v140, v128, v136
	ds_bpermute_b32 v141, v128, v137
	ds_bpermute_b32 v142, v128, v138
	s_waitcnt lgkmcnt(3)
	v_add_f32_e32 v135, v135, v139
	ds_bpermute_b32 v139, v129, v135
	s_waitcnt lgkmcnt(3)
	v_add_f32_e32 v136, v136, v140
	s_waitcnt lgkmcnt(2)
	v_add_f32_e32 v137, v137, v141
	s_waitcnt lgkmcnt(1)
	v_add_f32_e32 v138, v138, v142
	ds_bpermute_b32 v140, v129, v136
	ds_bpermute_b32 v141, v129, v137
	ds_bpermute_b32 v142, v129, v138
	s_waitcnt lgkmcnt(3)
	v_add_f32_e32 v135, v135, v139
	ds_bpermute_b32 v139, v130, v135
	s_waitcnt lgkmcnt(3)
	v_add_f32_e32 v136, v136, v140
	s_waitcnt lgkmcnt(2)
	v_add_f32_e32 v137, v137, v141
	s_waitcnt lgkmcnt(1)
	v_add_f32_e32 v138, v138, v142
	ds_bpermute_b32 v140, v130, v136
	ds_bpermute_b32 v141, v130, v137
	ds_bpermute_b32 v142, v130, v138
	s_waitcnt lgkmcnt(3)
	v_add_f32_e32 v135, v135, v139
	ds_bpermute_b32 v139, v131, v135
	s_waitcnt lgkmcnt(3)
	v_add_f32_e32 v136, v136, v140
	s_waitcnt lgkmcnt(2)
	v_add_f32_e32 v137, v137, v141
	s_waitcnt lgkmcnt(1)
	v_add_f32_e32 v138, v138, v142
	ds_bpermute_b32 v140, v131, v136
	ds_bpermute_b32 v141, v131, v137
	ds_bpermute_b32 v142, v131, v138
	s_waitcnt lgkmcnt(3)
	v_add_f32_e32 v135, v135, v139
	ds_bpermute_b32 v139, v132, v135
	s_waitcnt lgkmcnt(3)
	v_add_f32_e32 v136, v136, v140
	s_waitcnt lgkmcnt(2)
	v_add_f32_e32 v137, v137, v141
	s_waitcnt lgkmcnt(1)
	v_add_f32_e32 v138, v138, v142
	ds_bpermute_b32 v140, v132, v136
	ds_bpermute_b32 v141, v132, v137
	ds_bpermute_b32 v142, v132, v138
	s_waitcnt lgkmcnt(3)
	v_add_f32_e32 v135, v135, v139
	v_fmamk_f32 v135, v135, 0x3a800000, v133
	s_waitcnt lgkmcnt(2)
	v_add_f32_e32 v136, v136, v140
	s_waitcnt lgkmcnt(1)
	v_add_f32_e32 v137, v137, v141
	s_waitcnt lgkmcnt(0)
	v_add_f32_e32 v138, v138, v142
	v_fmamk_f32 v136, v136, 0x3a800000, v133
	v_fmamk_f32 v137, v137, 0x3a800000, v133
	v_mul_f32_e32 v139, 0x4f800000, v135
	v_cmp_gt_f32_e64 s[8:9], s30, v135
	v_fmamk_f32 v138, v138, 0x3a800000, v133
	v_mul_f32_e32 v140, 0x4f800000, v136
	v_cmp_gt_f32_e32 vcc, s30, v136
	v_mul_f32_e32 v141, 0x4f800000, v137
	v_cmp_gt_f32_e64 s[0:1], s30, v137
	v_cndmask_b32_e64 v135, v135, v139, s[8:9]
	v_mul_f32_e32 v142, 0x4f800000, v138
	v_cmp_gt_f32_e64 s[6:7], s30, v138
	v_cndmask_b32_e32 v136, v136, v140, vcc
	v_cndmask_b32_e64 v137, v137, v141, s[0:1]
	v_sqrt_f32_e32 v139, v135
	v_cndmask_b32_e64 v138, v138, v142, s[6:7]
	v_sqrt_f32_e32 v140, v136
	v_sqrt_f32_e32 v141, v137
	v_sqrt_f32_e32 v142, v138
	v_add_u32_e32 v143, -1, v139
	v_add_u32_e32 v144, 1, v139
	v_add_u32_e32 v145, -1, v140
	v_add_u32_e32 v147, -1, v141
	v_fma_f32 v151, -v143, v139, v135
	v_add_u32_e32 v146, 1, v140
	v_add_u32_e32 v148, 1, v141
	v_add_u32_e32 v149, -1, v142
	v_fma_f32 v152, -v144, v139, v135
	v_fma_f32 v153, -v145, v140, v136
	v_fma_f32 v155, -v147, v141, v137
	v_cmp_ge_f32_e64 s[10:11], 0, v151
	v_add_u32_e32 v150, 1, v142
	v_fma_f32 v154, -v146, v140, v136
	v_fma_f32 v156, -v148, v141, v137
	v_fma_f32 v157, -v149, v142, v138
	v_cndmask_b32_e64 v139, v139, v143, s[10:11]
	v_cmp_ge_f32_e64 s[10:11], 0, v153
	v_cmp_ge_f32_e64 s[12:13], 0, v155
	v_cmp_lt_f32_e64 s[16:17], 0, v152
	v_fma_f32 v158, -v150, v142, v138
	v_cndmask_b32_e64 v140, v140, v145, s[10:11]
	v_cmp_lt_f32_e64 s[10:11], 0, v154
	v_cndmask_b32_e64 v141, v141, v147, s[12:13]
	v_cmp_lt_f32_e64 s[12:13], 0, v156
	v_cmp_ge_f32_e64 s[14:15], 0, v157
	v_cndmask_b32_e64 v139, v139, v144, s[16:17]
	v_cndmask_b32_e64 v140, v140, v146, s[10:11]
	v_cndmask_b32_e64 v142, v142, v149, s[14:15]
	v_cmp_lt_f32_e64 s[14:15], 0, v158
	v_cndmask_b32_e64 v141, v141, v148, s[12:13]
	v_mul_f32_e32 v143, 0x37800000, v139
	v_cndmask_b32_e64 v142, v142, v150, s[14:15]
	v_mul_f32_e32 v144, 0x37800000, v140
	v_mul_f32_e32 v145, 0x37800000, v141
	v_cndmask_b32_e64 v139, v139, v143, s[8:9]
	v_cmp_class_f32_e64 s[8:9], v135, v134
	v_mul_f32_e32 v146, 0x37800000, v142
	v_cndmask_b32_e32 v140, v140, v144, vcc
	v_cmp_class_f32_e32 vcc, v136, v134
	v_cndmask_b32_e64 v141, v141, v145, s[0:1]
	v_cmp_class_f32_e64 s[0:1], v137, v134
	v_cndmask_b32_e64 v135, v139, v135, s[8:9]
	v_cndmask_b32_e64 v142, v142, v146, s[6:7]
	v_cmp_class_f32_e64 s[6:7], v138, v134
	v_cndmask_b32_e32 v139, v140, v136, vcc
	v_cndmask_b32_e64 v140, v141, v137, s[0:1]
	v_div_scale_f32 v136, s[0:1], v135, v135, 1.0
	v_cndmask_b32_e64 v141, v142, v138, s[6:7]
	v_div_scale_f32 v138, s[0:1], v139, v139, 1.0
	v_rcp_f32_e32 v147, v136
	v_div_scale_f32 v143, s[6:7], v140, v140, 1.0
	v_rcp_f32_e32 v148, v138
	v_div_scale_f32 v145, s[8:9], v141, v141, 1.0
	v_rcp_f32_e32 v149, v143
	v_rcp_f32_e32 v150, v145
	v_fma_f32 v151, -v136, v147, 1.0
	v_div_scale_f32 v137, vcc, 1.0, v135, 1.0
	v_fma_f32 v152, -v138, v148, 1.0
	v_fmac_f32_e32 v147, v151, v147
	v_div_scale_f32 v142, s[0:1], 1.0, v139, 1.0
	v_fma_f32 v153, -v143, v149, 1.0
	v_fmac_f32_e32 v148, v152, v148
	v_mul_f32_e32 v151, v137, v147
	v_div_scale_f32 v144, s[6:7], 1.0, v140, 1.0
	v_fma_f32 v154, -v145, v150, 1.0
	v_fmac_f32_e32 v149, v153, v149
	v_mul_f32_e32 v152, v142, v148
	v_fma_f32 v155, -v136, v151, v137
	v_div_scale_f32 v146, s[8:9], 1.0, v141, 1.0
	v_fmac_f32_e32 v150, v154, v150
	v_mul_f32_e32 v153, v144, v149
	v_fma_f32 v156, -v138, v152, v142
	v_fmac_f32_e32 v151, v155, v147
	v_mul_f32_e32 v154, v146, v150
	v_fma_f32 v157, -v143, v153, v144
	v_fmac_f32_e32 v152, v156, v148
	v_fma_f32 v136, -v136, v151, v137
	v_fma_f32 v158, -v145, v154, v146
	v_fmac_f32_e32 v153, v157, v149
	v_fma_f32 v137, -v138, v152, v142
	v_div_fmas_f32 v136, v136, v147, v151
	s_mov_b64 vcc, s[0:1]
	v_fmac_f32_e32 v154, v158, v150
	v_fma_f32 v138, -v143, v153, v144
	v_div_fixup_f32 v136, v136, v135, 1.0
	v_div_fmas_f32 v135, v137, v148, v152
	s_mov_b64 vcc, s[6:7]
	v_fma_f32 v142, -v145, v154, v146
	v_pk_mul_f32 v[124:125], v[124:125], v[136:137] op_sel_hi:[1,0]
	v_pk_mul_f32 v[120:121], v[120:121], v[136:137] op_sel_hi:[1,0]
	v_pk_mul_f32 v[116:117], v[116:117], v[136:137] op_sel_hi:[1,0]
	v_pk_mul_f32 v[112:113], v[112:113], v[136:137] op_sel_hi:[1,0]
	v_pk_mul_f32 v[122:123], v[122:123], v[136:137] op_sel_hi:[1,0]
	v_pk_mul_f32 v[118:119], v[118:119], v[136:137] op_sel_hi:[1,0]
	v_pk_mul_f32 v[114:115], v[114:115], v[136:137] op_sel_hi:[1,0]
	v_pk_mul_f32 v[110:111], v[110:111], v[136:137] op_sel_hi:[1,0]
	v_div_fixup_f32 v136, v135, v139, 1.0
	v_div_fmas_f32 v135, v138, v149, v153
	s_mov_b64 vcc, s[8:9]
	v_pk_fma_f32 v[116:117], v[4:5], v[116:117], v[12:13]
	v_pk_mul_f32 v[108:109], v[108:109], v[136:137] op_sel_hi:[1,0]
	v_pk_mul_f32 v[104:105], v[104:105], v[136:137] op_sel_hi:[1,0]
	v_pk_mul_f32 v[100:101], v[100:101], v[136:137] op_sel_hi:[1,0]
	v_pk_mul_f32 v[138:139], v[94:95], v[136:137] op_sel_hi:[1,0]
	v_pk_mul_f32 v[106:107], v[106:107], v[136:137] op_sel_hi:[1,0]
	v_pk_mul_f32 v[102:103], v[102:103], v[136:137] op_sel_hi:[1,0]
	v_pk_mul_f32 v[98:99], v[98:99], v[136:137] op_sel_hi:[1,0]
	v_pk_mul_f32 v[136:137], v[92:93], v[136:137] op_sel_hi:[1,0]
	v_div_fixup_f32 v140, v135, v140, 1.0
	v_div_fmas_f32 v135, v142, v150, v154
	v_pk_fma_f32 v[120:121], v[2:3], v[120:121], v[10:11]
	v_pk_fma_f32 v[124:125], v[0:1], v[124:125], v[8:9]
	v_pk_fma_f32 v[112:113], v[6:7], v[112:113], v[14:15]
	v_pk_fma_f32 v[110:111], v[22:23], v[110:111], v[30:31]
	v_pk_fma_f32 v[114:115], v[20:21], v[114:115], v[28:29]
	v_cvt_pk_bf16_f32 v92, v116, v117
	v_pk_fma_f32 v[116:117], v[22:23], v[136:137], v[30:31]
	v_div_fixup_f32 v136, v135, v141, 1.0
	v_pk_fma_f32 v[118:119], v[18:19], v[118:119], v[26:27]
	v_pk_fma_f32 v[122:123], v[16:17], v[122:123], v[24:25]
	v_cvt_pk_bf16_f32 v93, v112, v113
	v_cvt_pk_bf16_f32 v94, v124, v125
	v_cvt_pk_bf16_f32 v95, v120, v121
	v_pk_fma_f32 v[104:105], v[2:3], v[104:105], v[10:11]
	v_pk_fma_f32 v[108:109], v[0:1], v[108:109], v[8:9]
	v_pk_fma_f32 v[112:113], v[6:7], v[138:139], v[14:15]
	v_pk_fma_f32 v[100:101], v[4:5], v[100:101], v[12:13]
	v_pk_mul_f32 v[120:121], v[74:75], v[140:141] op_sel_hi:[1,0]
	v_pk_mul_f32 v[124:125], v[72:73], v[140:141] op_sel_hi:[1,0]
	global_store_dwordx4 v[96:97], v[92:95], off offset:-3072 sc1
	v_cvt_pk_bf16_f32 v72, v114, v115
	v_cvt_pk_bf16_f32 v73, v110, v111
	v_cvt_pk_bf16_f32 v74, v122, v123
	v_cvt_pk_bf16_f32 v75, v118, v119
	v_pk_mul_f32 v[110:111], v[56:57], v[136:137] op_sel_hi:[1,0]
	v_pk_mul_f32 v[114:115], v[54:55], v[136:137] op_sel_hi:[1,0]
	global_store_dwordx4 v[96:97], v[72:75], off offset:-2048 sc1
	v_cvt_pk_bf16_f32 v54, v100, v101
	v_cvt_pk_bf16_f32 v55, v112, v113
	v_cvt_pk_bf16_f32 v56, v108, v109
	v_cvt_pk_bf16_f32 v57, v104, v105
	v_pk_fma_f32 v[102:103], v[18:19], v[102:103], v[26:27]
	v_pk_fma_f32 v[106:107], v[16:17], v[106:107], v[24:25]
	v_pk_fma_f32 v[98:99], v[20:21], v[98:99], v[28:29]
	v_pk_mul_f32 v[90:91], v[90:91], v[140:141] op_sel_hi:[1,0]
	v_pk_mul_f32 v[86:87], v[86:87], v[140:141] op_sel_hi:[1,0]
	v_pk_mul_f32 v[78:79], v[78:79], v[140:141] op_sel_hi:[1,0]
	global_store_dwordx4 v[96:97], v[54:57], off offset:-1024 sc1
	v_pk_mul_f32 v[88:89], v[88:89], v[140:141] op_sel_hi:[1,0]
	v_pk_mul_f32 v[84:85], v[84:85], v[140:141] op_sel_hi:[1,0]
	v_cvt_pk_bf16_f32 v54, v98, v99
	v_cvt_pk_bf16_f32 v55, v116, v117
	v_cvt_pk_bf16_f32 v56, v106, v107
	v_cvt_pk_bf16_f32 v57, v102, v103
	v_pk_mul_f32 v[76:77], v[76:77], v[140:141] op_sel_hi:[1,0]
	v_pk_fma_f32 v[86:87], v[2:3], v[86:87], v[10:11]
	v_pk_fma_f32 v[90:91], v[0:1], v[90:91], v[8:9]
	v_pk_fma_f32 v[92:93], v[6:7], v[120:121], v[14:15]
	v_pk_fma_f32 v[78:79], v[4:5], v[78:79], v[12:13]
	global_store_dwordx4 v[82:83], v[54:57], off offset:-4096 sc1
	v_pk_fma_f32 v[84:85], v[18:19], v[84:85], v[26:27]
	v_pk_fma_f32 v[88:89], v[16:17], v[88:89], v[24:25]
	v_cvt_pk_bf16_f32 v54, v78, v79
	v_cvt_pk_bf16_f32 v55, v92, v93
	v_cvt_pk_bf16_f32 v56, v90, v91
	v_cvt_pk_bf16_f32 v57, v86, v87
	v_pk_fma_f32 v[94:95], v[22:23], v[124:125], v[30:31]
	v_pk_fma_f32 v[76:77], v[20:21], v[76:77], v[28:29]
	v_pk_mul_f32 v[70:71], v[70:71], v[136:137] op_sel_hi:[1,0]
	v_pk_mul_f32 v[66:67], v[66:67], v[136:137] op_sel_hi:[1,0]
	v_pk_mul_f32 v[62:63], v[62:63], v[136:137] op_sel_hi:[1,0]
	global_store_dwordx4 v[82:83], v[54:57], off offset:-3072 sc1
	v_pk_mul_f32 v[68:69], v[68:69], v[136:137] op_sel_hi:[1,0]
	v_pk_mul_f32 v[64:65], v[64:65], v[136:137] op_sel_hi:[1,0]
	v_cvt_pk_bf16_f32 v54, v76, v77
	v_cvt_pk_bf16_f32 v55, v94, v95
	v_cvt_pk_bf16_f32 v56, v88, v89
	v_cvt_pk_bf16_f32 v57, v84, v85
	v_pk_mul_f32 v[58:59], v[58:59], v[136:137] op_sel_hi:[1,0]
	v_pk_fma_f32 v[66:67], v[2:3], v[66:67], v[10:11]
	v_pk_fma_f32 v[70:71], v[0:1], v[70:71], v[8:9]
	v_pk_fma_f32 v[72:73], v[6:7], v[110:111], v[14:15]
	v_pk_fma_f32 v[62:63], v[4:5], v[62:63], v[12:13]
	global_store_dwordx4 v[82:83], v[54:57], off offset:-2048 sc1
	v_pk_fma_f32 v[64:65], v[18:19], v[64:65], v[26:27]
	v_pk_fma_f32 v[68:69], v[16:17], v[68:69], v[24:25]
	v_cvt_pk_bf16_f32 v54, v62, v63
	v_cvt_pk_bf16_f32 v55, v72, v73
	v_cvt_pk_bf16_f32 v56, v70, v71
	v_cvt_pk_bf16_f32 v57, v66, v67
	v_pk_fma_f32 v[74:75], v[22:23], v[114:115], v[30:31]
	v_pk_fma_f32 v[58:59], v[20:21], v[58:59], v[28:29]
	global_store_dwordx4 v[82:83], v[54:57], off offset:-1024 sc1
	s_mov_b64 vcc, s[4:5]
	s_nop 0
	v_cvt_pk_bf16_f32 v54, v58, v59
	v_cvt_pk_bf16_f32 v55, v74, v75
	v_cvt_pk_bf16_f32 v56, v68, v69
	v_cvt_pk_bf16_f32 v57, v64, v65
	global_store_dwordx4 v[82:83], v[54:57], off sc1
	v_lshl_add_u64 v[82:83], v[82:83], 0, s[24:25]
	s_cbranch_vccnz .LBB0_3498
